# mlstm_D epilogue: per-row bcum value requested before the V stage instead of at the epilogue start (was one exposed round trip)
# baseline (speedup 1.0000x reference)
; #define LAS __attribute__((address_space(3)))
; __device__ __forceinline__ unsigned cvt_pk_bf16(float lo, float hi) { unsigned r; asm volatile("v_cvt_pk_bf16_f32 %0, %1, %2" : "=v"(r) : "v"(lo), "v"(hi)); return r; }
; __device__ __forceinline__ void mlstm_D(LAS unsigned char* lds, int c, int h, const bf16_t* Z, const float* gi, const float* bcum, const float* marr, const bf16_t* CST, const float* NST,
;                                         const float* hgain, bf16_t* YCAT) {
;     ...
;         u32x2 w; w.x = cvt_pk_bf16(pv[0], pv[1]); w.y = cvt_pk_bf16(pv[2], pv[3]);
;         *(LAS u32x2*)(Pw + fr * PRS + (16 * j + 4 * fq) * 2) = w; }
;     rsum += __shfl_xor(rsum, 16); rsum += __shfl_xor(rsum, 32);
;     const float den = wi * nq + rsum;
;     f32x4 acc[16];
; #pragma unroll
;     for (int j = 0; j < 16; ++j) acc[j] = (f32x4){0.f, 0.f, 0.f, 0.f};
;     const bf16_t* cst = CST + (size_t)(c * NH + h) * DH * DH;
; #pragma unroll
;     for (int half = 0; half < 2; ++half) {
;         __syncthreads();
;         stage_tile<DH, 128, 8>(X, cst + half * 128, DH, tid);
;         __syncthreads();
.LBB0_769:
	s_or_b64 exec, exec, s[2:3]
	v_cvt_pk_bf16_f32 v2, v59, v52
	v_cvt_pk_bf16_f32 v3, v55, v53
	ds_write_b64 v30, v[2:3] offset:224
	v_lshrrev_b32_e32 v2, 28, v122
	v_lshrrev_b32_e32 v6, 28, v124
	v_add_u32_e32 v2, v99, v2
	v_add_u32_e32 v6, v118, v6
	v_lshrrev_b32_e32 v10, 28, v126
	v_ashrrev_i32_e32 v16, 4, v2
	v_ashrrev_i32_e32 v20, 4, v6
	v_add_u32_e32 v10, v119, v10
	v_and_b32_e32 v2, -16, v2
	v_ashrrev_i32_e32 v17, 31, v16
	v_and_b32_e32 v6, -16, v6
	v_ashrrev_i32_e32 v21, 31, v20
	v_ashrrev_i32_e32 v64, 4, v10
	v_and_b32_e32 v10, -16, v10
	v_sub_u32_e32 v135, v99, v2
	v_lshlrev_b64 v[2:3], 9, v[16:17]
	v_sub_u32_e32 v17, v118, v6
	v_lshlrev_b64 v[6:7], 9, v[20:21]
	v_sub_u32_e32 v21, v119, v10
	v_lshrrev_b32_e32 v10, 28, v128
	v_add_u32_e32 v10, v120, v10
	v_ashrrev_i32_e32 v65, 31, v64
	v_ashrrev_i32_e32 v118, 4, v10
	v_and_b32_e32 v10, -16, v10
	v_lshlrev_b64 v[30:31], 9, v[64:65]
	v_sub_u32_e32 v65, v120, v10
	v_lshrrev_b32_e32 v10, 28, v130
	v_add_u32_e32 v10, v123, v10
	v_ashrrev_i32_e32 v119, 31, v118
	v_ashrrev_i32_e32 v136, 4, v10
	v_and_b32_e32 v10, -16, v10
	v_lshlrev_b64 v[34:35], 9, v[118:119]
	v_sub_u32_e32 v119, v123, v10
	v_lshrrev_b32_e32 v10, 28, v131
	v_add_u32_e32 v10, v125, v10
	v_ashrrev_i32_e32 v138, 4, v10
	v_and_b32_e32 v10, -16, v10
	v_sub_u32_e32 v120, v125, v10
	v_lshrrev_b32_e32 v10, 28, v132
	v_add_u32_e32 v10, v127, v10
	s_ashr_i32 s23, s22, 31
	v_ashrrev_i32_e32 v137, 31, v136
	v_ashrrev_i32_e32 v140, 4, v10
	v_and_b32_e32 v10, -16, v10
	s_lshl_b64 s[2:3], s[22:23], 17
	v_lshlrev_b64 v[60:61], 9, v[136:137]
	v_sub_u32_e32 v137, v127, v10
	v_lshrrev_b32_e32 v10, 28, v133
	s_add_u32 s2, s56, s2
	v_add_u32_e32 v10, v129, v10
	s_addc_u32 s3, s57, s3
	v_lshlrev_b32_e32 v4, 3, v135
	v_ashrrev_i32_e32 v139, 31, v138
	v_ashrrev_i32_e32 v141, 31, v140
	v_ashrrev_i32_e32 v142, 4, v10
	v_and_b32_e32 v10, -16, v10
	v_ashrrev_i32_e32 v5, 31, v4
	v_lshlrev_b32_e32 v32, 3, v21
	v_lshlrev_b32_e32 v62, 3, v119
	v_lshlrev_b64 v[122:123], 9, v[138:139]
	v_lshlrev_b64 v[126:127], 9, v[140:141]
	v_lshlrev_b32_e32 v130, 3, v137
	v_sub_u32_e32 v139, v129, v10
	v_ashrrev_i32_e32 v143, 31, v142
	v_lshl_add_u64 v[2:3], s[2:3], 0, v[2:3]
	v_lshlrev_b32_e32 v8, 3, v17
	v_ashrrev_i32_e32 v33, 31, v32
	v_lshlrev_b32_e32 v36, 3, v65
	v_ashrrev_i32_e32 v63, 31, v62
	v_lshlrev_b32_e32 v124, 3, v120
	v_ashrrev_i32_e32 v131, 31, v130
	v_lshlrev_b64 v[128:129], 9, v[142:143]
	v_lshlrev_b32_e32 v132, 3, v139
	v_lshl_add_u64 v[2:3], v[4:5], 1, v[2:3]
	v_lshl_add_u64 v[4:5], s[2:3], 0, v[6:7]
	v_lshl_add_u64 v[6:7], s[2:3], 0, v[30:31]
	v_lshl_add_u64 v[60:61], s[2:3], 0, v[60:61]
	v_lshl_add_u64 v[126:127], s[2:3], 0, v[126:127]
	v_ashrrev_i32_e32 v9, 31, v8
	v_ashrrev_i32_e32 v37, 31, v36
	v_ashrrev_i32_e32 v125, 31, v124
	v_ashrrev_i32_e32 v133, 31, v132
	v_lshl_add_u64 v[6:7], v[32:33], 1, v[6:7]
	v_lshl_add_u64 v[30:31], s[2:3], 0, v[34:35]
	v_lshl_add_u64 v[196:197], v[62:63], 1, v[60:61]
	v_lshl_add_u64 v[60:61], s[2:3], 0, v[122:123]
	v_lshl_add_u64 v[204:205], v[130:131], 1, v[126:127]
	v_lshl_add_u64 v[126:127], s[2:3], 0, v[128:129]
	s_waitcnt lgkmcnt(0)
	s_barrier
	v_lshl_add_u64 v[4:5], v[8:9], 1, v[4:5]
	global_load_dwordx4 v[8:11], v[2:3], off
	global_load_dwordx4 v[12:15], v[4:5], off
	v_lshl_add_u64 v[192:193], v[36:37], 1, v[30:31]
	global_load_dwordx4 v[30:33], v[6:7], off
	global_load_dwordx4 v[34:37], v[192:193], off
	v_lshl_add_u64 v[200:201], v[124:125], 1, v[60:61]
	global_load_dwordx4 v[60:63], v[196:197], off
	global_load_dwordx4 v[122:125], v[200:201], off
	v_lshl_add_u64 v[208:209], v[132:133], 1, v[126:127]
	global_load_dwordx4 v[126:129], v[204:205], off
	global_load_dwordx4 v[130:133], v[208:209], off
	v_mul_lo_u32 v20, v20, s74
	v_lshlrev_b32_e32 v17, 4, v17
	v_add3_u32 v17, s51, v20, v17
	v_mul_lo_u32 v20, v64, s74
	v_lshlrev_b32_e32 v21, 4, v21
	v_add3_u32 v20, s51, v20, v21
	v_mul_lo_u32 v21, v118, s74
	v_lshlrev_b32_e32 v64, 4, v65
	v_add3_u32 v21, s51, v21, v64
	v_mul_lo_u32 v64, v136, s74
	v_lshlrev_b32_e32 v65, 4, v119
	v_add3_u32 v64, s51, v64, v65
	v_mul_lo_u32 v65, v138, s74
	v_lshlrev_b32_e32 v118, 4, v120
	v_mul_lo_u32 v16, v16, s74
	v_lshlrev_b32_e32 v135, 4, v135
	v_add3_u32 v65, s51, v65, v118
	v_mul_lo_u32 v118, v140, s74
	v_lshlrev_b32_e32 v119, 4, v137
	v_add3_u32 v16, s51, v16, v135
	v_add3_u32 v119, s51, v118, v119
	v_mul_lo_u32 v118, v142, s74
	v_lshlrev_b32_e32 v120, 4, v139
	v_add3_u32 v135, s51, v118, v120
	s_waitcnt vmcnt(7)
	ds_write_b128 v16, v[8:11]
	s_waitcnt vmcnt(6)
	ds_write_b128 v17, v[12:15]
	s_waitcnt vmcnt(5)
	ds_write_b128 v20, v[30:33]
	s_waitcnt vmcnt(4)
	ds_write_b128 v21, v[34:37]
	s_waitcnt vmcnt(3)
	ds_write_b128 v64, v[60:63]
	s_waitcnt vmcnt(2)
	ds_write_b128 v65, v[122:125]
	s_waitcnt vmcnt(1)
	ds_write_b128 v119, v[126:129]
	s_waitcnt vmcnt(0)
	ds_write_b128 v135, v[130:133]
	s_waitcnt lgkmcnt(0)
	s_barrier
; #define MFMA16(b, a, c) __builtin_amdgcn_mfma_f32_16x16x32_bf16((b), (a), (c), 0, 0, 0)
; __device__ __forceinline__ void mlstm_D(LAS unsigned char* lds, int c, int h, const bf16_t* Z, const float* gi, const float* bcum, const float* marr, const bf16_t* CST, const float* NST,
;                                         const float* hgain, bf16_t* YCAT) {
;     ...
; #pragma unroll
;         for (int ks = 0; ks < 4; ++ks)
;             { const bf16x8 aqh = *(const bf16x8*)(Z + trow * EVN + 1024 + h * DH + 32 * (half * 4 + ks) + 8 * fq);
; #pragma unroll
;               for (int j = 0; j < 16; ++j) acc[j] = MFMA16(row_frag(X, (128 + 8) * 2, 16 * j, 32 * ks, lane), aqh, acc[j]);
;               asm volatile("" ::: "memory"); }
	global_load_dwordx4 v[8:11], v[90:91], off offset:2048
	v_mul_u32_u24_e32 v118, 0x110, v71
	v_add_u32_e32 v228, v121, v118
	ds_read_b128 v[12:15], v228
	ds_read_b128 v[30:33], v228 offset:4352
	ds_read_b128 v[34:37], v228 offset:8704
	ds_read_b128 v[60:63], v228 offset:13056
	ds_read_b128 v[120:123], v228 offset:17408
	ds_read_b128 v[124:127], v228 offset:21760
	ds_read_b128 v[128:131], v228 offset:26112
	ds_read_b128 v[136:139], v228 offset:30464
	ds_read_b128 v[140:143], v228 offset:34816
	ds_read_b128 v[144:147], v228 offset:39168
	ds_read_b128 v[148:151], v228 offset:43520
	ds_read_b128 v[152:155], v228 offset:47872
	ds_read_b128 v[156:159], v228 offset:52224
	ds_read_b128 v[160:163], v228 offset:56576
	ds_read_b128 v[164:167], v228 offset:60928
	ds_read_b128 v[168:171], v228 offset:65280
	global_load_dwordx4 v[172:175], v[90:91], off offset:2112
	s_waitcnt vmcnt(1) lgkmcnt(14)
	v_mfma_f32_16x16x32_bf16 v[12:15], v[12:15], v[8:11], 0
	ds_read_b128 v[176:179], v228 offset:64
	v_mad_i64_i32 v[132:133], s[2:3], v101, s68, 0
	v_mfma_f32_16x16x32_bf16 v[30:33], v[30:33], v[8:11], 0
	v_ashrrev_i32_e32 v71, 31, v70
	s_waitcnt lgkmcnt(14)
	v_mfma_f32_16x16x32_bf16 v[34:37], v[34:37], v[8:11], 0
	s_waitcnt lgkmcnt(13)
	v_mfma_f32_16x16x32_bf16 v[60:63], v[60:63], v[8:11], 0
	s_waitcnt lgkmcnt(12)
	v_mfma_f32_16x16x32_bf16 v[120:123], v[120:123], v[8:11], 0
	s_waitcnt lgkmcnt(11)
	v_mfma_f32_16x16x32_bf16 v[124:127], v[124:127], v[8:11], 0
	s_waitcnt lgkmcnt(10)
	v_mfma_f32_16x16x32_bf16 v[128:131], v[128:131], v[8:11], 0
	s_waitcnt lgkmcnt(9)
	v_mfma_f32_16x16x32_bf16 v[136:139], v[136:139], v[8:11], 0
	s_waitcnt lgkmcnt(8)
	v_mfma_f32_16x16x32_bf16 v[140:143], v[140:143], v[8:11], 0
	s_waitcnt lgkmcnt(7)
	v_mfma_f32_16x16x32_bf16 v[144:147], v[144:147], v[8:11], 0
	s_waitcnt lgkmcnt(6)
	v_mfma_f32_16x16x32_bf16 v[148:151], v[148:151], v[8:11], 0
	s_waitcnt lgkmcnt(5)
	v_mfma_f32_16x16x32_bf16 v[152:155], v[152:155], v[8:11], 0
	s_waitcnt lgkmcnt(4)
	v_mfma_f32_16x16x32_bf16 v[156:159], v[156:159], v[8:11], 0
	s_waitcnt lgkmcnt(3)
	v_mfma_f32_16x16x32_bf16 v[160:163], v[160:163], v[8:11], 0
	s_waitcnt lgkmcnt(2)
	v_mfma_f32_16x16x32_bf16 v[164:167], v[164:167], v[8:11], 0
	s_waitcnt lgkmcnt(1)
	v_mfma_f32_16x16x32_bf16 v[8:11], v[168:171], v[8:11], 0
	ds_read_b128 v[168:171], v228 offset:4416
	s_waitcnt vmcnt(0) lgkmcnt(1)
	v_mfma_f32_16x16x32_bf16 v[12:15], v[176:179], v[172:175], v[12:15]
	ds_read_b128 v[176:179], v228 offset:8768
	s_waitcnt lgkmcnt(1)
	v_mfma_f32_16x16x32_bf16 v[30:33], v[168:171], v[172:175], v[30:33]
	ds_read_b128 v[168:171], v228 offset:13120
	s_waitcnt lgkmcnt(1)
	v_mfma_f32_16x16x32_bf16 v[34:37], v[176:179], v[172:175], v[34:37]
	ds_read_b128 v[176:179], v228 offset:17472
	s_waitcnt lgkmcnt(1)
	v_mfma_f32_16x16x32_bf16 v[60:63], v[168:171], v[172:175], v[60:63]
	ds_read_b128 v[168:171], v228 offset:21824
	s_waitcnt lgkmcnt(1)
	v_mfma_f32_16x16x32_bf16 v[120:123], v[176:179], v[172:175], v[120:123]
	ds_read_b128 v[176:179], v228 offset:26176
	s_waitcnt lgkmcnt(1)
	v_mfma_f32_16x16x32_bf16 v[124:127], v[168:171], v[172:175], v[124:127]
	ds_read_b128 v[168:171], v228 offset:30528
	s_waitcnt lgkmcnt(1)
	v_mfma_f32_16x16x32_bf16 v[128:131], v[176:179], v[172:175], v[128:131]
	ds_read_b128 v[176:179], v228 offset:34880
	s_waitcnt lgkmcnt(1)
	v_mfma_f32_16x16x32_bf16 v[136:139], v[168:171], v[172:175], v[136:139]
	ds_read_b128 v[168:171], v228 offset:39232
	s_waitcnt lgkmcnt(1)
	v_mfma_f32_16x16x32_bf16 v[140:143], v[176:179], v[172:175], v[140:143]
	ds_read_b128 v[176:179], v228 offset:43584
	s_waitcnt lgkmcnt(1)
	v_mfma_f32_16x16x32_bf16 v[144:147], v[168:171], v[172:175], v[144:147]
	ds_read_b128 v[168:171], v228 offset:47936
	s_waitcnt lgkmcnt(1)
	v_mfma_f32_16x16x32_bf16 v[148:151], v[176:179], v[172:175], v[148:151]
	ds_read_b128 v[176:179], v228 offset:52288
	s_waitcnt lgkmcnt(1)
	v_mfma_f32_16x16x32_bf16 v[152:155], v[168:171], v[172:175], v[152:155]
	ds_read_b128 v[168:171], v228 offset:56640
	s_waitcnt lgkmcnt(1)
	v_mfma_f32_16x16x32_bf16 v[156:159], v[176:179], v[172:175], v[156:159]
	s_waitcnt lgkmcnt(0)
	v_mfma_f32_16x16x32_bf16 v[160:163], v[168:171], v[172:175], v[160:163]
	ds_read_b128 v[168:171], v228 offset:60992
	ds_read_b128 v[176:179], v228 offset:65344
	global_load_dwordx4 v[180:183], v[90:91], off offset:2176
	s_waitcnt lgkmcnt(1)
	v_mfma_f32_16x16x32_bf16 v[164:167], v[168:171], v[172:175], v[164:167]
	ds_read_b128 v[168:171], v228 offset:128
	s_waitcnt lgkmcnt(1)
	v_mfma_f32_16x16x32_bf16 v[8:11], v[176:179], v[172:175], v[8:11]
	ds_read_b128 v[172:175], v228 offset:4480
	s_waitcnt vmcnt(0) lgkmcnt(1)
	v_mfma_f32_16x16x32_bf16 v[12:15], v[168:171], v[180:183], v[12:15]
	ds_read_b128 v[168:171], v228 offset:8832
	s_waitcnt lgkmcnt(1)
	v_mfma_f32_16x16x32_bf16 v[30:33], v[172:175], v[180:183], v[30:33]
	ds_read_b128 v[172:175], v228 offset:13184
	s_waitcnt lgkmcnt(1)
	v_mfma_f32_16x16x32_bf16 v[34:37], v[168:171], v[180:183], v[34:37]
	ds_read_b128 v[168:171], v228 offset:17536
	s_waitcnt lgkmcnt(1)
	v_mfma_f32_16x16x32_bf16 v[60:63], v[172:175], v[180:183], v[60:63]
	ds_read_b128 v[172:175], v228 offset:21888
	s_waitcnt lgkmcnt(1)
	v_mfma_f32_16x16x32_bf16 v[120:123], v[168:171], v[180:183], v[120:123]
	ds_read_b128 v[168:171], v228 offset:26240
	s_waitcnt lgkmcnt(1)
	v_mfma_f32_16x16x32_bf16 v[124:127], v[172:175], v[180:183], v[124:127]
	ds_read_b128 v[172:175], v228 offset:30592
	s_waitcnt lgkmcnt(1)
	v_mfma_f32_16x16x32_bf16 v[128:131], v[168:171], v[180:183], v[128:131]
	ds_read_b128 v[168:171], v228 offset:34944
	s_waitcnt lgkmcnt(1)
; #define MFMA16(b, a, c) __builtin_amdgcn_mfma_f32_16x16x32_bf16((b), (a), (c), 0, 0, 0)
; __device__ __forceinline__ void mlstm_D(LAS unsigned char* lds, int c, int h, const bf16_t* Z, const float* gi, const float* bcum, const float* marr, const bf16_t* CST, const float* NST,
;                                         const float* hgain, bf16_t* YCAT) {
;     ...
;     for (int half = 0; half < 2; ++half) {
;         __syncthreads();
;         stage_tile<DH, 128, 8>(X, cst + half * 128, DH, tid);
;         __syncthreads();
; #pragma unroll
;         for (int ks = 0; ks < 4; ++ks)
;             { const bf16x8 aqh = *(const bf16x8*)(Z + trow * EVN + 1024 + h * DH + 32 * (half * 4 + ks) + 8 * fq);
; #pragma unroll
;               for (int j = 0; j < 16; ++j) acc[j] = MFMA16(row_frag(X, (128 + 8) * 2, 16 * j, 32 * ks, lane), aqh, acc[j]);
;               asm volatile("" ::: "memory"); }
	v_mfma_f32_16x16x32_bf16 v[136:139], v[172:175], v[180:183], v[136:139]
	ds_read_b128 v[172:175], v228 offset:39296
	s_waitcnt lgkmcnt(1)
	v_mfma_f32_16x16x32_bf16 v[140:143], v[168:171], v[180:183], v[140:143]
	ds_read_b128 v[168:171], v228 offset:43648
	s_waitcnt lgkmcnt(1)
	v_mfma_f32_16x16x32_bf16 v[144:147], v[172:175], v[180:183], v[144:147]
	ds_read_b128 v[172:175], v228 offset:48000
	s_waitcnt lgkmcnt(1)
	v_mfma_f32_16x16x32_bf16 v[148:151], v[168:171], v[180:183], v[148:151]
	ds_read_b128 v[168:171], v228 offset:52352
	s_waitcnt lgkmcnt(1)
	v_mfma_f32_16x16x32_bf16 v[152:155], v[172:175], v[180:183], v[152:155]
	ds_read_b128 v[172:175], v228 offset:56704
	s_waitcnt lgkmcnt(1)
	v_mfma_f32_16x16x32_bf16 v[156:159], v[168:171], v[180:183], v[156:159]
	s_waitcnt lgkmcnt(0)
	v_mfma_f32_16x16x32_bf16 v[160:163], v[172:175], v[180:183], v[160:163]
	ds_read_b128 v[168:171], v228 offset:61056
	ds_read_b128 v[172:175], v228 offset:65408
	global_load_dwordx4 v[176:179], v[90:91], off offset:2240
	s_waitcnt lgkmcnt(1)
	v_mfma_f32_16x16x32_bf16 v[164:167], v[168:171], v[180:183], v[164:167]
	ds_read_b128 v[168:171], v228 offset:192
	s_waitcnt lgkmcnt(1)
	v_mfma_f32_16x16x32_bf16 v[8:11], v[172:175], v[180:183], v[8:11]
	ds_read_b128 v[172:175], v228 offset:4544
	s_waitcnt vmcnt(0) lgkmcnt(1)
	v_mfma_f32_16x16x32_bf16 v[12:15], v[168:171], v[176:179], v[12:15]
	ds_read_b128 v[168:171], v228 offset:8896
	s_waitcnt lgkmcnt(1)
	v_mfma_f32_16x16x32_bf16 v[30:33], v[172:175], v[176:179], v[30:33]
	ds_read_b128 v[172:175], v228 offset:13248
	s_waitcnt lgkmcnt(1)
	v_mfma_f32_16x16x32_bf16 v[34:37], v[168:171], v[176:179], v[34:37]
	ds_read_b128 v[168:171], v228 offset:17600
	s_waitcnt lgkmcnt(1)
	v_mfma_f32_16x16x32_bf16 v[60:63], v[172:175], v[176:179], v[60:63]
	ds_read_b128 v[172:175], v228 offset:21952
	s_waitcnt lgkmcnt(1)
	v_mfma_f32_16x16x32_bf16 v[120:123], v[168:171], v[176:179], v[120:123]
	ds_read_b128 v[168:171], v228 offset:26304
	s_waitcnt lgkmcnt(1)
	v_mfma_f32_16x16x32_bf16 v[124:127], v[172:175], v[176:179], v[124:127]
	ds_read_b128 v[172:175], v228 offset:30656
	s_waitcnt lgkmcnt(1)
	v_mfma_f32_16x16x32_bf16 v[128:131], v[168:171], v[176:179], v[128:131]
	ds_read_b128 v[168:171], v228 offset:35008
	s_waitcnt lgkmcnt(1)
	v_mfma_f32_16x16x32_bf16 v[136:139], v[172:175], v[176:179], v[136:139]
	ds_read_b128 v[172:175], v228 offset:39360
	s_waitcnt lgkmcnt(1)
	v_mfma_f32_16x16x32_bf16 v[140:143], v[168:171], v[176:179], v[140:143]
	ds_read_b128 v[168:171], v228 offset:43712
	s_waitcnt lgkmcnt(1)
	v_mfma_f32_16x16x32_bf16 v[144:147], v[172:175], v[176:179], v[144:147]
	ds_read_b128 v[172:175], v228 offset:48064
	s_waitcnt lgkmcnt(1)
	v_mfma_f32_16x16x32_bf16 v[148:151], v[168:171], v[176:179], v[148:151]
	s_waitcnt lgkmcnt(0)
	v_mfma_f32_16x16x32_bf16 v[152:155], v[172:175], v[176:179], v[152:155]
	ds_read_b128 v[168:171], v228 offset:52416
	ds_read_b128 v[172:175], v228 offset:56768
	s_waitcnt lgkmcnt(1)
	v_mfma_f32_16x16x32_bf16 v[156:159], v[168:171], v[176:179], v[156:159]
	ds_read_b128 v[168:171], v228 offset:61120
	ds_read_b128 v[180:183], v228 offset:65472
	s_waitcnt lgkmcnt(0)
	s_barrier
	global_load_dwordx4 v[184:187], v[2:3], off offset:256
	s_nop 0
	global_load_dwordx4 v[2:5], v[4:5], off offset:256
	s_nop 0
	global_load_dwordx4 v[188:191], v[6:7], off offset:256
	s_nop 0
	global_load_dwordx4 v[192:195], v[192:193], off offset:256
	s_nop 0
	global_load_dwordx4 v[196:199], v[196:197], off offset:256
	s_nop 0
	global_load_dwordx4 v[200:203], v[200:201], off offset:256
	s_nop 0
	global_load_dwordx4 v[204:207], v[204:205], off offset:256
	s_nop 0
	global_load_dwordx4 v[208:211], v[208:209], off offset:256
	s_waitcnt vmcnt(7)
	ds_write_b128 v16, v[184:187]
	s_waitcnt vmcnt(6)
	ds_write_b128 v17, v[2:5]
	s_waitcnt vmcnt(5)
	ds_write_b128 v20, v[188:191]
	s_waitcnt vmcnt(4)
	ds_write_b128 v21, v[192:195]
	s_waitcnt vmcnt(3)
	ds_write_b128 v64, v[196:199]
	s_waitcnt vmcnt(2)
	ds_write_b128 v65, v[200:203]
	s_waitcnt vmcnt(1)
	ds_write_b128 v119, v[204:207]
	s_waitcnt vmcnt(0)
	ds_write_b128 v135, v[208:211]
	s_waitcnt lgkmcnt(0)
	s_barrier
	global_load_dwordx4 v[2:5], v[90:91], off offset:2304
	v_mfma_f32_16x16x32_bf16 v[164:167], v[168:171], v[176:179], v[164:167]
	ds_read_b128 v[168:171], v228
	v_mad_i64_i32 v[64:65], s[2:3], v93, s68, 0
	v_mfma_f32_16x16x32_bf16 v[160:163], v[172:175], v[176:179], v[160:163]
	ds_read_b128 v[172:175], v228 offset:4352
	v_and_b32_e32 v119, 63, v99
	v_mfma_f32_16x16x32_bf16 v[6:9], v[180:183], v[176:179], v[8:11]
	s_waitcnt vmcnt(0) lgkmcnt(1)
	v_mfma_f32_16x16x32_bf16 v[10:13], v[168:171], v[2:5], v[12:15]
	s_nop 2
	ds_read_b128 v[14:17], v228 offset:8704
	ds_read_b128 v[168:171], v228 offset:13056
	s_waitcnt lgkmcnt(1)
	v_mfma_f32_16x16x32_bf16 v[14:17], v[14:17], v[2:5], v[34:37]
	s_nop 2
	ds_read_b128 v[34:37], v228 offset:17408
	s_waitcnt lgkmcnt(1)
	v_mfma_f32_16x16x32_bf16 v[60:63], v[168:171], v[2:5], v[60:63]
	ds_read_b128 v[168:171], v228 offset:21760
	s_waitcnt lgkmcnt(1)
	v_mfma_f32_16x16x32_bf16 v[34:37], v[34:37], v[2:5], v[120:123]
	s_nop 2
	ds_read_b128 v[120:123], v228 offset:26112
	s_waitcnt lgkmcnt(1)
	v_mfma_f32_16x16x32_bf16 v[124:127], v[168:171], v[2:5], v[124:127]
	ds_read_b128 v[168:171], v228 offset:30464
	s_waitcnt lgkmcnt(1)
	v_mfma_f32_16x16x32_bf16 v[120:123], v[120:123], v[2:5], v[128:131]
	s_nop 2
	ds_read_b128 v[128:131], v228 offset:34816
	s_waitcnt lgkmcnt(1)
	v_mfma_f32_16x16x32_bf16 v[136:139], v[168:171], v[2:5], v[136:139]
	ds_read_b128 v[168:171], v228 offset:39168
	s_waitcnt lgkmcnt(1)
; #define LAS __attribute__((address_space(3)))
; __device__ __forceinline__ unsigned cvt_pk_bf16(float lo, float hi) { unsigned r; asm volatile("v_cvt_pk_bf16_f32 %0, %1, %2" : "=v"(r) : "v"(lo), "v"(hi)); return r; }
; #define MFMA16(b, a, c) __builtin_amdgcn_mfma_f32_16x16x32_bf16((b), (a), (c), 0, 0, 0)
; __device__ __forceinline__ void mlstm_D(LAS unsigned char* lds, int c, int h, const bf16_t* Z, const float* gi, const float* bcum, const float* marr, const bf16_t* CST, const float* NST,
;                                         const float* hgain, bf16_t* YCAT) {
;     ...
;         for (int i = 0; i < 4; ++i) { const int s = 16 * j + 4 * fq + i; const float p = (s <= tl) ? S[j][i] * SC * expf(gS[s] - Mt) : 0.f; pv[i] = p; rsum += p; }
;         u32x2 w; w.x = cvt_pk_bf16(pv[0], pv[1]); w.y = cvt_pk_bf16(pv[2], pv[3]);
;         *(LAS u32x2*)(Pw + fr * PRS + (16 * j + 4 * fq) * 2) = w; }
;     rsum += __shfl_xor(rsum, 16); rsum += __shfl_xor(rsum, 32);
;     const float den = wi * nq + rsum;
;     f32x4 acc[16];
; #pragma unroll
;     for (int j = 0; j < 16; ++j) acc[j] = (f32x4){0.f, 0.f, 0.f, 0.f};
;     const bf16_t* cst = CST + (size_t)(c * NH + h) * DH * DH;
; #pragma unroll
;     for (int half = 0; half < 2; ++half) {
;         __syncthreads();
;         stage_tile<DH, 128, 8>(X, cst + half * 128, DH, tid);
;         __syncthreads();
; #pragma unroll
;         for (int ks = 0; ks < 4; ++ks)
;             { const bf16x8 aqh = *(const bf16x8*)(Z + trow * EVN + 1024 + h * DH + 32 * (half * 4 + ks) + 8 * fq);
; #pragma unroll
;               for (int j = 0; j < 16; ++j) acc[j] = MFMA16(row_frag(X, (128 + 8) * 2, 16 * j, 32 * ks, lane), aqh, acc[j]);
;               asm volatile("" ::: "memory"); }
	v_mfma_f32_16x16x32_bf16 v[128:131], v[128:131], v[2:5], v[140:143]
	s_nop 2
	ds_read_b128 v[140:143], v228 offset:43520
	s_waitcnt lgkmcnt(1)
	v_mfma_f32_16x16x32_bf16 v[144:147], v[168:171], v[2:5], v[144:147]
	ds_read_b128 v[168:171], v228 offset:47872
	s_waitcnt lgkmcnt(1)
	v_mfma_f32_16x16x32_bf16 v[140:143], v[140:143], v[2:5], v[148:151]
	s_nop 2
	ds_read_b128 v[148:151], v228 offset:52224
	s_waitcnt lgkmcnt(1)
	v_mfma_f32_16x16x32_bf16 v[152:155], v[168:171], v[2:5], v[152:155]
	ds_read_b128 v[168:171], v228 offset:56576
	s_waitcnt lgkmcnt(1)
	v_mfma_f32_16x16x32_bf16 v[148:151], v[148:151], v[2:5], v[156:159]
	s_waitcnt lgkmcnt(0)
	v_mfma_f32_16x16x32_bf16 v[156:159], v[168:171], v[2:5], v[160:163]
	s_nop 2
	ds_read_b128 v[160:163], v228 offset:60928
	ds_read_b128 v[168:171], v228 offset:65280
	v_mfma_f32_16x16x32_bf16 v[30:33], v[172:175], v[2:5], v[30:33]
	global_load_dwordx4 v[172:175], v[90:91], off offset:2368
	s_waitcnt lgkmcnt(1)
	v_mfma_f32_16x16x32_bf16 v[160:163], v[160:163], v[2:5], v[164:167]
	s_nop 2
	ds_read_b128 v[164:167], v228 offset:64
	s_waitcnt lgkmcnt(1)
	v_mfma_f32_16x16x32_bf16 v[2:5], v[168:171], v[2:5], v[6:9]
	s_nop 2
	ds_read_b128 v[6:9], v228 offset:4416
	s_waitcnt vmcnt(0) lgkmcnt(1)
	v_mfma_f32_16x16x32_bf16 v[10:13], v[164:167], v[172:175], v[10:13]
	ds_read_b128 v[164:167], v228 offset:8768
	s_waitcnt lgkmcnt(1)
	v_mfma_f32_16x16x32_bf16 v[6:9], v[6:9], v[172:175], v[30:33]
	s_nop 2
	ds_read_b128 v[30:33], v228 offset:13120
	s_waitcnt lgkmcnt(1)
	v_mfma_f32_16x16x32_bf16 v[14:17], v[164:167], v[172:175], v[14:17]
	ds_read_b128 v[164:167], v228 offset:17472
	s_waitcnt lgkmcnt(1)
	v_mfma_f32_16x16x32_bf16 v[30:33], v[30:33], v[172:175], v[60:63]
	s_nop 2
	ds_read_b128 v[60:63], v228 offset:21824
	s_waitcnt lgkmcnt(1)
	v_mfma_f32_16x16x32_bf16 v[34:37], v[164:167], v[172:175], v[34:37]
	ds_read_b128 v[164:167], v228 offset:26176
	s_waitcnt lgkmcnt(1)
	v_mfma_f32_16x16x32_bf16 v[60:63], v[60:63], v[172:175], v[124:127]
	s_nop 2
	ds_read_b128 v[124:127], v228 offset:30528
	s_waitcnt lgkmcnt(1)
	v_mfma_f32_16x16x32_bf16 v[120:123], v[164:167], v[172:175], v[120:123]
	ds_read_b128 v[164:167], v228 offset:34880
	s_waitcnt lgkmcnt(1)
	v_mfma_f32_16x16x32_bf16 v[124:127], v[124:127], v[172:175], v[136:139]
	s_nop 2
	ds_read_b128 v[136:139], v228 offset:39232
	s_waitcnt lgkmcnt(1)
	v_mfma_f32_16x16x32_bf16 v[128:131], v[164:167], v[172:175], v[128:131]
	ds_read_b128 v[164:167], v228 offset:43584
	s_waitcnt lgkmcnt(1)
	v_mfma_f32_16x16x32_bf16 v[136:139], v[136:139], v[172:175], v[144:147]
	s_nop 2
	ds_read_b128 v[144:147], v228 offset:47936
	s_waitcnt lgkmcnt(1)
	v_mfma_f32_16x16x32_bf16 v[140:143], v[164:167], v[172:175], v[140:143]
	ds_read_b128 v[164:167], v228 offset:52288
	s_waitcnt lgkmcnt(1)
	v_mfma_f32_16x16x32_bf16 v[144:147], v[144:147], v[172:175], v[152:155]
	s_nop 2
	ds_read_b128 v[152:155], v228 offset:56640
	s_waitcnt lgkmcnt(1)
	v_mfma_f32_16x16x32_bf16 v[148:151], v[164:167], v[172:175], v[148:151]
	ds_read_b128 v[164:167], v228 offset:60992
	ds_read_b128 v[168:171], v228 offset:65344
	s_waitcnt lgkmcnt(2)
	v_mfma_f32_16x16x32_bf16 v[152:155], v[152:155], v[172:175], v[156:159]
	s_nop 2
	global_load_dwordx4 v[156:159], v[90:91], off offset:2432
	ds_read_b128 v[176:179], v228 offset:128
	ds_read_b128 v[180:183], v228 offset:4480
	s_waitcnt lgkmcnt(3)
	v_mfma_f32_16x16x32_bf16 v[160:163], v[164:167], v[172:175], v[160:163]
	ds_read_b128 v[164:167], v228 offset:8832
	ds_read_b128 v[184:187], v228 offset:13184
	ds_read_b128 v[188:191], v228 offset:17536
	ds_read_b128 v[192:195], v228 offset:21888
	s_waitcnt lgkmcnt(6)
	v_mfma_f32_16x16x32_bf16 v[168:171], v[168:171], v[172:175], v[2:5]
	ds_read_b128 v[172:175], v228 offset:26240
	ds_read_b128 v[196:199], v228 offset:30592
	ds_read_b128 v[200:203], v228 offset:34944
	ds_read_b128 v[204:207], v228 offset:39296
	s_waitcnt vmcnt(0) lgkmcnt(9)
	v_mfma_f32_16x16x32_bf16 v[176:179], v[176:179], v[156:159], v[10:13]
	s_nop 2
	ds_read_b128 v[10:13], v228 offset:43648
	ds_read_b128 v[208:211], v228 offset:48000
	ds_read_b128 v[212:215], v228 offset:52352
	ds_read_b128 v[216:219], v228 offset:56704
	ds_read_b128 v[220:223], v228 offset:61056
	ds_read_b128 v[224:227], v228 offset:65408
	global_load_dwordx4 v[2:5], v[90:91], off offset:2496
	s_waitcnt lgkmcnt(14)
	v_mfma_f32_16x16x32_bf16 v[180:183], v[180:183], v[156:159], v[6:9]
	v_mad_i64_i32 v[90:91], s[2:3], v100, s68, 0
	s_nop 1
	v_add_f32_e32 v6, 0, v39
	v_add_f32_e32 v6, v6, v38
	v_add_f32_e32 v6, v6, v41
	v_add_f32_e32 v6, v6, v40
	v_add_f32_e32 v6, v6, v43
	v_add_f32_e32 v6, v6, v42
	s_waitcnt lgkmcnt(13)
	v_mfma_f32_16x16x32_bf16 v[164:167], v[164:167], v[156:159], v[14:17]
	s_nop 2
	v_add_f32_e32 v14, v6, v27
	s_waitcnt lgkmcnt(5)
	v_mfma_f32_16x16x32_bf16 v[6:9], v[10:13], v[156:159], v[140:143]
	v_add_f32_e32 v10, v14, v26
	v_add_f32_e32 v10, v10, v29
	v_add_f32_e32 v14, v10, v28
	v_add_f32_e32 v14, v14, v23
	v_add_f32_e32 v14, v14, v22
	v_add_f32_e32 v20, v14, v25
	v_add_f32_e32 v20, v20, v24
	v_add_f32_e32 v19, v20, v19
	v_add_f32_e32 v22, v19, v18
	v_add_f32_e32 v22, v22, v45
	v_add_f32_e32 v26, v22, v44
	v_add_f32_e32 v26, v26, v47
	v_add_f32_e32 v46, v26, v46
	v_add_f32_e32 v46, v46, v49
	v_add_f32_e32 v135, v46, v48
	v_add_f32_e32 v51, v135, v51
	v_add_f32_e32 v50, v51, v50
	v_add_f32_e32 v50, v50, v56
	v_add_f32_e32 v50, v50, v54
	s_waitcnt lgkmcnt(4)
	v_mfma_f32_16x16x32_bf16 v[10:13], v[208:211], v[156:159], v[144:147]
	ds_read_b128 v[42:45], v228 offset:192
	ds_read_b128 v[46:49], v228 offset:8896
	ds_read_b128 v[140:143], v228 offset:13248
	s_waitcnt lgkmcnt(6)
; #define LAS __attribute__((address_space(3)))
; #define MFMA16(b, a, c) __builtin_amdgcn_mfma_f32_16x16x32_bf16((b), (a), (c), 0, 0, 0)
; __device__ __forceinline__ void mlstm_D(LAS unsigned char* lds, int c, int h, const bf16_t* Z, const float* gi, const float* bcum, const float* marr, const bf16_t* CST, const float* NST,
;                                         const float* hgain, bf16_t* YCAT) {
;     ...
;     const float Mt = Mrow[tl]; const float SC = 0.0625f; const float wi = expf(mc - Mt) * SC;
;     float rsum = 0.f;
; #pragma unroll
;     for (int j = 0; j < 8; ++j) { float pv[4];
; #pragma unroll
;         for (int i = 0; i < 4; ++i) { const int s = 16 * j + 4 * fq + i; const float p = (s <= tl) ? S[j][i] * SC * expf(gS[s] - Mt) : 0.f; pv[i] = p; rsum += p; }
;         u32x2 w; w.x = cvt_pk_bf16(pv[0], pv[1]); w.y = cvt_pk_bf16(pv[2], pv[3]);
;         *(LAS u32x2*)(Pw + fr * PRS + (16 * j + 4 * fq) * 2) = w; }
;     rsum += __shfl_xor(rsum, 16); rsum += __shfl_xor(rsum, 32);
;     const float den = wi * nq + rsum;
;     f32x4 acc[16];
; #pragma unroll
;     for (int j = 0; j < 16; ++j) acc[j] = (f32x4){0.f, 0.f, 0.f, 0.f};
;     const bf16_t* cst = CST + (size_t)(c * NH + h) * DH * DH;
; #pragma unroll
;     for (int half = 0; half < 2; ++half) {
;         __syncthreads();
;         stage_tile<DH, 128, 8>(X, cst + half * 128, DH, tid);
;         __syncthreads();
; #pragma unroll
;         for (int ks = 0; ks < 4; ++ks)
;             { const bf16x8 aqh = *(const bf16x8*)(Z + trow * EVN + 1024 + h * DH + 32 * (half * 4 + ks) + 8 * fq);
; #pragma unroll
;               for (int j = 0; j < 16; ++j) acc[j] = MFMA16(row_frag(X, (128 + 8) * 2, 16 * j, 32 * ks, lane), aqh, acc[j]);
;               asm volatile("" ::: "memory"); }
;     }
; #pragma unroll
;     for (int j = 0; j < 16; ++j) acc[j] = acc[j] * wi;
;     __syncthreads();
;     stage_tile<CH, DH, 16>(X, Z + (size_t)t0 * EVN + 3072 + h * DH, EVN, tid);
;     __syncthreads();
; #pragma unroll 1
;     for (int ks = 0; ks < 4; ++ks) { const bf16x8 ap = *(const LAS bf16x8*)(Pw + fr * PRS + (32 * ks + 8 * fq) * 2);
; #pragma unroll
;         for (int j = 0; j < 16; ++j) acc[j] = MFMA16(tr_frag(X, (DH + 16) * 2, 32 * ks, 16 * j, lane), ap, acc[j]); }
;     const float mt = bcum[trow * 4 + h] + Mt; const float inv = 1.0f / fmaxf(fabsf(den), expf(-mt));
	v_mfma_f32_16x16x32_bf16 v[14:17], v[212:215], v[156:159], v[148:151]
	ds_read_b128 v[144:147], v228 offset:17600
	v_add_f32_e32 v50, v50, v58
	v_add_f32_e32 v50, v50, v57
	ds_read_b128 v[148:151], v228 offset:21952
	v_mfma_f32_16x16x32_bf16 v[184:187], v[184:187], v[156:159], v[30:33]
	v_add_f32_e32 v50, v50, v59
	v_sub_f32_e32 v51, v95, v116
	v_mul_f32_e32 v54, 0x3fb8aa3b, v51
	v_mfma_f32_16x16x32_bf16 v[188:191], v[188:191], v[156:159], v[34:37]
	v_mad_i64_i32 v[32:33], s[2:3], v105, s68, 0
	v_mad_i64_i32 v[30:31], s[2:3], v106, s68, 0
	v_mfma_f32_16x16x32_bf16 v[60:63], v[192:195], v[156:159], v[60:63]
	v_mad_i64_i32 v[192:193], s[2:3], v102, s68, 0
	v_mad_i64_i32 v[36:37], s[2:3], v103, s68, 0
	v_mad_i64_i32 v[34:35], s[2:3], v104, s68, 0
	v_mfma_f32_16x16x32_bf16 v[120:123], v[172:175], v[156:159], v[120:123]
	s_lshl_b32 s2, s5, 1
	s_add_u32 s3, s37, s2
	s_addc_u32 s7, s66, 0
	v_mfma_f32_16x16x32_bf16 v[124:127], v[196:199], v[156:159], v[124:127]
	s_add_u32 s6, s3, 0x1800
	s_addc_u32 s7, s7, 0
	v_lshl_add_u64 v[36:37], s[6:7], 0, v[36:37]
	v_mfma_f32_16x16x32_bf16 v[128:131], v[200:203], v[156:159], v[128:131]
	v_lshl_add_u64 v[36:37], v[82:83], 1, v[36:37]
	v_lshl_add_u64 v[34:35], s[6:7], 0, v[34:35]
	v_lshl_add_u64 v[34:35], v[84:85], 1, v[34:35]
	v_mfma_f32_16x16x32_bf16 v[38:41], v[204:207], v[156:159], v[136:139]
	v_lshl_add_u64 v[32:33], s[6:7], 0, v[32:33]
	v_lshl_add_u64 v[32:33], v[86:87], 1, v[32:33]
	v_lshl_add_u64 v[30:31], s[6:7], 0, v[30:31]
	s_waitcnt lgkmcnt(7)
	v_mfma_f32_16x16x32_bf16 v[18:21], v[216:219], v[156:159], v[152:155]
	ds_read_b128 v[136:139], v228 offset:4544
	v_lshl_add_u64 v[30:31], v[88:89], 1, v[30:31]
	v_cmp_ngt_f32_e32 vcc, s71, v51
	s_waitcnt lgkmcnt(7)
	v_mfma_f32_16x16x32_bf16 v[22:25], v[220:223], v[156:159], v[160:163]
	s_mov_b32 s3, 4
	s_waitcnt lgkmcnt(6)
	v_mfma_f32_16x16x32_bf16 v[26:29], v[224:227], v[156:159], v[168:171]
	ds_read_b128 v[56:59], v228 offset:26304
	ds_read_b128 v[152:155], v228 offset:30656
	ds_read_b128 v[156:159], v228 offset:35008
	ds_read_b128 v[160:163], v228 offset:39360
	s_waitcnt vmcnt(0) lgkmcnt(2)
	v_mfma_f32_16x16x32_bf16 v[124:127], v[152:155], v[2:5], v[124:127]
	s_waitcnt lgkmcnt(0)
	v_mfma_f32_16x16x32_bf16 v[152:155], v[160:163], v[2:5], v[38:41]
	s_nop 2
	v_lshl_add_u64 v[38:39], s[6:7], 0, v[64:65]
	v_lshl_add_u64 v[38:39], v[74:75], 1, v[38:39]
	v_mfma_f32_16x16x32_bf16 v[42:45], v[42:45], v[2:5], v[176:179]
	v_mfma_f32_16x16x32_bf16 v[46:49], v[46:49], v[2:5], v[164:167]
	v_mfma_f32_16x16x32_bf16 v[148:151], v[148:151], v[2:5], v[60:63]
	s_nop 2
	ds_read_b128 v[60:63], v228 offset:43712
	ds_read_b128 v[164:167], v228 offset:48064
	ds_read_b128 v[168:171], v228 offset:52416
	ds_read_b128 v[172:175], v228 offset:56768
	v_mfma_f32_16x16x32_bf16 v[120:123], v[56:59], v[2:5], v[120:123]
	ds_read_b128 v[56:59], v228 offset:61120
	ds_read_b128 v[176:179], v228 offset:65472
	v_lshlrev_b32_e32 v247, 4, v70
	v_mov_b32_e32 v248, s36
	v_lshl_add_u32 v247, v248, 2, v247
	global_load_dword v246, v247, s[34:35]
	s_waitcnt lgkmcnt(0)
	s_barrier
	v_mfma_f32_16x16x32_bf16 v[128:131], v[156:159], v[2:5], v[128:131]
	global_load_dwordx4 v[156:159], v[38:39], off
	v_lshl_add_u64 v[38:39], s[6:7], 0, v[90:91]
	v_lshl_add_u64 v[38:39], v[76:77], 1, v[38:39]
	global_load_dwordx4 v[160:163], v[38:39], off
	v_lshl_add_u64 v[38:39], s[6:7], 0, v[132:133]
	v_lshl_add_u64 v[38:39], v[78:79], 1, v[38:39]
	v_mfma_f32_16x16x32_bf16 v[136:139], v[136:139], v[2:5], v[180:183]
	global_load_dwordx4 v[82:85], v[34:35], off
	global_load_dwordx4 v[86:89], v[30:31], off
	v_mul_lo_u32 v77, v93, s75
	global_load_dwordx4 v[180:183], v[38:39], off
	v_lshl_add_u64 v[38:39], s[6:7], 0, v[192:193]
	v_lshl_add_u64 v[38:39], v[80:81], 1, v[38:39]
	global_load_dwordx4 v[78:81], v[38:39], off
	v_mfma_f32_16x16x32_bf16 v[140:143], v[140:143], v[2:5], v[184:187]
	v_add3_u32 v77, s51, v77, v107
	v_fma_f32 v30, v51, s70, -v54
	v_rndne_f32_e32 v31, v54
	global_load_dwordx4 v[184:187], v[36:37], off
	v_mfma_f32_16x16x32_bf16 v[144:147], v[144:147], v[2:5], v[188:191]
	v_fmac_f32_e32 v30, 0x32a5705f, v51
	s_waitcnt vmcnt(6)
	ds_write_b128 v77, v[156:159]
	global_load_dwordx4 v[188:191], v[32:33], off
	v_mul_lo_u32 v77, v100, s75
	v_add3_u32 v77, s51, v77, v108
	s_waitcnt vmcnt(6)
	ds_write_b128 v77, v[160:163]
	v_mul_lo_u32 v77, v101, s75
	v_add3_u32 v77, s51, v77, v109
	v_sub_f32_e32 v32, v54, v31
	v_add_f32_e32 v30, v32, v30
	v_exp_f32_e32 v30, v30
	s_waitcnt vmcnt(3)
	ds_write_b128 v77, v[180:183]
	v_mul_lo_u32 v77, v102, s75
	v_add3_u32 v77, s51, v77, v110
	s_waitcnt vmcnt(2)
	ds_write_b128 v77, v[78:81]
	v_mul_lo_u32 v77, v103, s75
	v_add3_u32 v77, s51, v77, v111
	v_cvt_i32_f32_e32 v31, v31
	v_add_f32_e32 v32, v50, v52
	s_waitcnt vmcnt(1)
	ds_write_b128 v77, v[184:187]
	v_mul_lo_u32 v77, v104, s75
	v_add3_u32 v77, s51, v77, v112
	ds_write_b128 v77, v[82:85]
	v_mul_lo_u32 v77, v105, s75
	v_add_f32_e32 v32, v32, v55
	v_add3_u32 v77, s51, v77, v113
	v_add_f32_e32 v75, v32, v53
	v_mfma_f32_16x16x32_bf16 v[6:9], v[60:63], v[2:5], v[6:9]
	v_ldexp_f32 v30, v30, v31
	ds_bpermute_b32 v76, v98, v75
	v_cndmask_b32_e32 v30, 0, v30, vcc
	v_mfma_f32_16x16x32_bf16 v[10:13], v[164:167], v[2:5], v[10:13]
	v_cmp_nlt_f32_e32 vcc, s72, v51
	v_lshlrev_b32_e32 v78, 3, v119
	v_add_u32_e32 v79, s4, v118
	v_mfma_f32_16x16x32_bf16 v[14:17], v[168:171], v[2:5], v[14:17]
	v_add3_u32 v66, v79, v66, s53
	s_waitcnt vmcnt(0)
; #define LAS __attribute__((address_space(3)))
; #define MFMA16(b, a, c) __builtin_amdgcn_mfma_f32_16x16x32_bf16((b), (a), (c), 0, 0, 0)
; __device__ __forceinline__ void mlstm_D(LAS unsigned char* lds, int c, int h, const bf16_t* Z, const float* gi, const float* bcum, const float* marr, const bf16_t* CST, const float* NST,
;                                         const float* hgain, bf16_t* YCAT) {
;     ...
;     for (int j = 0; j < 16; ++j) acc[j] = acc[j] * wi;
;     __syncthreads();
;     stage_tile<CH, DH, 16>(X, Z + (size_t)t0 * EVN + 3072 + h * DH, EVN, tid);
;     __syncthreads();
; #pragma unroll 1
;     for (int ks = 0; ks < 4; ++ks) { const bf16x8 ap = *(const LAS bf16x8*)(Pw + fr * PRS + (32 * ks + 8 * fq) * 2);
; #pragma unroll
;         for (int j = 0; j < 16; ++j) acc[j] = MFMA16(tr_frag(X, (DH + 16) * 2, 32 * ks, 16 * j, lane), ap, acc[j]); }
	ds_write_b128 v77, v[188:191]
	v_mul_lo_u32 v77, v106, s75
	v_mfma_f32_16x16x32_bf16 v[164:167], v[172:175], v[2:5], v[18:21]
	v_add3_u32 v77, s51, v77, v114
	ds_write_b128 v77, v[86:89]
	v_bfe_u32 v77, v99, 2, 2
	v_mfma_f32_16x16x32_bf16 v[168:171], v[56:59], v[2:5], v[22:25]
	v_cndmask_b32_e32 v18, v97, v30, vcc
	v_mul_u32_u24_e32 v77, 0x220, v77
	v_mul_f32_e32 v74, 0x3d800000, v18
	v_mfma_f32_16x16x32_bf16 v[2:5], v[176:179], v[2:5], v[26:29]
	v_mad_u32_u24 v77, v134, s73, v77
	v_pk_mul_f32 v[64:65], v[74:75], v[44:45] op_sel_hi:[0,1]
	v_pk_mul_f32 v[62:63], v[74:75], v[42:43] op_sel_hi:[0,1]
	v_pk_mul_f32 v[60:61], v[74:75], v[138:139] op_sel_hi:[0,1]
	v_pk_mul_f32 v[58:59], v[74:75], v[136:137] op_sel_hi:[0,1]
	v_pk_mul_f32 v[56:57], v[74:75], v[48:49] op_sel_hi:[0,1]
	v_pk_mul_f32 v[54:55], v[74:75], v[46:47] op_sel_hi:[0,1]
	v_pk_mul_f32 v[52:53], v[74:75], v[142:143] op_sel_hi:[0,1]
	v_pk_mul_f32 v[50:51], v[74:75], v[140:141] op_sel_hi:[0,1]
	v_pk_mul_f32 v[48:49], v[74:75], v[146:147] op_sel_hi:[0,1]
	v_pk_mul_f32 v[46:47], v[74:75], v[144:145] op_sel_hi:[0,1]
	v_pk_mul_f32 v[44:45], v[74:75], v[150:151] op_sel_hi:[0,1]
	v_pk_mul_f32 v[42:43], v[74:75], v[148:149] op_sel_hi:[0,1]
	v_pk_mul_f32 v[40:41], v[74:75], v[122:123] op_sel_hi:[0,1]
	v_pk_mul_f32 v[38:39], v[74:75], v[120:121] op_sel_hi:[0,1]
	v_pk_mul_f32 v[36:37], v[74:75], v[126:127] op_sel_hi:[0,1]
	v_pk_mul_f32 v[34:35], v[74:75], v[124:125] op_sel_hi:[0,1]
	v_pk_mul_f32 v[32:33], v[74:75], v[130:131] op_sel_hi:[0,1]
	v_pk_mul_f32 v[30:31], v[74:75], v[128:129] op_sel_hi:[0,1]
	v_pk_mul_f32 v[28:29], v[74:75], v[154:155] op_sel_hi:[0,1]
	v_pk_mul_f32 v[26:27], v[74:75], v[152:153] op_sel_hi:[0,1]
	v_pk_mul_f32 v[24:25], v[74:75], v[8:9] op_sel_hi:[0,1]
	v_pk_mul_f32 v[22:23], v[74:75], v[6:7] op_sel_hi:[0,1]
	v_pk_mul_f32 v[20:21], v[74:75], v[12:13] op_sel_hi:[0,1]
	v_pk_mul_f32 v[18:19], v[74:75], v[10:11] op_sel_hi:[0,1]
	v_pk_mul_f32 v[16:17], v[74:75], v[16:17] op_sel_hi:[0,1]
	v_pk_mul_f32 v[14:15], v[74:75], v[14:15] op_sel_hi:[0,1]
	v_pk_mul_f32 v[12:13], v[74:75], v[166:167] op_sel_hi:[0,1]
	v_pk_mul_f32 v[10:11], v[74:75], v[164:165] op_sel_hi:[0,1]
	v_pk_mul_f32 v[8:9], v[74:75], v[170:171] op_sel_hi:[0,1]
	v_pk_mul_f32 v[6:7], v[74:75], v[168:169] op_sel_hi:[0,1]
	v_pk_mul_f32 v[4:5], v[74:75], v[4:5] op_sel_hi:[0,1]
	v_pk_mul_f32 v[2:3], v[74:75], v[2:3] op_sel_hi:[0,1]
	v_and_or_b32 v77, v78, 24, v77
	s_waitcnt lgkmcnt(0)
	s_barrier
.LBB0_770:
	v_add_u32_e32 v82, s51, v66
	v_add_u32_e32 v90, s51, v77
	ds_read_b64_tr_b16 v[80:81], v90 offset:2176
	ds_read_b64_tr_b16 v[78:79], v90
	ds_read_b128 v[82:85], v82
	ds_read_b64_tr_b16 v[86:87], v90 offset:32
	ds_read_b64_tr_b16 v[88:89], v90 offset:2208
	ds_read_b64_tr_b16 v[102:103], v90 offset:2240
	ds_read_b64_tr_b16 v[100:101], v90 offset:64
	ds_read_b64_tr_b16 v[104:105], v90 offset:96
	ds_read_b64_tr_b16 v[108:109], v90 offset:480
	s_waitcnt lgkmcnt(6)
	v_mfma_f32_16x16x32_bf16 v[62:65], v[78:81], v[82:85], v[62:65]
	ds_read_b64_tr_b16 v[78:79], v90 offset:128
	ds_read_b64_tr_b16 v[106:107], v90 offset:2272
	ds_read_b64_tr_b16 v[80:81], v90 offset:2304
	s_add_i32 s3, s3, -1
	v_add_u32_e32 v66, 64, v66
	s_waitcnt lgkmcnt(7)
	v_mfma_f32_16x16x32_bf16 v[58:61], v[86:89], v[82:85], v[58:61]
	ds_read_b64_tr_b16 v[86:87], v90 offset:160
	ds_read_b64_tr_b16 v[88:89], v90 offset:2336
	s_cmp_lg_u32 s3, 0
	v_add_u32_e32 v77, 0x4400, v77
	s_waitcnt lgkmcnt(7)
	v_mfma_f32_16x16x32_bf16 v[54:57], v[100:103], v[82:85], v[54:57]
	s_waitcnt lgkmcnt(3)
	v_mfma_f32_16x16x32_bf16 v[50:53], v[104:107], v[82:85], v[50:53]
	ds_read_b64_tr_b16 v[102:103], v90 offset:2368
	ds_read_b64_tr_b16 v[100:101], v90 offset:192
	ds_read_b64_tr_b16 v[104:105], v90 offset:224
	s_waitcnt lgkmcnt(5)
	v_mfma_f32_16x16x32_bf16 v[46:49], v[78:81], v[82:85], v[46:49]
	ds_read_b64_tr_b16 v[78:79], v90 offset:256
	ds_read_b64_tr_b16 v[106:107], v90 offset:2400
	ds_read_b64_tr_b16 v[80:81], v90 offset:2432
	s_waitcnt lgkmcnt(6)
	v_mfma_f32_16x16x32_bf16 v[42:45], v[86:89], v[82:85], v[42:45]
	ds_read_b64_tr_b16 v[86:87], v90 offset:288
	ds_read_b64_tr_b16 v[88:89], v90 offset:2464
	s_waitcnt lgkmcnt(6)
	v_mfma_f32_16x16x32_bf16 v[38:41], v[100:103], v[82:85], v[38:41]
	s_waitcnt lgkmcnt(3)
	v_mfma_f32_16x16x32_bf16 v[34:37], v[104:107], v[82:85], v[34:37]
	ds_read_b64_tr_b16 v[102:103], v90 offset:2496
	ds_read_b64_tr_b16 v[100:101], v90 offset:320
	ds_read_b64_tr_b16 v[104:105], v90 offset:352
	s_waitcnt lgkmcnt(5)
	v_mfma_f32_16x16x32_bf16 v[30:33], v[78:81], v[82:85], v[30:33]
	ds_read_b64_tr_b16 v[78:79], v90 offset:384
	ds_read_b64_tr_b16 v[106:107], v90 offset:2528
	ds_read_b64_tr_b16 v[80:81], v90 offset:2560
	s_waitcnt lgkmcnt(6)
	v_mfma_f32_16x16x32_bf16 v[26:29], v[86:89], v[82:85], v[26:29]
	ds_read_b64_tr_b16 v[88:89], v90 offset:2592
	s_waitcnt lgkmcnt(5)
	v_mfma_f32_16x16x32_bf16 v[22:25], v[100:103], v[82:85], v[22:25]
	ds_read_b64_tr_b16 v[86:87], v90 offset:416
	ds_read_b64_tr_b16 v[100:101], v90 offset:448
	ds_read_b64_tr_b16 v[102:103], v90 offset:2624
	ds_read_b64_tr_b16 v[110:111], v90 offset:2656
	s_waitcnt lgkmcnt(6)
	v_mfma_f32_16x16x32_bf16 v[18:21], v[104:107], v[82:85], v[18:21]
	s_waitcnt lgkmcnt(5)
	v_mfma_f32_16x16x32_bf16 v[14:17], v[78:81], v[82:85], v[14:17]
	s_waitcnt lgkmcnt(3)
	v_mfma_f32_16x16x32_bf16 v[10:13], v[86:89], v[82:85], v[10:13]
	s_waitcnt lgkmcnt(1)
	v_mfma_f32_16x16x32_bf16 v[6:9], v[100:103], v[82:85], v[6:9]
	s_waitcnt lgkmcnt(0)
	v_mfma_f32_16x16x32_bf16 v[2:5], v[108:111], v[82:85], v[2:5]
	s_cbranch_scc1 .LBB0_770
; __device__ __forceinline__ void mlstm_D(LAS unsigned char* lds, int c, int h, const bf16_t* Z, const float* gi, const float* bcum, const float* marr, const bf16_t* CST, const float* NST,
;                                         const float* hgain, bf16_t* YCAT) {
;     ...
;     const float mt = bcum[trow * 4 + h] + Mt; const float inv = 1.0f / fmaxf(fabsf(den), expf(-mt));
;     float ss = 0.f;
; #pragma unroll
;     for (int j = 0; j < 16; ++j) { acc[j] = acc[j] * inv; ss += (acc[j][0] * acc[j][0] + acc[j][1] * acc[j][1]) + (acc[j][2] * acc[j][2] + acc[j][3] * acc[j][3]); }
;     ss += __shfl_xor(ss, 16); ss += __shfl_xor(ss, 32);
	v_lshl_add_u64 v[78:79], v[70:71], 4, s[34:35]
	s_lshl_b32 s24, s36, 2
	v_lshl_add_u64 v[78:79], v[78:79], 0, s[24:25]
	s_nop 0
	v_add_f32_e32 v93, v75, v76
	ds_bpermute_b32 v95, v115, v93
	v_lshlrev_b64 v[70:71], 12, v[70:71]
	s_mov_b32 s3, s25
	v_lshl_add_u64 v[70:71], s[26:27], 0, v[70:71]
	v_lshl_add_u64 v[70:71], v[70:71], 0, s[2:3]
	v_and_b32_e32 v66, 8, v117
	v_or_b32_e32 v75, s5, v117
	v_lshlrev_b32_e32 v66, 1, v66
	v_lshl_add_u64 v[72:73], v[72:73], 0, s[44:45]
	v_lshl_add_u64 v[70:71], v[70:71], 0, v[66:67]
	v_lshlrev_b32_e32 v66, 1, v75
	s_add_i32 s22, s22, s52
	s_cmpk_gt_i32 s22, 0xff
	s_waitcnt vmcnt(0)
	v_mov_b32_e32 v77, v246
	v_add_f32_e32 v80, v116, v77
	v_mul_f32_e32 v76, 0xbfb8aa3b, v80
	v_fma_f32 v77, v80, s76, -v76
	v_rndne_f32_e32 v78, v76
	v_fmac_f32_e32 v77, 0xb2a5705f, v80
	v_sub_f32_e32 v76, v76, v78
	v_add_f32_e32 v76, v76, v77
	v_cvt_i32_f32_e32 v81, v78
	v_exp_f32_e32 v82, v76
	s_waitcnt lgkmcnt(0)
	v_pk_add_f32 v[78:79], v[92:93], v[94:95]
	v_cmp_nlt_f32_e32 vcc, s77, v80
	v_fmac_f32_e32 v79, v78, v74
	v_ldexp_f32 v74, v82, v81
	v_cndmask_b32_e32 v74, 0, v74, vcc
	v_cmp_ngt_f32_e32 vcc, s78, v80
	v_lshl_add_u64 v[76:77], v[72:73], 0, v[66:67]
	global_load_dwordx2 v[80:81], v[76:77], off
	v_cndmask_b32_e32 v74, v97, v74, vcc
	v_max_f32_e64 v74, |v79|, v74
	v_div_scale_f32 v78, s[2:3], v74, v74, 1.0
	v_rcp_f32_e32 v79, v78
	v_div_scale_f32 v76, vcc, 1.0, v74, 1.0
	v_fma_f32 v77, -v78, v79, 1.0
	v_fmac_f32_e32 v79, v77, v79
	v_mul_f32_e32 v77, v76, v79
	v_fma_f32 v82, -v78, v77, v76
	v_fmac_f32_e32 v77, v82, v79
	v_fma_f32 v76, -v78, v77, v76
	v_div_fmas_f32 v76, v76, v79, v77
	v_div_fixup_f32 v74, v76, v74, 1.0
	v_pk_mul_f32 v[64:65], v[64:65], v[74:75] op_sel_hi:[1,0]
	v_pk_mul_f32 v[82:83], v[62:63], v[74:75] op_sel_hi:[1,0]
	v_pk_mul_f32 v[60:61], v[60:61], v[74:75] op_sel_hi:[1,0]
	v_pk_mul_f32 v[62:63], v[58:59], v[74:75] op_sel_hi:[1,0]
	v_pk_mul_f32 v[58:59], v[54:55], v[74:75] op_sel_hi:[1,0]
	v_pk_mul_f32 v[54:55], v[50:51], v[74:75] op_sel_hi:[1,0]
	v_pk_mul_f32 v[50:51], v[46:47], v[74:75] op_sel_hi:[1,0]
	v_pk_mul_f32 v[46:47], v[42:43], v[74:75] op_sel_hi:[1,0]
	v_pk_mul_f32 v[42:43], v[38:39], v[74:75] op_sel_hi:[1,0]
	v_pk_mul_f32 v[38:39], v[34:35], v[74:75] op_sel_hi:[1,0]
	v_pk_mul_f32 v[34:35], v[30:31], v[74:75] op_sel_hi:[1,0]
	v_pk_mul_f32 v[30:31], v[26:27], v[74:75] op_sel_hi:[1,0]
	v_pk_mul_f32 v[26:27], v[64:65], v[64:65]
	v_pk_mul_f32 v[76:77], v[82:83], v[82:83]
	v_pk_mul_f32 v[78:79], v[60:61], v[60:61]
	v_pk_mul_f32 v[84:85], v[62:63], v[62:63]
	v_pk_mul_f32 v[56:57], v[56:57], v[74:75] op_sel_hi:[1,0]
	v_pk_mov_b32 v[110:111], v[76:77], v[26:27] op_sel:[1,0]
	v_mov_b32_e32 v77, v27
	v_pk_mov_b32 v[26:27], v[84:85], v[78:79] op_sel:[1,0]
	v_mov_b32_e32 v85, v79
	v_mul_f32_e32 v86, v58, v58
	v_mul_f32_e32 v88, v56, v56
	v_pk_add_f32 v[76:77], v[110:111], v[76:77]
	v_pk_add_f32 v[26:27], v[26:27], v[84:85]
	v_pk_mul_f32 v[52:53], v[52:53], v[74:75] op_sel_hi:[1,0]
	v_pk_mul_f32 v[48:49], v[48:49], v[74:75] op_sel_hi:[1,0]
	v_pk_fma_f32 v[78:79], v[58:59], v[58:59], v[86:87] op_sel_hi:[1,1,0]
	v_pk_fma_f32 v[86:87], v[56:57], v[56:57], v[88:89] op_sel_hi:[1,1,0]
	v_pk_add_f32 v[76:77], v[76:77], v[76:77] op_sel_hi:[0,1]
	v_pk_add_f32 v[26:27], v[26:27], v[26:27] op_sel_hi:[0,1]
	v_pk_mul_f32 v[90:91], v[48:49], v[48:49]
	v_pk_mul_f32 v[92:93], v[50:51], v[50:51]
	v_mul_f32_e32 v78, v54, v54
	v_mul_f32_e32 v86, v55, v55
	v_mul_f32_e32 v76, v52, v52
	v_mul_f32_e32 v26, v53, v53
	v_pk_mul_f32 v[44:45], v[44:45], v[74:75] op_sel_hi:[1,0]
	v_pk_mov_b32 v[88:89], v[92:93], v[90:91] op_sel:[1,0]
	v_mov_b32_e32 v93, v91
	v_pk_add_f32 v[78:79], v[78:79], v[86:87]
	v_pk_add_f32 v[26:27], v[76:77], v[26:27]
	v_mul_f32_e32 v94, v46, v46
	v_mul_f32_e32 v100, v44, v44
	v_pk_add_f32 v[84:85], v[88:89], v[92:93]
	v_pk_add_f32 v[26:27], v[78:79], v[26:27]
	v_pk_mul_f32 v[40:41], v[40:41], v[74:75] op_sel_hi:[1,0]
	v_pk_mul_f32 v[36:37], v[36:37], v[74:75] op_sel_hi:[1,0]
	v_pk_fma_f32 v[90:91], v[46:47], v[46:47], v[94:95] op_sel_hi:[1,1,0]
	v_pk_fma_f32 v[94:95], v[44:45], v[44:45], v[100:101] op_sel_hi:[1,1,0]
	v_pk_add_f32 v[84:85], v[84:85], v[84:85] op_sel_hi:[0,1]
	v_pk_add_f32 v[26:27], v[26:27], v[26:27] op_sel_hi:[0,1]
	v_pk_mul_f32 v[102:103], v[36:37], v[36:37]
	v_pk_mul_f32 v[104:105], v[38:39], v[38:39]
	v_mul_f32_e32 v90, v42, v42
	v_mul_f32_e32 v94, v43, v43
	v_mul_f32_e32 v84, v40, v40
	v_mul_f32_e32 v26, v41, v41
	v_pk_mul_f32 v[32:33], v[32:33], v[74:75] op_sel_hi:[1,0]
	v_pk_mov_b32 v[100:101], v[104:105], v[102:103] op_sel:[1,0]
	v_mov_b32_e32 v105, v103
	v_pk_add_f32 v[86:87], v[90:91], v[94:95]
	v_pk_add_f32 v[26:27], v[84:85], v[26:27]
	v_mul_f32_e32 v106, v34, v34
	v_mul_f32_e32 v108, v32, v32
	v_pk_add_f32 v[88:89], v[100:101], v[104:105]
	v_pk_add_f32 v[26:27], v[86:87], v[26:27]
	v_pk_mul_f32 v[28:29], v[28:29], v[74:75] op_sel_hi:[1,0]
	v_pk_fma_f32 v[102:103], v[34:35], v[34:35], v[106:107] op_sel_hi:[1,1,0]
	v_pk_fma_f32 v[106:107], v[32:33], v[32:33], v[108:109] op_sel_hi:[1,1,0]
	v_pk_add_f32 v[88:89], v[88:89], v[88:89] op_sel_hi:[0,1]
	v_pk_add_f32 v[26:27], v[26:27], v[26:27] op_sel_hi:[0,1]
	v_mul_f32_e32 v102, v30, v30
	v_mul_f32_e32 v106, v31, v31
	v_mul_f32_e32 v88, v28, v28
	v_mul_f32_e32 v26, v29, v29
	v_pk_add_f32 v[76:77], v[102:103], v[106:107]
	v_pk_add_f32 v[26:27], v[88:89], v[26:27]
	v_pk_mul_f32 v[24:25], v[24:25], v[74:75] op_sel_hi:[1,0]
	v_lshlrev_b32_e32 v75, 2, v75
	v_pk_add_f32 v[26:27], v[76:77], v[26:27]
	global_load_dwordx4 v[76:79], v75, s[28:29]
	v_pk_add_f32 v[84:85], v[26:27], v[26:27] op_sel_hi:[0,1]
	v_pk_mul_f32 v[26:27], v[22:23], v[74:75] op_sel_hi:[1,0]
; __device__ __forceinline__ unsigned cvt_pk_bf16(float lo, float hi) { unsigned r; asm volatile("v_cvt_pk_bf16_f32 %0, %1, %2" : "=v"(r) : "v"(lo), "v"(hi)); return r; }
; __device__ __forceinline__ void mlstm_D(LAS unsigned char* lds, int c, int h, const bf16_t* Z, const float* gi, const float* bcum, const float* marr, const bf16_t* CST, const float* NST,
;                                         const float* hgain, bf16_t* YCAT) {
;     ...
;     for (int j = 0; j < 16; ++j) { acc[j] = acc[j] * inv; ss += (acc[j][0] * acc[j][0] + acc[j][1] * acc[j][1]) + (acc[j][2] * acc[j][2] + acc[j][3] * acc[j][3]); }
;     ss += __shfl_xor(ss, 16); ss += __shfl_xor(ss, 32);
;     const float rs = rsqrtf(ss * (1.0f / DH) + EPS);
; #pragma unroll
;     for (int j = 0; j < 16; j += 2) { u32x2 ab[2];
; #pragma unroll
;         for (int n = 0; n < 2; ++n) { const int col = h * DH + 16 * (j + n) + 4 * fq;
;             const f32x4 gn = *(const f32x4*)(hgain + col); const u32x2 ov = *(const u32x2*)(Z + trow * EVN + 4096 + col);
;             const float o0 = bf_lo(ov.x), o1 = bf_hi(ov.x), o2 = bf_lo(ov.y), o3 = bf_hi(ov.y);
;             const float y0 = acc[j + n][0] * rs * gn[0] / (1.0f + expf(-o0)), y1 = acc[j + n][1] * rs * gn[1] / (1.0f + expf(-o1));
;             const float y2 = acc[j + n][2] * rs * gn[2] / (1.0f + expf(-o2)), y3 = acc[j + n][3] * rs * gn[3] / (1.0f + expf(-o3));
;             ab[n].x = cvt_pk_bf16(y0, y1); ab[n].y = cvt_pk_bf16(y2, y3); }
	v_pk_mul_f32 v[22:23], v[24:25], v[24:25]
	v_pk_mul_f32 v[86:87], v[26:27], v[26:27]
	v_pk_mul_f32 v[20:21], v[20:21], v[74:75] op_sel_hi:[1,0]
	v_pk_mov_b32 v[88:89], v[86:87], v[22:23] op_sel:[1,0]
	v_mov_b32_e32 v87, v23
	v_pk_add_f32 v[22:23], v[88:89], v[86:87]
	v_pk_mul_f32 v[16:17], v[16:17], v[74:75] op_sel_hi:[1,0]
	v_pk_add_f32 v[86:87], v[22:23], v[22:23] op_sel_hi:[0,1]
	v_pk_mul_f32 v[22:23], v[18:19], v[74:75] op_sel_hi:[1,0]
	v_pk_mul_f32 v[14:15], v[14:15], v[74:75] op_sel_hi:[1,0]
	v_mul_f32_e32 v18, v22, v22
	v_pk_fma_f32 v[18:19], v[22:23], v[22:23], v[18:19] op_sel_hi:[1,1,0]
	v_mul_f32_e32 v86, v16, v16
	v_mul_f32_e32 v18, v20, v20
	v_pk_fma_f32 v[88:89], v[20:21], v[20:21], v[18:19] op_sel_hi:[1,1,0]
	v_mul_f32_e32 v18, v14, v14
	v_mul_f32_e32 v88, v15, v15
	v_mul_f32_e32 v84, v17, v17
	v_pk_add_f32 v[18:19], v[18:19], v[88:89]
	v_pk_add_f32 v[84:85], v[86:87], v[84:85]
	v_pk_mul_f32 v[12:13], v[12:13], v[74:75] op_sel_hi:[1,0]
	v_pk_add_f32 v[18:19], v[18:19], v[84:85]
	v_pk_mul_f32 v[10:11], v[10:11], v[74:75] op_sel_hi:[1,0]
	v_pk_add_f32 v[18:19], v[18:19], v[18:19] op_sel_hi:[0,1]
	v_pk_mul_f32 v[84:85], v[12:13], v[12:13]
	v_pk_mul_f32 v[86:87], v[10:11], v[10:11]
	v_pk_mul_f32 v[6:7], v[6:7], v[74:75] op_sel_hi:[1,0]
	v_pk_mov_b32 v[88:89], v[86:87], v[84:85] op_sel:[1,0]
	v_mov_b32_e32 v87, v85
	v_pk_mul_f32 v[8:9], v[8:9], v[74:75] op_sel_hi:[1,0]
	v_mul_f32_e32 v18, v6, v6
	v_pk_add_f32 v[84:85], v[88:89], v[86:87]
	v_pk_fma_f32 v[86:87], v[6:7], v[6:7], v[18:19] op_sel_hi:[1,1,0]
	v_mul_f32_e32 v18, v8, v8
	v_pk_add_f32 v[84:85], v[84:85], v[84:85] op_sel_hi:[0,1]
	v_pk_fma_f32 v[88:89], v[8:9], v[8:9], v[18:19] op_sel_hi:[1,1,0]
	v_pk_mul_f32 v[4:5], v[4:5], v[74:75] op_sel_hi:[1,0]
	v_pk_mul_f32 v[2:3], v[2:3], v[74:75] op_sel_hi:[1,0]
	v_mul_f32_e32 v84, v4, v4
	v_mul_f32_e32 v86, v2, v2
	v_mul_f32_e32 v88, v3, v3
	v_mul_f32_e32 v18, v5, v5
	v_pk_add_f32 v[86:87], v[86:87], v[88:89]
	v_pk_add_f32 v[18:19], v[84:85], v[18:19]
	s_waitcnt vmcnt(1)
	v_lshlrev_b32_e32 v84, 16, v80
	v_pk_add_f32 v[18:19], v[86:87], v[18:19]
	v_mul_f32_e32 v74, 0xbfb8aa3b, v84
	v_add_f32_e32 v18, v18, v19
	ds_bpermute_b32 v19, v98, v18
	v_fma_f32 v85, v84, s76, -v74
	v_rndne_f32_e32 v86, v74
	v_fmac_f32_e32 v85, 0xb2a5705f, v84
	v_sub_f32_e32 v74, v74, v86
	s_waitcnt lgkmcnt(0)
	v_add_f32_e32 v18, v18, v19
	ds_bpermute_b32 v19, v115, v18
	v_add_f32_e32 v74, v74, v85
	v_exp_f32_e32 v85, v74
	v_cvt_i32_f32_e32 v86, v86
	v_and_b32_e32 v80, 0xffff0000, v80
	s_waitcnt lgkmcnt(0)
	v_add_f32_e32 v18, v18, v19
	v_fmamk_f32 v18, v18, 0x3b800000, v1
	v_mul_f32_e32 v19, 0x4b800000, v18
	v_cmp_gt_f32_e32 vcc, s79, v18
	s_nop 1
	v_cndmask_b32_e32 v18, v18, v19, vcc
	v_rsq_f32_e32 v18, v18
	s_nop 0
	v_mul_f32_e32 v19, 0x45800000, v18
	v_cndmask_b32_e32 v74, v18, v19, vcc
	v_ldexp_f32 v19, v85, v86
	v_cmp_nlt_f32_e32 vcc, s77, v84
	v_mul_f32_e32 v18, v82, v74
	v_mul_f32_e32 v83, v83, v74
	v_cndmask_b32_e32 v19, 0, v19, vcc
	v_cmp_ngt_f32_e32 vcc, s78, v84
	s_waitcnt vmcnt(0)
	v_mul_f32_e32 v18, v76, v18
	v_mul_f32_e32 v77, v77, v83
	v_cndmask_b32_e32 v19, v97, v19, vcc
	v_add_f32_e32 v19, 1.0, v19
	v_div_scale_f32 v76, s[2:3], v19, v19, v18
	v_rcp_f32_e32 v82, v76
	v_cmp_nlt_f32_e64 s[2:3], s77, v80
	v_lshlrev_b32_e32 v84, 16, v81
	v_mul_f32_e32 v64, v64, v74
	v_fma_f32 v85, -v76, v82, 1.0
	v_fmac_f32_e32 v82, v85, v82
	v_div_scale_f32 v85, vcc, v18, v19, v18
	v_mul_f32_e32 v86, v85, v82
	v_fma_f32 v87, -v76, v86, v85
	v_fmac_f32_e32 v86, v87, v82
	v_mul_f32_e32 v87, 0xbfb8aa3b, v80
	v_fma_f32 v88, v80, s76, -v87
	v_rndne_f32_e32 v89, v87
	v_fmac_f32_e32 v88, 0xb2a5705f, v80
	v_sub_f32_e32 v87, v87, v89
	v_add_f32_e32 v87, v87, v88
	v_exp_f32_e32 v87, v87
	v_cvt_i32_f32_e32 v88, v89
	v_fma_f32 v76, -v76, v86, v85
	v_div_fmas_f32 v76, v76, v82, v86
	v_div_fixup_f32 v18, v76, v19, v18
	v_ldexp_f32 v83, v87, v88
	v_cndmask_b32_e64 v83, 0, v83, s[2:3]
	v_cmp_ngt_f32_e64 s[2:3], s78, v80
	v_mul_f32_e32 v64, v78, v64
	v_and_b32_e32 v81, 0xffff0000, v81
	v_cndmask_b32_e64 v80, v97, v83, s[2:3]
	v_add_f32_e32 v80, 1.0, v80
	v_div_scale_f32 v83, s[2:3], v80, v80, v77
	v_rcp_f32_e32 v85, v83
	v_cmp_nlt_f32_e64 s[2:3], s77, v84
	v_mul_f32_e32 v65, v65, v74
	v_mul_f32_e32 v65, v79, v65
	v_fma_f32 v19, -v83, v85, 1.0
	v_fmac_f32_e32 v85, v19, v85
	v_div_scale_f32 v19, vcc, v77, v80, v77
	v_mul_f32_e32 v76, v19, v85
	v_fma_f32 v82, -v83, v76, v19
	v_fmac_f32_e32 v76, v82, v85
	v_mul_f32_e32 v82, 0xbfb8aa3b, v84
	v_fma_f32 v86, v84, s76, -v82
	v_rndne_f32_e32 v87, v82
	v_fmac_f32_e32 v86, 0xb2a5705f, v84
	v_sub_f32_e32 v82, v82, v87
	v_add_f32_e32 v82, v82, v86
	v_exp_f32_e32 v82, v82
	v_cvt_i32_f32_e32 v86, v87
	v_fma_f32 v19, -v83, v76, v19
	v_div_fmas_f32 v19, v19, v85, v76
	v_div_fixup_f32 v19, v19, v80, v77
	v_ldexp_f32 v78, v82, v86
	v_cndmask_b32_e64 v78, 0, v78, s[2:3]
	v_cmp_ngt_f32_e64 s[2:3], s78, v84
	v_mul_f32_e32 v62, v62, v74
	v_mul_f32_e32 v63, v63, v74
	v_cndmask_b32_e64 v78, v97, v78, s[2:3]
	v_add_f32_e32 v78, 1.0, v78
	v_div_scale_f32 v82, s[2:3], v78, v78, v64
	v_rcp_f32_e32 v83, v82
	v_cmp_nlt_f32_e64 s[2:3], s77, v81
	v_mul_f32_e32 v60, v60, v74
	v_mul_f32_e32 v61, v61, v74
	v_fma_f32 v76, -v82, v83, 1.0
	v_fmac_f32_e32 v83, v76, v83
	v_div_scale_f32 v76, vcc, v64, v78, v64
	v_mul_f32_e32 v77, v76, v83
	v_fma_f32 v80, -v82, v77, v76
	v_fmac_f32_e32 v77, v80, v83
	v_mul_f32_e32 v80, 0xbfb8aa3b, v81
	v_fma_f32 v84, v81, s76, -v80
	v_rndne_f32_e32 v85, v80
	v_fmac_f32_e32 v84, 0xb2a5705f, v81
	v_sub_f32_e32 v80, v80, v85
	v_add_f32_e32 v80, v80, v84
	v_exp_f32_e32 v80, v80
	v_cvt_i32_f32_e32 v84, v85
	v_fma_f32 v76, -v82, v77, v76
; __device__ __forceinline__ unsigned cvt_pk_bf16(float lo, float hi) { unsigned r; asm volatile("v_cvt_pk_bf16_f32 %0, %1, %2" : "=v"(r) : "v"(lo), "v"(hi)); return r; }
; __device__ __forceinline__ void mlstm_D(LAS unsigned char* lds, int c, int h, const bf16_t* Z, const float* gi, const float* bcum, const float* marr, const bf16_t* CST, const float* NST,
;                                         const float* hgain, bf16_t* YCAT) {
;     ...
;     const float rs = rsqrtf(ss * (1.0f / DH) + EPS);
; #pragma unroll
;     for (int j = 0; j < 16; j += 2) { u32x2 ab[2];
; #pragma unroll
;         for (int n = 0; n < 2; ++n) { const int col = h * DH + 16 * (j + n) + 4 * fq;
;             const f32x4 gn = *(const f32x4*)(hgain + col); const u32x2 ov = *(const u32x2*)(Z + trow * EVN + 4096 + col);
;             const float o0 = bf_lo(ov.x), o1 = bf_hi(ov.x), o2 = bf_lo(ov.y), o3 = bf_hi(ov.y);
;             const float y0 = acc[j + n][0] * rs * gn[0] / (1.0f + expf(-o0)), y1 = acc[j + n][1] * rs * gn[1] / (1.0f + expf(-o1));
;             const float y2 = acc[j + n][2] * rs * gn[2] / (1.0f + expf(-o2)), y3 = acc[j + n][3] * rs * gn[3] / (1.0f + expf(-o3));
;             ab[n].x = cvt_pk_bf16(y0, y1); ab[n].y = cvt_pk_bf16(y2, y3); }
	v_div_fmas_f32 v76, v76, v83, v77
	v_div_fixup_f32 v64, v76, v78, v64
	v_ldexp_f32 v79, v80, v84
	v_cndmask_b32_e64 v79, 0, v79, s[2:3]
	v_cmp_ngt_f32_e64 s[2:3], s78, v81
	v_mul_f32_e32 v58, v58, v74
	v_mul_f32_e32 v59, v59, v74
	v_cndmask_b32_e64 v79, v97, v79, s[2:3]
	v_add_f32_e32 v79, 1.0, v79
	v_div_scale_f32 v80, s[2:3], v79, v79, v65
	v_rcp_f32_e32 v81, v80
	v_mul_f32_e32 v56, v56, v74
	v_mul_f32_e32 v57, v57, v74
	v_mul_f32_e32 v54, v54, v74
	v_fma_f32 v76, -v80, v81, 1.0
	v_fmac_f32_e32 v81, v76, v81
	v_div_scale_f32 v76, vcc, v65, v79, v65
	v_mul_f32_e32 v77, v76, v81
	v_fma_f32 v78, -v80, v77, v76
	v_fmac_f32_e32 v77, v78, v81
	v_fma_f32 v76, -v80, v77, v76
	v_cvt_pk_bf16_f32 v80, v18, v19
	v_or_b32_e32 v18, 32, v66
	v_mov_b32_e32 v19, v67
	v_div_fmas_f32 v76, v76, v81, v77
	v_lshl_add_u64 v[18:19], v[72:73], 0, v[18:19]
	v_div_fixup_f32 v65, v76, v79, v65
	v_cvt_pk_bf16_f32 v64, v64, v65
	global_load_dwordx2 v[18:19], v[18:19], off
	s_nop 0
	global_load_dwordx4 v[76:79], v75, s[28:29] offset:64
	v_mul_f32_e32 v55, v55, v74
	v_mul_f32_e32 v52, v52, v74
	v_mul_f32_e32 v53, v53, v74
	v_mul_f32_e32 v50, v50, v74
	v_mul_f32_e32 v51, v51, v74
	v_mul_f32_e32 v48, v48, v74
	v_mul_f32_e32 v49, v49, v74
	v_mul_f32_e32 v46, v46, v74
	v_mul_f32_e32 v47, v47, v74
	v_mul_f32_e32 v44, v44, v74
	v_mul_f32_e32 v45, v45, v74
	v_mul_f32_e32 v42, v42, v74
	v_mul_f32_e32 v43, v43, v74
	v_mul_f32_e32 v40, v40, v74
	v_mul_f32_e32 v41, v41, v74
	v_mul_f32_e32 v38, v38, v74
	v_mul_f32_e32 v39, v39, v74
	v_mul_f32_e32 v36, v36, v74
	v_mul_f32_e32 v37, v37, v74
	v_mul_f32_e32 v34, v34, v74
	v_mul_f32_e32 v35, v35, v74
	v_mul_f32_e32 v32, v32, v74
	v_mul_f32_e32 v33, v33, v74
	v_mul_f32_e32 v30, v30, v74
	v_mul_f32_e32 v31, v31, v74
	v_mul_f32_e32 v28, v28, v74
	v_mul_f32_e32 v29, v29, v74
	v_mul_f32_e32 v26, v26, v74
	v_mul_f32_e32 v27, v27, v74
	v_mul_f32_e32 v24, v24, v74
	v_mul_f32_e32 v25, v25, v74
	v_mul_f32_e32 v22, v22, v74
	v_mul_f32_e32 v23, v23, v74
	v_mul_f32_e32 v20, v20, v74
	v_mul_f32_e32 v21, v21, v74
	v_mul_f32_e32 v14, v14, v74
	v_mul_f32_e32 v15, v15, v74
	v_mul_f32_e32 v16, v16, v74
	v_mul_f32_e32 v17, v17, v74
	v_mul_f32_e32 v10, v10, v74
	v_mul_f32_e32 v11, v11, v74
	v_mul_f32_e32 v12, v12, v74
	v_mul_f32_e32 v13, v13, v74
	v_mul_f32_e32 v6, v6, v74
	v_mul_f32_e32 v7, v7, v74
	v_mul_f32_e32 v8, v8, v74
	v_mul_f32_e32 v9, v9, v74
	v_mul_f32_e32 v2, v2, v74
	v_mul_f32_e32 v3, v3, v74
	v_mul_f32_e32 v4, v4, v74
	v_mul_f32_e32 v5, v5, v74
	s_waitcnt vmcnt(1)
	v_lshlrev_b32_e32 v65, 16, v18
	v_mul_f32_e32 v81, 0xbfb8aa3b, v65
	v_fma_f32 v82, v65, s76, -v81
	v_rndne_f32_e32 v83, v81
	v_fmac_f32_e32 v82, 0xb2a5705f, v65
	v_sub_f32_e32 v81, v81, v83
	v_add_f32_e32 v81, v81, v82
	v_exp_f32_e32 v81, v81
	v_cvt_i32_f32_e32 v82, v83
	s_waitcnt vmcnt(0)
	v_mul_f32_e32 v62, v76, v62
	v_cmp_nlt_f32_e32 vcc, s77, v65
	v_and_b32_e32 v18, 0xffff0000, v18
	v_ldexp_f32 v76, v81, v82
	v_cndmask_b32_e32 v76, 0, v76, vcc
	v_cmp_ngt_f32_e32 vcc, s78, v65
	v_mul_f32_e32 v63, v77, v63
	v_lshlrev_b32_e32 v82, 16, v19
	v_cndmask_b32_e32 v65, v97, v76, vcc
	v_add_f32_e32 v65, 1.0, v65
	v_div_scale_f32 v76, s[2:3], v65, v65, v62
	v_rcp_f32_e32 v81, v76
	v_cmp_nlt_f32_e64 s[2:3], s77, v18
	v_mul_f32_e32 v60, v78, v60
	v_and_b32_e32 v19, 0xffff0000, v19
	v_fma_f32 v84, -v76, v81, 1.0
	v_fmac_f32_e32 v81, v84, v81
	v_div_scale_f32 v84, vcc, v62, v65, v62
	v_mul_f32_e32 v85, v84, v81
	v_fma_f32 v86, -v76, v85, v84
	v_fmac_f32_e32 v85, v86, v81
	v_mul_f32_e32 v86, 0xbfb8aa3b, v18
	v_fma_f32 v87, v18, s76, -v86
	v_rndne_f32_e32 v88, v86
	v_fmac_f32_e32 v87, 0xb2a5705f, v18
	v_sub_f32_e32 v86, v86, v88
	v_add_f32_e32 v86, v86, v87
	v_exp_f32_e32 v86, v86
	v_cvt_i32_f32_e32 v87, v88
	v_fma_f32 v76, -v76, v85, v84
	v_div_fmas_f32 v76, v76, v81, v85
	v_div_fixup_f32 v62, v76, v65, v62
	v_ldexp_f32 v77, v86, v87
	v_cndmask_b32_e64 v77, 0, v77, s[2:3]
	v_cmp_ngt_f32_e64 s[2:3], s78, v18
	v_mul_f32_e32 v61, v79, v61
	v_and_b32_e32 v83, 16, v99
	v_cndmask_b32_e64 v18, v97, v77, s[2:3]
	v_add_f32_e32 v18, 1.0, v18
	v_div_scale_f32 v77, s[2:3], v18, v18, v63
	v_rcp_f32_e32 v84, v77
	v_cmp_nlt_f32_e64 s[2:3], s77, v82
	v_fma_f32 v65, -v77, v84, 1.0
	v_fmac_f32_e32 v84, v65, v84
	v_div_scale_f32 v65, vcc, v63, v18, v63
	v_mul_f32_e32 v76, v65, v84
	v_fma_f32 v81, -v77, v76, v65
	v_fmac_f32_e32 v76, v81, v84
	v_mul_f32_e32 v81, 0xbfb8aa3b, v82
	v_fma_f32 v85, v82, s76, -v81
	v_rndne_f32_e32 v86, v81
	v_fmac_f32_e32 v85, 0xb2a5705f, v82
	v_sub_f32_e32 v81, v81, v86
	v_add_f32_e32 v81, v81, v85
	v_exp_f32_e32 v81, v81
	v_cvt_i32_f32_e32 v85, v86
	v_fma_f32 v65, -v77, v76, v65
	v_div_fmas_f32 v65, v65, v84, v76
	v_div_fixup_f32 v18, v65, v18, v63
	v_ldexp_f32 v77, v81, v85
	v_cndmask_b32_e64 v77, 0, v77, s[2:3]
	v_cmp_ngt_f32_e64 s[2:3], s78, v82
	v_cvt_pk_bf16_f32 v18, v62, v18
	s_nop 1
	v_cndmask_b32_e64 v77, v97, v77, s[2:3]
	v_add_f32_e32 v77, 1.0, v77
	v_div_scale_f32 v78, s[2:3], v77, v77, v60
	v_rcp_f32_e32 v81, v78
	v_cmp_nlt_f32_e64 s[2:3], s77, v19
	v_fma_f32 v63, -v78, v81, 1.0
	v_fmac_f32_e32 v81, v63, v81
	v_div_scale_f32 v63, vcc, v60, v77, v60
	v_mul_f32_e32 v65, v63, v81
	v_fma_f32 v76, -v78, v65, v63
	v_fmac_f32_e32 v65, v76, v81
	v_mul_f32_e32 v76, 0xbfb8aa3b, v19
	v_fma_f32 v82, v19, s76, -v76
	v_rndne_f32_e32 v84, v76
	v_fmac_f32_e32 v82, 0xb2a5705f, v19
	v_sub_f32_e32 v76, v76, v84
	v_add_f32_e32 v76, v76, v82
	v_exp_f32_e32 v76, v76
	v_cvt_i32_f32_e32 v82, v84
	v_fma_f32 v63, -v78, v65, v63
	v_div_fmas_f32 v63, v63, v81, v65
	v_div_fixup_f32 v60, v63, v77, v60
	v_ldexp_f32 v76, v76, v82
	v_cndmask_b32_e64 v76, 0, v76, s[2:3]
	v_cmp_ngt_f32_e64 s[2:3], s78, v19
	s_nop 1
	v_cndmask_b32_e64 v19, v97, v76, s[2:3]
	v_add_f32_e32 v19, 1.0, v19
	v_div_scale_f32 v76, s[2:3], v19, v19, v61
	v_rcp_f32_e32 v78, v76
	v_cmp_eq_u32_e64 s[2:3], 0, v83
	v_fma_f32 v63, -v76, v78, 1.0
	v_fmac_f32_e32 v78, v63, v78
	v_div_scale_f32 v63, vcc, v61, v19, v61
	v_mul_f32_e32 v65, v63, v78
	v_fma_f32 v77, -v76, v65, v63
	v_fmac_f32_e32 v65, v77, v78
	v_fma_f32 v63, -v76, v65, v63
	v_div_fmas_f32 v63, v63, v78, v65
	v_div_fixup_f32 v19, v63, v19, v61
	v_cvt_pk_bf16_f32 v19, v60, v19
	v_cndmask_b32_e64 v61, v80, v18, s[2:3]
	v_cndmask_b32_e64 v60, v64, v19, s[2:3]
	ds_bpermute_b32 v61, v98, v61
	ds_bpermute_b32 v65, v98, v60
	s_waitcnt lgkmcnt(1)
; __device__ __forceinline__ unsigned cvt_pk_bf16(float lo, float hi) { unsigned r; asm volatile("v_cvt_pk_bf16_f32 %0, %1, %2" : "=v"(r) : "v"(lo), "v"(hi)); return r; }
; __device__ __forceinline__ void mlstm_D(LAS unsigned char* lds, int c, int h, const bf16_t* Z, const float* gi, const float* bcum, const float* marr, const bf16_t* CST, const float* NST,
;                                         const float* hgain, bf16_t* YCAT) {
;     ...
;         for (int n = 0; n < 2; ++n) { const int col = h * DH + 16 * (j + n) + 4 * fq;
;             const f32x4 gn = *(const f32x4*)(hgain + col); const u32x2 ov = *(const u32x2*)(Z + trow * EVN + 4096 + col);
;             const float o0 = bf_lo(ov.x), o1 = bf_hi(ov.x), o2 = bf_lo(ov.y), o3 = bf_hi(ov.y);
;             const float y0 = acc[j + n][0] * rs * gn[0] / (1.0f + expf(-o0)), y1 = acc[j + n][1] * rs * gn[1] / (1.0f + expf(-o1));
;             const float y2 = acc[j + n][2] * rs * gn[2] / (1.0f + expf(-o2)), y3 = acc[j + n][3] * rs * gn[3] / (1.0f + expf(-o3));
;             ab[n].x = cvt_pk_bf16(y0, y1); ab[n].y = cvt_pk_bf16(y2, y3); }
;         const bool odd = fq & 1; const u32x2 give = odd ? ab[0] : ab[1];
;         u32x2 got; got.x = (unsigned)__shfl_xor((int)give.x, 16); got.y = (unsigned)__shfl_xor((int)give.y, 16);
;         u32x4 w; if (odd) { w.x = got.x; w.y = got.y; w.z = ab[1].x; w.w = ab[1].y; } else { w.x = ab[0].x; w.y = ab[0].y; w.z = got.x; w.w = got.y; }
;         *(u32x4*)(YCAT + trow * D + 1024 + h * DH + 16 * (j + (odd ? 1 : 0)) + 4 * (fq & 2)) = w; if ((j & 3) == 2) asm volatile("" ::: "memory"); }
	v_cndmask_b32_e64 v62, v18, v61, s[2:3]
	s_waitcnt lgkmcnt(0)
	v_cndmask_b32_e64 v63, v19, v65, s[2:3]
	v_lshlrev_b32_e32 v18, 1, v83
	v_mov_b32_e32 v19, v67
	v_lshl_add_u64 v[18:19], v[70:71], 0, v[18:19]
	v_cndmask_b32_e64 v60, v61, v80, s[2:3]
	v_cndmask_b32_e64 v61, v65, v64, s[2:3]
	v_add_co_u32_e32 v64, vcc, 4.0, v18
	s_nop 1
	v_addc_co_u32_e32 v65, vcc, 0, v19, vcc
	global_store_dwordx4 v[64:65], v[60:63], off offset:2048
	v_lshl_add_u64 v[18:19], v[18:19], 0, s[46:47]
	s_nop 0
	v_or_b32_e32 v60, 64, v66
	v_mov_b32_e32 v61, v67
	v_lshl_add_u64 v[60:61], v[72:73], 0, v[60:61]
	global_load_dwordx2 v[64:65], v[60:61], off
	s_nop 0
	global_load_dwordx4 v[60:63], v75, s[28:29] offset:128
	s_waitcnt vmcnt(1)
	v_lshlrev_b32_e32 v70, 16, v64
	v_mul_f32_e32 v71, 0xbfb8aa3b, v70
	v_fma_f32 v76, v70, s76, -v71
	v_rndne_f32_e32 v77, v71
	v_fmac_f32_e32 v76, 0xb2a5705f, v70
	v_sub_f32_e32 v71, v71, v77
	v_add_f32_e32 v71, v71, v76
	v_exp_f32_e32 v71, v71
	v_cvt_i32_f32_e32 v76, v77
	s_waitcnt vmcnt(0)
	v_mul_f32_e32 v58, v60, v58
	v_cmp_nlt_f32_e32 vcc, s77, v70
	v_and_b32_e32 v64, 0xffff0000, v64
	v_ldexp_f32 v60, v71, v76
	v_cndmask_b32_e32 v60, 0, v60, vcc
	v_cmp_ngt_f32_e32 vcc, s78, v70
	v_mul_f32_e32 v59, v61, v59
	v_lshlrev_b32_e32 v76, 16, v65
	v_cndmask_b32_e32 v60, v97, v60, vcc
	v_add_f32_e32 v60, 1.0, v60
	v_div_scale_f32 v70, s[4:5], v60, v60, v58
	v_rcp_f32_e32 v71, v70
	v_cmp_nlt_f32_e64 s[4:5], s77, v64
	v_mul_f32_e32 v56, v62, v56
	v_and_b32_e32 v65, 0xffff0000, v65
	v_fma_f32 v77, -v70, v71, 1.0
	v_fmac_f32_e32 v71, v77, v71
	v_div_scale_f32 v77, vcc, v58, v60, v58
	v_mul_f32_e32 v78, v77, v71
	v_fma_f32 v79, -v70, v78, v77
	v_fmac_f32_e32 v78, v79, v71
	v_mul_f32_e32 v79, 0xbfb8aa3b, v64
	v_fma_f32 v80, v64, s76, -v79
	v_rndne_f32_e32 v81, v79
	v_fmac_f32_e32 v80, 0xb2a5705f, v64
	v_sub_f32_e32 v79, v79, v81
	v_add_f32_e32 v79, v79, v80
	v_exp_f32_e32 v79, v79
	v_cvt_i32_f32_e32 v80, v81
	v_fma_f32 v70, -v70, v78, v77
	v_div_fmas_f32 v70, v70, v71, v78
	v_div_fixup_f32 v58, v70, v60, v58
	v_ldexp_f32 v61, v79, v80
	v_cndmask_b32_e64 v61, 0, v61, s[4:5]
	v_cmp_ngt_f32_e64 s[4:5], s78, v64
	v_mul_f32_e32 v57, v63, v57
	s_nop 0
	v_cndmask_b32_e64 v61, v97, v61, s[4:5]
	v_add_f32_e32 v61, 1.0, v61
	v_div_scale_f32 v64, s[4:5], v61, v61, v59
	v_rcp_f32_e32 v77, v64
	v_cmp_nlt_f32_e64 s[4:5], s77, v76
	v_fma_f32 v60, -v64, v77, 1.0
	v_fmac_f32_e32 v77, v60, v77
	v_div_scale_f32 v60, vcc, v59, v61, v59
	v_mul_f32_e32 v70, v60, v77
	v_fma_f32 v71, -v64, v70, v60
	v_fmac_f32_e32 v70, v71, v77
	v_mul_f32_e32 v71, 0xbfb8aa3b, v76
	v_fma_f32 v78, v76, s76, -v71
	v_rndne_f32_e32 v79, v71
	v_fmac_f32_e32 v78, 0xb2a5705f, v76
	v_sub_f32_e32 v71, v71, v79
	v_add_f32_e32 v71, v71, v78
	v_exp_f32_e32 v71, v71
	v_cvt_i32_f32_e32 v78, v79
	v_fma_f32 v60, -v64, v70, v60
	v_div_fmas_f32 v60, v60, v77, v70
	v_div_fixup_f32 v59, v60, v61, v59
	v_ldexp_f32 v62, v71, v78
	v_cndmask_b32_e64 v62, 0, v62, s[4:5]
	v_cmp_ngt_f32_e64 s[4:5], s78, v76
	s_nop 1
	v_cndmask_b32_e64 v62, v97, v62, s[4:5]
	v_add_f32_e32 v62, 1.0, v62
	v_div_scale_f32 v64, s[4:5], v62, v62, v56
	v_rcp_f32_e32 v71, v64
	v_cmp_nlt_f32_e64 s[4:5], s77, v65
	v_fma_f32 v60, -v64, v71, 1.0
	v_fmac_f32_e32 v71, v60, v71
	v_div_scale_f32 v60, vcc, v56, v62, v56
	v_mul_f32_e32 v61, v60, v71
	v_fma_f32 v70, -v64, v61, v60
	v_fmac_f32_e32 v61, v70, v71
	v_mul_f32_e32 v70, 0xbfb8aa3b, v65
	v_fma_f32 v76, v65, s76, -v70
	v_rndne_f32_e32 v77, v70
	v_fmac_f32_e32 v76, 0xb2a5705f, v65
	v_sub_f32_e32 v70, v70, v77
	v_add_f32_e32 v70, v70, v76
	v_exp_f32_e32 v70, v70
	v_cvt_i32_f32_e32 v76, v77
	v_fma_f32 v60, -v64, v61, v60
	v_div_fmas_f32 v60, v60, v71, v61
	v_div_fixup_f32 v56, v60, v62, v56
	v_ldexp_f32 v63, v70, v76
	v_cndmask_b32_e64 v63, 0, v63, s[4:5]
	v_cmp_ngt_f32_e64 s[4:5], s78, v65
	s_nop 1
	v_cndmask_b32_e64 v63, v97, v63, s[4:5]
	v_add_f32_e32 v63, 1.0, v63
	v_div_scale_f32 v64, s[4:5], v63, v63, v57
	v_rcp_f32_e32 v65, v64
	s_nop 0
	v_fma_f32 v60, -v64, v65, 1.0
	v_fmac_f32_e32 v65, v60, v65
	v_div_scale_f32 v60, vcc, v57, v63, v57
	v_mul_f32_e32 v61, v60, v65
	v_fma_f32 v62, -v64, v61, v60
	v_fmac_f32_e32 v61, v62, v65
	v_fma_f32 v60, -v64, v61, v60
	v_div_fmas_f32 v60, v60, v65, v61
	v_div_fixup_f32 v57, v60, v63, v57
	v_cvt_pk_bf16_f32 v62, v58, v59
	v_cvt_pk_bf16_f32 v63, v56, v57
	v_or_b32_e32 v56, 0x60, v66
	v_mov_b32_e32 v57, v67
	v_lshl_add_u64 v[56:57], v[72:73], 0, v[56:57]
	global_load_dwordx2 v[60:61], v[56:57], off
	s_nop 0
	global_load_dwordx4 v[56:59], v75, s[28:29] offset:192
	s_waitcnt vmcnt(1)
	v_lshlrev_b32_e32 v64, 16, v60
	v_mul_f32_e32 v65, 0xbfb8aa3b, v64
	v_fma_f32 v70, v64, s76, -v65
	v_rndne_f32_e32 v71, v65
	v_fmac_f32_e32 v70, 0xb2a5705f, v64
	v_sub_f32_e32 v65, v65, v71
	v_add_f32_e32 v65, v65, v70
	v_exp_f32_e32 v65, v65
	v_cvt_i32_f32_e32 v70, v71
	s_waitcnt vmcnt(0)
; __device__ __forceinline__ unsigned cvt_pk_bf16(float lo, float hi) { unsigned r; asm volatile("v_cvt_pk_bf16_f32 %0, %1, %2" : "=v"(r) : "v"(lo), "v"(hi)); return r; }
; __device__ __forceinline__ void mlstm_D(LAS unsigned char* lds, int c, int h, const bf16_t* Z, const float* gi, const float* bcum, const float* marr, const bf16_t* CST, const float* NST,
;                                         const float* hgain, bf16_t* YCAT) {
;     ...
; #pragma unroll
;     for (int j = 0; j < 16; j += 2) { u32x2 ab[2];
; #pragma unroll
;         for (int n = 0; n < 2; ++n) { const int col = h * DH + 16 * (j + n) + 4 * fq;
;             const f32x4 gn = *(const f32x4*)(hgain + col); const u32x2 ov = *(const u32x2*)(Z + trow * EVN + 4096 + col);
;             const float o0 = bf_lo(ov.x), o1 = bf_hi(ov.x), o2 = bf_lo(ov.y), o3 = bf_hi(ov.y);
;             const float y0 = acc[j + n][0] * rs * gn[0] / (1.0f + expf(-o0)), y1 = acc[j + n][1] * rs * gn[1] / (1.0f + expf(-o1));
;             const float y2 = acc[j + n][2] * rs * gn[2] / (1.0f + expf(-o2)), y3 = acc[j + n][3] * rs * gn[3] / (1.0f + expf(-o3));
;             ab[n].x = cvt_pk_bf16(y0, y1); ab[n].y = cvt_pk_bf16(y2, y3); }
;         const bool odd = fq & 1; const u32x2 give = odd ? ab[0] : ab[1];
;         u32x2 got; got.x = (unsigned)__shfl_xor((int)give.x, 16); got.y = (unsigned)__shfl_xor((int)give.y, 16);
;         u32x4 w; if (odd) { w.x = got.x; w.y = got.y; w.z = ab[1].x; w.w = ab[1].y; } else { w.x = ab[0].x; w.y = ab[0].y; w.z = got.x; w.w = got.y; }
;         *(u32x4*)(YCAT + trow * D + 1024 + h * DH + 16 * (j + (odd ? 1 : 0)) + 4 * (fq & 2)) = w; if ((j & 3) == 2) asm volatile("" ::: "memory"); }
	v_mul_f32_e32 v54, v56, v54
	v_cmp_nlt_f32_e32 vcc, s77, v64
	v_and_b32_e32 v60, 0xffff0000, v60
	v_ldexp_f32 v56, v65, v70
	v_cndmask_b32_e32 v56, 0, v56, vcc
	v_cmp_ngt_f32_e32 vcc, s78, v64
	v_mul_f32_e32 v55, v57, v55
	v_lshlrev_b32_e32 v70, 16, v61
	v_cndmask_b32_e32 v56, v97, v56, vcc
	v_add_f32_e32 v56, 1.0, v56
	v_div_scale_f32 v64, s[4:5], v56, v56, v54
	v_rcp_f32_e32 v65, v64
	v_cmp_nlt_f32_e64 s[4:5], s77, v60
	v_mul_f32_e32 v52, v58, v52
	v_and_b32_e32 v61, 0xffff0000, v61
	v_fma_f32 v71, -v64, v65, 1.0
	v_fmac_f32_e32 v65, v71, v65
	v_div_scale_f32 v71, vcc, v54, v56, v54
	v_mul_f32_e32 v76, v71, v65
	v_fma_f32 v77, -v64, v76, v71
	v_fmac_f32_e32 v76, v77, v65
	v_mul_f32_e32 v77, 0xbfb8aa3b, v60
	v_fma_f32 v78, v60, s76, -v77
	v_rndne_f32_e32 v79, v77
	v_fmac_f32_e32 v78, 0xb2a5705f, v60
	v_sub_f32_e32 v77, v77, v79
	v_add_f32_e32 v77, v77, v78
	v_exp_f32_e32 v77, v77
	v_cvt_i32_f32_e32 v78, v79
	v_fma_f32 v64, -v64, v76, v71
	v_div_fmas_f32 v64, v64, v65, v76
	v_div_fixup_f32 v54, v64, v56, v54
	v_ldexp_f32 v57, v77, v78
	v_cndmask_b32_e64 v57, 0, v57, s[4:5]
	v_cmp_ngt_f32_e64 s[4:5], s78, v60
	v_mul_f32_e32 v53, v59, v53
	s_nop 0
	v_cndmask_b32_e64 v57, v97, v57, s[4:5]
	v_add_f32_e32 v57, 1.0, v57
	v_div_scale_f32 v60, s[4:5], v57, v57, v55
	v_rcp_f32_e32 v71, v60
	v_cmp_nlt_f32_e64 s[4:5], s77, v70
	v_fma_f32 v56, -v60, v71, 1.0
	v_fmac_f32_e32 v71, v56, v71
	v_div_scale_f32 v56, vcc, v55, v57, v55
	v_mul_f32_e32 v64, v56, v71
	v_fma_f32 v65, -v60, v64, v56
	v_fmac_f32_e32 v64, v65, v71
	v_mul_f32_e32 v65, 0xbfb8aa3b, v70
	v_fma_f32 v76, v70, s76, -v65
	v_rndne_f32_e32 v77, v65
	v_fmac_f32_e32 v76, 0xb2a5705f, v70
	v_sub_f32_e32 v65, v65, v77
	v_add_f32_e32 v65, v65, v76
	v_exp_f32_e32 v65, v65
	v_cvt_i32_f32_e32 v76, v77
	v_fma_f32 v56, -v60, v64, v56
	v_div_fmas_f32 v56, v56, v71, v64
	v_div_fixup_f32 v55, v56, v57, v55
	v_ldexp_f32 v58, v65, v76
	v_cndmask_b32_e64 v58, 0, v58, s[4:5]
	v_cmp_ngt_f32_e64 s[4:5], s78, v70
	v_cvt_pk_bf16_f32 v54, v54, v55
	s_nop 1
	v_cndmask_b32_e64 v58, v97, v58, s[4:5]
	v_add_f32_e32 v58, 1.0, v58
	v_div_scale_f32 v60, s[4:5], v58, v58, v52
	v_rcp_f32_e32 v65, v60
	v_cmp_nlt_f32_e64 s[4:5], s77, v61
	v_fma_f32 v56, -v60, v65, 1.0
	v_fmac_f32_e32 v65, v56, v65
	v_div_scale_f32 v56, vcc, v52, v58, v52
	v_mul_f32_e32 v57, v56, v65
	v_fma_f32 v64, -v60, v57, v56
	v_fmac_f32_e32 v57, v64, v65
	v_mul_f32_e32 v64, 0xbfb8aa3b, v61
	v_fma_f32 v70, v61, s76, -v64
	v_rndne_f32_e32 v71, v64
	v_fmac_f32_e32 v70, 0xb2a5705f, v61
	v_sub_f32_e32 v64, v64, v71
	v_add_f32_e32 v64, v64, v70
	v_exp_f32_e32 v64, v64
	v_cvt_i32_f32_e32 v70, v71
	v_fma_f32 v56, -v60, v57, v56
	v_div_fmas_f32 v56, v56, v65, v57
	v_div_fixup_f32 v52, v56, v58, v52
	v_ldexp_f32 v59, v64, v70
	v_cndmask_b32_e64 v59, 0, v59, s[4:5]
	v_cmp_ngt_f32_e64 s[4:5], s78, v61
	s_nop 1
	v_cndmask_b32_e64 v59, v97, v59, s[4:5]
	v_add_f32_e32 v59, 1.0, v59
	v_div_scale_f32 v60, s[4:5], v59, v59, v53
	v_rcp_f32_e32 v61, v60
	s_nop 0
	v_fma_f32 v56, -v60, v61, 1.0
	v_fmac_f32_e32 v61, v56, v61
	v_div_scale_f32 v56, vcc, v53, v59, v53
	v_mul_f32_e32 v57, v56, v61
	v_fma_f32 v58, -v60, v57, v56
	v_fmac_f32_e32 v57, v58, v61
	v_fma_f32 v56, -v60, v57, v56
	v_div_fmas_f32 v56, v56, v61, v57
	v_div_fixup_f32 v53, v56, v59, v53
	v_cvt_pk_bf16_f32 v53, v52, v53
	v_cndmask_b32_e64 v52, v62, v54, s[2:3]
	v_cndmask_b32_e64 v55, v63, v53, s[2:3]
	ds_bpermute_b32 v52, v98, v52
	ds_bpermute_b32 v56, v98, v55
	s_waitcnt lgkmcnt(1)
	v_cndmask_b32_e64 v54, v54, v52, s[2:3]
	v_cndmask_b32_e64 v52, v52, v62, s[2:3]
	s_waitcnt lgkmcnt(0)
	v_cndmask_b32_e64 v55, v53, v56, s[2:3]
	v_cndmask_b32_e64 v53, v56, v63, s[2:3]
	global_store_dwordx4 v[18:19], v[52:55], off offset:64
	s_nop 1
	v_or_b32_e32 v52, 0x80, v66
	v_mov_b32_e32 v53, v67
	v_lshl_add_u64 v[52:53], v[72:73], 0, v[52:53]
	global_load_dwordx2 v[56:57], v[52:53], off
	s_nop 0
	global_load_dwordx4 v[52:55], v75, s[28:29] offset:256
	s_waitcnt vmcnt(1)
	v_lshlrev_b32_e32 v58, 16, v56
	v_mul_f32_e32 v59, 0xbfb8aa3b, v58
	v_fma_f32 v60, v58, s76, -v59
	v_rndne_f32_e32 v61, v59
	v_fmac_f32_e32 v60, 0xb2a5705f, v58
	v_sub_f32_e32 v59, v59, v61
	v_add_f32_e32 v59, v59, v60
	v_exp_f32_e32 v59, v59
	v_cvt_i32_f32_e32 v60, v61
	s_waitcnt vmcnt(0)
; __device__ __forceinline__ unsigned cvt_pk_bf16(float lo, float hi) { unsigned r; asm volatile("v_cvt_pk_bf16_f32 %0, %1, %2" : "=v"(r) : "v"(lo), "v"(hi)); return r; }
; __device__ __forceinline__ void mlstm_D(LAS unsigned char* lds, int c, int h, const bf16_t* Z, const float* gi, const float* bcum, const float* marr, const bf16_t* CST, const float* NST,
;                                         const float* hgain, bf16_t* YCAT) {
;     ...
; #pragma unroll
;     for (int j = 0; j < 16; j += 2) { u32x2 ab[2];
; #pragma unroll
;         for (int n = 0; n < 2; ++n) { const int col = h * DH + 16 * (j + n) + 4 * fq;
;             const f32x4 gn = *(const f32x4*)(hgain + col); const u32x2 ov = *(const u32x2*)(Z + trow * EVN + 4096 + col);
;             const float o0 = bf_lo(ov.x), o1 = bf_hi(ov.x), o2 = bf_lo(ov.y), o3 = bf_hi(ov.y);
;             const float y0 = acc[j + n][0] * rs * gn[0] / (1.0f + expf(-o0)), y1 = acc[j + n][1] * rs * gn[1] / (1.0f + expf(-o1));
;             const float y2 = acc[j + n][2] * rs * gn[2] / (1.0f + expf(-o2)), y3 = acc[j + n][3] * rs * gn[3] / (1.0f + expf(-o3));
;             ab[n].x = cvt_pk_bf16(y0, y1); ab[n].y = cvt_pk_bf16(y2, y3); }
;         const bool odd = fq & 1; const u32x2 give = odd ? ab[0] : ab[1];
;         u32x2 got; got.x = (unsigned)__shfl_xor((int)give.x, 16); got.y = (unsigned)__shfl_xor((int)give.y, 16);
;         u32x4 w; if (odd) { w.x = got.x; w.y = got.y; w.z = ab[1].x; w.w = ab[1].y; } else { w.x = ab[0].x; w.y = ab[0].y; w.z = got.x; w.w = got.y; }
;         *(u32x4*)(YCAT + trow * D + 1024 + h * DH + 16 * (j + (odd ? 1 : 0)) + 4 * (fq & 2)) = w; if ((j & 3) == 2) asm volatile("" ::: "memory"); }
	v_mul_f32_e32 v50, v52, v50
	v_cmp_nlt_f32_e32 vcc, s77, v58
	v_and_b32_e32 v56, 0xffff0000, v56
	v_ldexp_f32 v52, v59, v60
	v_cndmask_b32_e32 v52, 0, v52, vcc
	v_cmp_ngt_f32_e32 vcc, s78, v58
	v_mul_f32_e32 v51, v53, v51
	v_lshlrev_b32_e32 v60, 16, v57
	v_cndmask_b32_e32 v52, v97, v52, vcc
	v_add_f32_e32 v52, 1.0, v52
	v_div_scale_f32 v58, s[4:5], v52, v52, v50
	v_rcp_f32_e32 v59, v58
	v_cmp_nlt_f32_e64 s[4:5], s77, v56
	v_mul_f32_e32 v48, v54, v48
	v_and_b32_e32 v57, 0xffff0000, v57
	v_fma_f32 v61, -v58, v59, 1.0
	v_fmac_f32_e32 v59, v61, v59
	v_div_scale_f32 v61, vcc, v50, v52, v50
	v_mul_f32_e32 v62, v61, v59
	v_fma_f32 v63, -v58, v62, v61
	v_fmac_f32_e32 v62, v63, v59
	v_mul_f32_e32 v63, 0xbfb8aa3b, v56
	v_fma_f32 v64, v56, s76, -v63
	v_rndne_f32_e32 v65, v63
	v_fmac_f32_e32 v64, 0xb2a5705f, v56
	v_sub_f32_e32 v63, v63, v65
	v_add_f32_e32 v63, v63, v64
	v_exp_f32_e32 v63, v63
	v_cvt_i32_f32_e32 v64, v65
	v_fma_f32 v58, -v58, v62, v61
	v_div_fmas_f32 v58, v58, v59, v62
	v_div_fixup_f32 v50, v58, v52, v50
	v_ldexp_f32 v53, v63, v64
	v_cndmask_b32_e64 v53, 0, v53, s[4:5]
	v_cmp_ngt_f32_e64 s[4:5], s78, v56
	v_mul_f32_e32 v49, v55, v49
	s_nop 0
	v_cndmask_b32_e64 v53, v97, v53, s[4:5]
	v_add_f32_e32 v53, 1.0, v53
	v_div_scale_f32 v56, s[4:5], v53, v53, v51
	v_rcp_f32_e32 v61, v56
	v_cmp_nlt_f32_e64 s[4:5], s77, v60
	v_fma_f32 v52, -v56, v61, 1.0
	v_fmac_f32_e32 v61, v52, v61
	v_div_scale_f32 v52, vcc, v51, v53, v51
	v_mul_f32_e32 v58, v52, v61
	v_fma_f32 v59, -v56, v58, v52
	v_fmac_f32_e32 v58, v59, v61
	v_mul_f32_e32 v59, 0xbfb8aa3b, v60
	v_fma_f32 v62, v60, s76, -v59
	v_rndne_f32_e32 v63, v59
	v_fmac_f32_e32 v62, 0xb2a5705f, v60
	v_sub_f32_e32 v59, v59, v63
	v_add_f32_e32 v59, v59, v62
	v_exp_f32_e32 v59, v59
	v_cvt_i32_f32_e32 v62, v63
	v_fma_f32 v52, -v56, v58, v52
	v_div_fmas_f32 v52, v52, v61, v58
	v_div_fixup_f32 v51, v52, v53, v51
	v_ldexp_f32 v54, v59, v62
	v_cndmask_b32_e64 v54, 0, v54, s[4:5]
	v_cmp_ngt_f32_e64 s[4:5], s78, v60
	s_nop 1
	v_cndmask_b32_e64 v54, v97, v54, s[4:5]
	v_add_f32_e32 v54, 1.0, v54
	v_div_scale_f32 v56, s[4:5], v54, v54, v48
	v_rcp_f32_e32 v59, v56
	v_cmp_nlt_f32_e64 s[4:5], s77, v57
	v_fma_f32 v52, -v56, v59, 1.0
	v_fmac_f32_e32 v59, v52, v59
	v_div_scale_f32 v52, vcc, v48, v54, v48
	v_mul_f32_e32 v53, v52, v59
	v_fma_f32 v58, -v56, v53, v52
	v_fmac_f32_e32 v53, v58, v59
	v_mul_f32_e32 v58, 0xbfb8aa3b, v57
	v_fma_f32 v60, v57, s76, -v58
	v_rndne_f32_e32 v61, v58
	v_fmac_f32_e32 v60, 0xb2a5705f, v57
	v_sub_f32_e32 v58, v58, v61
	v_add_f32_e32 v58, v58, v60
	v_exp_f32_e32 v58, v58
	v_cvt_i32_f32_e32 v60, v61
	v_fma_f32 v52, -v56, v53, v52
	v_div_fmas_f32 v52, v52, v59, v53
	v_div_fixup_f32 v48, v52, v54, v48
	v_ldexp_f32 v55, v58, v60
	v_cndmask_b32_e64 v55, 0, v55, s[4:5]
	v_cmp_ngt_f32_e64 s[4:5], s78, v57
	s_nop 1
	v_cndmask_b32_e64 v55, v97, v55, s[4:5]
	v_add_f32_e32 v55, 1.0, v55
	v_div_scale_f32 v56, s[4:5], v55, v55, v49
	v_rcp_f32_e32 v57, v56
	s_nop 0
	v_fma_f32 v52, -v56, v57, 1.0
	v_fmac_f32_e32 v57, v52, v57
	v_div_scale_f32 v52, vcc, v49, v55, v49
	v_mul_f32_e32 v53, v52, v57
	v_fma_f32 v54, -v56, v53, v52
	v_fmac_f32_e32 v53, v54, v57
	v_fma_f32 v52, -v56, v53, v52
	v_div_fmas_f32 v52, v52, v57, v53
	v_div_fixup_f32 v49, v52, v55, v49
	v_cvt_pk_bf16_f32 v54, v50, v51
	v_cvt_pk_bf16_f32 v55, v48, v49
	v_or_b32_e32 v48, 0xa0, v66
	v_mov_b32_e32 v49, v67
	v_lshl_add_u64 v[48:49], v[72:73], 0, v[48:49]
	global_load_dwordx2 v[52:53], v[48:49], off
	s_nop 0
	global_load_dwordx4 v[48:51], v75, s[28:29] offset:320
	s_waitcnt vmcnt(1)
	v_lshlrev_b32_e32 v56, 16, v52
	v_mul_f32_e32 v57, 0xbfb8aa3b, v56
	v_fma_f32 v58, v56, s76, -v57
	v_rndne_f32_e32 v59, v57
	v_fmac_f32_e32 v58, 0xb2a5705f, v56
	v_sub_f32_e32 v57, v57, v59
	v_add_f32_e32 v57, v57, v58
	v_exp_f32_e32 v57, v57
	v_cvt_i32_f32_e32 v58, v59
	s_waitcnt vmcnt(0)
	v_mul_f32_e32 v46, v48, v46
	v_cmp_nlt_f32_e32 vcc, s77, v56
	v_and_b32_e32 v52, 0xffff0000, v52
	v_ldexp_f32 v48, v57, v58
	v_cndmask_b32_e32 v48, 0, v48, vcc
	v_cmp_ngt_f32_e32 vcc, s78, v56
	v_mul_f32_e32 v47, v49, v47
	v_lshlrev_b32_e32 v58, 16, v53
	v_cndmask_b32_e32 v48, v97, v48, vcc
	v_add_f32_e32 v48, 1.0, v48
	v_div_scale_f32 v56, s[4:5], v48, v48, v46
	v_rcp_f32_e32 v57, v56
	v_cmp_nlt_f32_e64 s[4:5], s77, v52
	v_mul_f32_e32 v44, v50, v44
	v_and_b32_e32 v53, 0xffff0000, v53
	v_fma_f32 v59, -v56, v57, 1.0
	v_fmac_f32_e32 v57, v59, v57
	v_div_scale_f32 v59, vcc, v46, v48, v46
	v_mul_f32_e32 v60, v59, v57
	v_fma_f32 v61, -v56, v60, v59
	v_fmac_f32_e32 v60, v61, v57
	v_mul_f32_e32 v61, 0xbfb8aa3b, v52
	v_fma_f32 v62, v52, s76, -v61
	v_rndne_f32_e32 v63, v61
	v_fmac_f32_e32 v62, 0xb2a5705f, v52
	v_sub_f32_e32 v61, v61, v63
	v_add_f32_e32 v61, v61, v62
	v_exp_f32_e32 v61, v61
	v_cvt_i32_f32_e32 v62, v63
	v_fma_f32 v56, -v56, v60, v59
	v_div_fmas_f32 v56, v56, v57, v60
	v_div_fixup_f32 v46, v56, v48, v46
	v_ldexp_f32 v49, v61, v62
	v_cndmask_b32_e64 v49, 0, v49, s[4:5]
	v_cmp_ngt_f32_e64 s[4:5], s78, v52
	v_mul_f32_e32 v45, v51, v45
	s_nop 0
	v_cndmask_b32_e64 v49, v97, v49, s[4:5]
	v_add_f32_e32 v49, 1.0, v49
	v_div_scale_f32 v52, s[4:5], v49, v49, v47
	v_rcp_f32_e32 v59, v52
	v_cmp_nlt_f32_e64 s[4:5], s77, v58
	v_fma_f32 v48, -v52, v59, 1.0
	v_fmac_f32_e32 v59, v48, v59
	v_div_scale_f32 v48, vcc, v47, v49, v47
	v_mul_f32_e32 v56, v48, v59
	v_fma_f32 v57, -v52, v56, v48
	v_fmac_f32_e32 v56, v57, v59
	v_mul_f32_e32 v57, 0xbfb8aa3b, v58
	v_fma_f32 v60, v58, s76, -v57
	v_rndne_f32_e32 v61, v57
	v_fmac_f32_e32 v60, 0xb2a5705f, v58
	v_sub_f32_e32 v57, v57, v61
	v_add_f32_e32 v57, v57, v60
	v_exp_f32_e32 v57, v57
	v_cvt_i32_f32_e32 v60, v61
	v_fma_f32 v48, -v52, v56, v48
; __device__ __forceinline__ unsigned cvt_pk_bf16(float lo, float hi) { unsigned r; asm volatile("v_cvt_pk_bf16_f32 %0, %1, %2" : "=v"(r) : "v"(lo), "v"(hi)); return r; }
; __device__ __forceinline__ void mlstm_D(LAS unsigned char* lds, int c, int h, const bf16_t* Z, const float* gi, const float* bcum, const float* marr, const bf16_t* CST, const float* NST,
;                                         const float* hgain, bf16_t* YCAT) {
;     ...
; #pragma unroll
;     for (int j = 0; j < 16; j += 2) { u32x2 ab[2];
; #pragma unroll
;         for (int n = 0; n < 2; ++n) { const int col = h * DH + 16 * (j + n) + 4 * fq;
;             const f32x4 gn = *(const f32x4*)(hgain + col); const u32x2 ov = *(const u32x2*)(Z + trow * EVN + 4096 + col);
;             const float o0 = bf_lo(ov.x), o1 = bf_hi(ov.x), o2 = bf_lo(ov.y), o3 = bf_hi(ov.y);
;             const float y0 = acc[j + n][0] * rs * gn[0] / (1.0f + expf(-o0)), y1 = acc[j + n][1] * rs * gn[1] / (1.0f + expf(-o1));
;             const float y2 = acc[j + n][2] * rs * gn[2] / (1.0f + expf(-o2)), y3 = acc[j + n][3] * rs * gn[3] / (1.0f + expf(-o3));
;             ab[n].x = cvt_pk_bf16(y0, y1); ab[n].y = cvt_pk_bf16(y2, y3); }
;         const bool odd = fq & 1; const u32x2 give = odd ? ab[0] : ab[1];
;         u32x2 got; got.x = (unsigned)__shfl_xor((int)give.x, 16); got.y = (unsigned)__shfl_xor((int)give.y, 16);
;         u32x4 w; if (odd) { w.x = got.x; w.y = got.y; w.z = ab[1].x; w.w = ab[1].y; } else { w.x = ab[0].x; w.y = ab[0].y; w.z = got.x; w.w = got.y; }
;         *(u32x4*)(YCAT + trow * D + 1024 + h * DH + 16 * (j + (odd ? 1 : 0)) + 4 * (fq & 2)) = w; if ((j & 3) == 2) asm volatile("" ::: "memory"); }
	v_div_fmas_f32 v48, v48, v59, v56
	v_div_fixup_f32 v47, v48, v49, v47
	v_ldexp_f32 v50, v57, v60
	v_cndmask_b32_e64 v50, 0, v50, s[4:5]
	v_cmp_ngt_f32_e64 s[4:5], s78, v58
	v_cvt_pk_bf16_f32 v46, v46, v47
	s_nop 1
	v_cndmask_b32_e64 v50, v97, v50, s[4:5]
	v_add_f32_e32 v50, 1.0, v50
	v_div_scale_f32 v52, s[4:5], v50, v50, v44
	v_rcp_f32_e32 v57, v52
	v_cmp_nlt_f32_e64 s[4:5], s77, v53
	v_fma_f32 v48, -v52, v57, 1.0
	v_fmac_f32_e32 v57, v48, v57
	v_div_scale_f32 v48, vcc, v44, v50, v44
	v_mul_f32_e32 v49, v48, v57
	v_fma_f32 v56, -v52, v49, v48
	v_fmac_f32_e32 v49, v56, v57
	v_mul_f32_e32 v56, 0xbfb8aa3b, v53
	v_fma_f32 v58, v53, s76, -v56
	v_rndne_f32_e32 v59, v56
	v_fmac_f32_e32 v58, 0xb2a5705f, v53
	v_sub_f32_e32 v56, v56, v59
	v_add_f32_e32 v56, v56, v58
	v_exp_f32_e32 v56, v56
	v_cvt_i32_f32_e32 v58, v59
	v_fma_f32 v48, -v52, v49, v48
	v_div_fmas_f32 v48, v48, v57, v49
	v_div_fixup_f32 v44, v48, v50, v44
	v_ldexp_f32 v51, v56, v58
	v_cndmask_b32_e64 v51, 0, v51, s[4:5]
	v_cmp_ngt_f32_e64 s[4:5], s78, v53
	s_nop 1
	v_cndmask_b32_e64 v51, v97, v51, s[4:5]
	v_add_f32_e32 v51, 1.0, v51
	v_div_scale_f32 v52, s[4:5], v51, v51, v45
	v_rcp_f32_e32 v53, v52
	s_nop 0
	v_fma_f32 v48, -v52, v53, 1.0
	v_fmac_f32_e32 v53, v48, v53
	v_div_scale_f32 v48, vcc, v45, v51, v45
	v_mul_f32_e32 v49, v48, v53
	v_fma_f32 v50, -v52, v49, v48
	v_fmac_f32_e32 v49, v50, v53
	v_fma_f32 v48, -v52, v49, v48
	v_div_fmas_f32 v48, v48, v53, v49
	v_div_fixup_f32 v45, v48, v51, v45
	v_cvt_pk_bf16_f32 v45, v44, v45
	v_cndmask_b32_e64 v44, v54, v46, s[2:3]
	v_cndmask_b32_e64 v47, v55, v45, s[2:3]
	ds_bpermute_b32 v44, v98, v44
	ds_bpermute_b32 v48, v98, v47
	s_waitcnt lgkmcnt(1)
	v_cndmask_b32_e64 v46, v46, v44, s[2:3]
	v_cndmask_b32_e64 v44, v44, v54, s[2:3]
	s_waitcnt lgkmcnt(0)
	v_cndmask_b32_e64 v47, v45, v48, s[2:3]
	v_cndmask_b32_e64 v45, v48, v55, s[2:3]
	global_store_dwordx4 v[18:19], v[44:47], off offset:128
	s_nop 1
	v_or_b32_e32 v44, 0xc0, v66
	v_mov_b32_e32 v45, v67
	v_lshl_add_u64 v[44:45], v[72:73], 0, v[44:45]
	global_load_dwordx2 v[48:49], v[44:45], off
	s_nop 0
	global_load_dwordx4 v[44:47], v75, s[28:29] offset:384
	s_waitcnt vmcnt(1)
	v_lshlrev_b32_e32 v50, 16, v48
	v_mul_f32_e32 v51, 0xbfb8aa3b, v50
	v_fma_f32 v52, v50, s76, -v51
	v_rndne_f32_e32 v53, v51
	v_fmac_f32_e32 v52, 0xb2a5705f, v50
	v_sub_f32_e32 v51, v51, v53
	v_add_f32_e32 v51, v51, v52
	v_exp_f32_e32 v51, v51
	v_cvt_i32_f32_e32 v52, v53
	s_waitcnt vmcnt(0)
	v_mul_f32_e32 v42, v42, v44
	v_cmp_nlt_f32_e32 vcc, s77, v50
	v_and_b32_e32 v48, 0xffff0000, v48
	v_ldexp_f32 v44, v51, v52
	v_cndmask_b32_e32 v44, 0, v44, vcc
	v_cmp_ngt_f32_e32 vcc, s78, v50
	v_mul_f32_e32 v43, v43, v45
	v_lshlrev_b32_e32 v52, 16, v49
	v_cndmask_b32_e32 v44, v97, v44, vcc
	v_add_f32_e32 v44, 1.0, v44
	v_div_scale_f32 v50, s[4:5], v44, v44, v42
	v_rcp_f32_e32 v51, v50
	v_cmp_nlt_f32_e64 s[4:5], s77, v48
	v_mul_f32_e32 v40, v40, v46
	v_and_b32_e32 v49, 0xffff0000, v49
	v_fma_f32 v53, -v50, v51, 1.0
	v_fmac_f32_e32 v51, v53, v51
	v_div_scale_f32 v53, vcc, v42, v44, v42
	v_mul_f32_e32 v54, v53, v51
	v_fma_f32 v55, -v50, v54, v53
	v_fmac_f32_e32 v54, v55, v51
	v_mul_f32_e32 v55, 0xbfb8aa3b, v48
	v_fma_f32 v56, v48, s76, -v55
	v_rndne_f32_e32 v57, v55
	v_fmac_f32_e32 v56, 0xb2a5705f, v48
	v_sub_f32_e32 v55, v55, v57
	v_add_f32_e32 v55, v55, v56
	v_exp_f32_e32 v55, v55
	v_cvt_i32_f32_e32 v56, v57
	v_fma_f32 v50, -v50, v54, v53
	v_div_fmas_f32 v50, v50, v51, v54
	v_div_fixup_f32 v42, v50, v44, v42
	v_ldexp_f32 v45, v55, v56
	v_cndmask_b32_e64 v45, 0, v45, s[4:5]
	v_cmp_ngt_f32_e64 s[4:5], s78, v48
	v_mul_f32_e32 v41, v41, v47
	s_nop 0
	v_cndmask_b32_e64 v45, v97, v45, s[4:5]
	v_add_f32_e32 v45, 1.0, v45
	v_div_scale_f32 v48, s[4:5], v45, v45, v43
	v_rcp_f32_e32 v53, v48
	v_cmp_nlt_f32_e64 s[4:5], s77, v52
	v_fma_f32 v44, -v48, v53, 1.0
	v_fmac_f32_e32 v53, v44, v53
	v_div_scale_f32 v44, vcc, v43, v45, v43
	v_mul_f32_e32 v50, v44, v53
	v_fma_f32 v51, -v48, v50, v44
	v_fmac_f32_e32 v50, v51, v53
	v_mul_f32_e32 v51, 0xbfb8aa3b, v52
	v_fma_f32 v54, v52, s76, -v51
	v_rndne_f32_e32 v55, v51
	v_fmac_f32_e32 v54, 0xb2a5705f, v52
	v_sub_f32_e32 v51, v51, v55
	v_add_f32_e32 v51, v51, v54
	v_exp_f32_e32 v51, v51
	v_cvt_i32_f32_e32 v54, v55
	v_fma_f32 v44, -v48, v50, v44
	v_div_fmas_f32 v44, v44, v53, v50
	v_div_fixup_f32 v43, v44, v45, v43
	v_ldexp_f32 v46, v51, v54
	v_cndmask_b32_e64 v46, 0, v46, s[4:5]
	v_cmp_ngt_f32_e64 s[4:5], s78, v52
	s_nop 1
	v_cndmask_b32_e64 v46, v97, v46, s[4:5]
	v_add_f32_e32 v46, 1.0, v46
	v_div_scale_f32 v48, s[4:5], v46, v46, v40
	v_rcp_f32_e32 v51, v48
	v_cmp_nlt_f32_e64 s[4:5], s77, v49
	v_fma_f32 v44, -v48, v51, 1.0
	v_fmac_f32_e32 v51, v44, v51
	v_div_scale_f32 v44, vcc, v40, v46, v40
	v_mul_f32_e32 v45, v44, v51
	v_fma_f32 v50, -v48, v45, v44
	v_fmac_f32_e32 v45, v50, v51
	v_mul_f32_e32 v50, 0xbfb8aa3b, v49
	v_fma_f32 v52, v49, s76, -v50
	v_rndne_f32_e32 v53, v50
	v_fmac_f32_e32 v52, 0xb2a5705f, v49
	v_sub_f32_e32 v50, v50, v53
	v_add_f32_e32 v50, v50, v52
	v_exp_f32_e32 v50, v50
	v_cvt_i32_f32_e32 v52, v53
	v_fma_f32 v44, -v48, v45, v44
	v_div_fmas_f32 v44, v44, v51, v45
	v_div_fixup_f32 v40, v44, v46, v40
	v_ldexp_f32 v47, v50, v52
	v_cndmask_b32_e64 v47, 0, v47, s[4:5]
	v_cmp_ngt_f32_e64 s[4:5], s78, v49
	s_nop 1
	v_cndmask_b32_e64 v47, v97, v47, s[4:5]
	v_add_f32_e32 v47, 1.0, v47
	v_div_scale_f32 v48, s[4:5], v47, v47, v41
	v_rcp_f32_e32 v49, v48
	s_nop 0
	v_fma_f32 v44, -v48, v49, 1.0
	v_fmac_f32_e32 v49, v44, v49
	v_div_scale_f32 v44, vcc, v41, v47, v41
	v_mul_f32_e32 v45, v44, v49
	v_fma_f32 v46, -v48, v45, v44
	v_fmac_f32_e32 v45, v46, v49
	v_fma_f32 v44, -v48, v45, v44
	v_div_fmas_f32 v44, v44, v49, v45
	v_div_fixup_f32 v41, v44, v47, v41
	v_cvt_pk_bf16_f32 v46, v42, v43
	v_cvt_pk_bf16_f32 v47, v40, v41
	v_or_b32_e32 v40, 0xe0, v66
	v_mov_b32_e32 v41, v67
	v_lshl_add_u64 v[40:41], v[72:73], 0, v[40:41]
	global_load_dwordx2 v[44:45], v[40:41], off
	s_nop 0
	global_load_dwordx4 v[40:43], v75, s[28:29] offset:448
	s_waitcnt vmcnt(1)
; __device__ __forceinline__ unsigned cvt_pk_bf16(float lo, float hi) { unsigned r; asm volatile("v_cvt_pk_bf16_f32 %0, %1, %2" : "=v"(r) : "v"(lo), "v"(hi)); return r; }
; __device__ __forceinline__ void mlstm_D(LAS unsigned char* lds, int c, int h, const bf16_t* Z, const float* gi, const float* bcum, const float* marr, const bf16_t* CST, const float* NST,
;                                         const float* hgain, bf16_t* YCAT) {
;     ...
; #pragma unroll
;     for (int j = 0; j < 16; j += 2) { u32x2 ab[2];
; #pragma unroll
;         for (int n = 0; n < 2; ++n) { const int col = h * DH + 16 * (j + n) + 4 * fq;
;             const f32x4 gn = *(const f32x4*)(hgain + col); const u32x2 ov = *(const u32x2*)(Z + trow * EVN + 4096 + col);
;             const float o0 = bf_lo(ov.x), o1 = bf_hi(ov.x), o2 = bf_lo(ov.y), o3 = bf_hi(ov.y);
;             const float y0 = acc[j + n][0] * rs * gn[0] / (1.0f + expf(-o0)), y1 = acc[j + n][1] * rs * gn[1] / (1.0f + expf(-o1));
;             const float y2 = acc[j + n][2] * rs * gn[2] / (1.0f + expf(-o2)), y3 = acc[j + n][3] * rs * gn[3] / (1.0f + expf(-o3));
;             ab[n].x = cvt_pk_bf16(y0, y1); ab[n].y = cvt_pk_bf16(y2, y3); }
;         const bool odd = fq & 1; const u32x2 give = odd ? ab[0] : ab[1];
;         u32x2 got; got.x = (unsigned)__shfl_xor((int)give.x, 16); got.y = (unsigned)__shfl_xor((int)give.y, 16);
;         u32x4 w; if (odd) { w.x = got.x; w.y = got.y; w.z = ab[1].x; w.w = ab[1].y; } else { w.x = ab[0].x; w.y = ab[0].y; w.z = got.x; w.w = got.y; }
;         *(u32x4*)(YCAT + trow * D + 1024 + h * DH + 16 * (j + (odd ? 1 : 0)) + 4 * (fq & 2)) = w; if ((j & 3) == 2) asm volatile("" ::: "memory"); }
	v_lshlrev_b32_e32 v48, 16, v44
	v_mul_f32_e32 v49, 0xbfb8aa3b, v48
	v_fma_f32 v50, v48, s76, -v49
	v_rndne_f32_e32 v51, v49
	v_fmac_f32_e32 v50, 0xb2a5705f, v48
	v_sub_f32_e32 v49, v49, v51
	v_add_f32_e32 v49, v49, v50
	v_exp_f32_e32 v49, v49
	v_cvt_i32_f32_e32 v50, v51
	s_waitcnt vmcnt(0)
	v_mul_f32_e32 v38, v38, v40
	v_cmp_nlt_f32_e32 vcc, s77, v48
	v_and_b32_e32 v44, 0xffff0000, v44
	v_ldexp_f32 v40, v49, v50
	v_cndmask_b32_e32 v40, 0, v40, vcc
	v_cmp_ngt_f32_e32 vcc, s78, v48
	v_mul_f32_e32 v39, v39, v41
	v_lshlrev_b32_e32 v50, 16, v45
	v_cndmask_b32_e32 v40, v97, v40, vcc
	v_add_f32_e32 v40, 1.0, v40
	v_div_scale_f32 v48, s[4:5], v40, v40, v38
	v_rcp_f32_e32 v49, v48
	v_cmp_nlt_f32_e64 s[4:5], s77, v44
	v_mul_f32_e32 v36, v36, v42
	v_and_b32_e32 v45, 0xffff0000, v45
	v_fma_f32 v51, -v48, v49, 1.0
	v_fmac_f32_e32 v49, v51, v49
	v_div_scale_f32 v51, vcc, v38, v40, v38
	v_mul_f32_e32 v52, v51, v49
	v_fma_f32 v53, -v48, v52, v51
	v_fmac_f32_e32 v52, v53, v49
	v_mul_f32_e32 v53, 0xbfb8aa3b, v44
	v_fma_f32 v54, v44, s76, -v53
	v_rndne_f32_e32 v55, v53
	v_fmac_f32_e32 v54, 0xb2a5705f, v44
	v_sub_f32_e32 v53, v53, v55
	v_add_f32_e32 v53, v53, v54
	v_exp_f32_e32 v53, v53
	v_cvt_i32_f32_e32 v54, v55
	v_fma_f32 v48, -v48, v52, v51
	v_div_fmas_f32 v48, v48, v49, v52
	v_div_fixup_f32 v38, v48, v40, v38
	v_ldexp_f32 v41, v53, v54
	v_cndmask_b32_e64 v41, 0, v41, s[4:5]
	v_cmp_ngt_f32_e64 s[4:5], s78, v44
	v_mul_f32_e32 v37, v37, v43
	s_nop 0
	v_cndmask_b32_e64 v41, v97, v41, s[4:5]
	v_add_f32_e32 v41, 1.0, v41
	v_div_scale_f32 v44, s[4:5], v41, v41, v39
	v_rcp_f32_e32 v51, v44
	v_cmp_nlt_f32_e64 s[4:5], s77, v50
	v_fma_f32 v40, -v44, v51, 1.0
	v_fmac_f32_e32 v51, v40, v51
	v_div_scale_f32 v40, vcc, v39, v41, v39
	v_mul_f32_e32 v48, v40, v51
	v_fma_f32 v49, -v44, v48, v40
	v_fmac_f32_e32 v48, v49, v51
	v_mul_f32_e32 v49, 0xbfb8aa3b, v50
	v_fma_f32 v52, v50, s76, -v49
	v_rndne_f32_e32 v53, v49
	v_fmac_f32_e32 v52, 0xb2a5705f, v50
	v_sub_f32_e32 v49, v49, v53
	v_add_f32_e32 v49, v49, v52
	v_exp_f32_e32 v49, v49
	v_cvt_i32_f32_e32 v52, v53
	v_fma_f32 v40, -v44, v48, v40
	v_div_fmas_f32 v40, v40, v51, v48
	v_div_fixup_f32 v39, v40, v41, v39
	v_ldexp_f32 v42, v49, v52
	v_cndmask_b32_e64 v42, 0, v42, s[4:5]
	v_cmp_ngt_f32_e64 s[4:5], s78, v50
	v_cvt_pk_bf16_f32 v38, v38, v39
	s_nop 1
	v_cndmask_b32_e64 v42, v97, v42, s[4:5]
	v_add_f32_e32 v42, 1.0, v42
	v_div_scale_f32 v44, s[4:5], v42, v42, v36
	v_rcp_f32_e32 v49, v44
	v_cmp_nlt_f32_e64 s[4:5], s77, v45
	v_fma_f32 v40, -v44, v49, 1.0
	v_fmac_f32_e32 v49, v40, v49
	v_div_scale_f32 v40, vcc, v36, v42, v36
	v_mul_f32_e32 v41, v40, v49
	v_fma_f32 v48, -v44, v41, v40
	v_fmac_f32_e32 v41, v48, v49
	v_mul_f32_e32 v48, 0xbfb8aa3b, v45
	v_fma_f32 v50, v45, s76, -v48
	v_rndne_f32_e32 v51, v48
	v_fmac_f32_e32 v50, 0xb2a5705f, v45
	v_sub_f32_e32 v48, v48, v51
	v_add_f32_e32 v48, v48, v50
	v_exp_f32_e32 v48, v48
	v_cvt_i32_f32_e32 v50, v51
	v_fma_f32 v40, -v44, v41, v40
	v_div_fmas_f32 v40, v40, v49, v41
	v_div_fixup_f32 v36, v40, v42, v36
	v_ldexp_f32 v43, v48, v50
	v_cndmask_b32_e64 v43, 0, v43, s[4:5]
	v_cmp_ngt_f32_e64 s[4:5], s78, v45
	s_nop 1
	v_cndmask_b32_e64 v43, v97, v43, s[4:5]
	v_add_f32_e32 v43, 1.0, v43
	v_div_scale_f32 v44, s[4:5], v43, v43, v37
	v_rcp_f32_e32 v45, v44
	s_nop 0
	v_fma_f32 v40, -v44, v45, 1.0
	v_fmac_f32_e32 v45, v40, v45
	v_div_scale_f32 v40, vcc, v37, v43, v37
	v_mul_f32_e32 v41, v40, v45
	v_fma_f32 v42, -v44, v41, v40
	v_fmac_f32_e32 v41, v42, v45
	v_fma_f32 v40, -v44, v41, v40
	v_div_fmas_f32 v40, v40, v45, v41
	v_div_fixup_f32 v37, v40, v43, v37
	v_cvt_pk_bf16_f32 v37, v36, v37
	v_cndmask_b32_e64 v36, v46, v38, s[2:3]
	v_cndmask_b32_e64 v39, v47, v37, s[2:3]
	ds_bpermute_b32 v36, v98, v36
	ds_bpermute_b32 v40, v98, v39
	s_waitcnt lgkmcnt(1)
	v_cndmask_b32_e64 v38, v38, v36, s[2:3]
	v_cndmask_b32_e64 v36, v36, v46, s[2:3]
	s_waitcnt lgkmcnt(0)
	v_cndmask_b32_e64 v39, v37, v40, s[2:3]
	v_cndmask_b32_e64 v37, v40, v47, s[2:3]
	global_store_dwordx4 v[18:19], v[36:39], off offset:192
	s_nop 1
	v_or_b32_e32 v36, 0x100, v66
	v_mov_b32_e32 v37, v67
	v_lshl_add_u64 v[36:37], v[72:73], 0, v[36:37]
	global_load_dwordx2 v[40:41], v[36:37], off
	s_nop 0
	global_load_dwordx4 v[36:39], v75, s[28:29] offset:512
	s_waitcnt vmcnt(1)
	v_lshlrev_b32_e32 v42, 16, v40
	v_mul_f32_e32 v43, 0xbfb8aa3b, v42
	v_fma_f32 v44, v42, s76, -v43
	v_rndne_f32_e32 v45, v43
	v_fmac_f32_e32 v44, 0xb2a5705f, v42
	v_sub_f32_e32 v43, v43, v45
	v_add_f32_e32 v43, v43, v44
	v_exp_f32_e32 v43, v43
	v_cvt_i32_f32_e32 v44, v45
	s_waitcnt vmcnt(0)
; __device__ __forceinline__ unsigned cvt_pk_bf16(float lo, float hi) { unsigned r; asm volatile("v_cvt_pk_bf16_f32 %0, %1, %2" : "=v"(r) : "v"(lo), "v"(hi)); return r; }
; __device__ __forceinline__ void mlstm_D(LAS unsigned char* lds, int c, int h, const bf16_t* Z, const float* gi, const float* bcum, const float* marr, const bf16_t* CST, const float* NST,
;                                         const float* hgain, bf16_t* YCAT) {
;     ...
; #pragma unroll
;     for (int j = 0; j < 16; j += 2) { u32x2 ab[2];
; #pragma unroll
;         for (int n = 0; n < 2; ++n) { const int col = h * DH + 16 * (j + n) + 4 * fq;
;             const f32x4 gn = *(const f32x4*)(hgain + col); const u32x2 ov = *(const u32x2*)(Z + trow * EVN + 4096 + col);
;             const float o0 = bf_lo(ov.x), o1 = bf_hi(ov.x), o2 = bf_lo(ov.y), o3 = bf_hi(ov.y);
;             const float y0 = acc[j + n][0] * rs * gn[0] / (1.0f + expf(-o0)), y1 = acc[j + n][1] * rs * gn[1] / (1.0f + expf(-o1));
;             const float y2 = acc[j + n][2] * rs * gn[2] / (1.0f + expf(-o2)), y3 = acc[j + n][3] * rs * gn[3] / (1.0f + expf(-o3));
;             ab[n].x = cvt_pk_bf16(y0, y1); ab[n].y = cvt_pk_bf16(y2, y3); }
;         const bool odd = fq & 1; const u32x2 give = odd ? ab[0] : ab[1];
;         u32x2 got; got.x = (unsigned)__shfl_xor((int)give.x, 16); got.y = (unsigned)__shfl_xor((int)give.y, 16);
;         u32x4 w; if (odd) { w.x = got.x; w.y = got.y; w.z = ab[1].x; w.w = ab[1].y; } else { w.x = ab[0].x; w.y = ab[0].y; w.z = got.x; w.w = got.y; }
;         *(u32x4*)(YCAT + trow * D + 1024 + h * DH + 16 * (j + (odd ? 1 : 0)) + 4 * (fq & 2)) = w; if ((j & 3) == 2) asm volatile("" ::: "memory"); }
	v_mul_f32_e32 v34, v34, v36
	v_cmp_nlt_f32_e32 vcc, s77, v42
	v_and_b32_e32 v40, 0xffff0000, v40
	v_ldexp_f32 v36, v43, v44
	v_cndmask_b32_e32 v36, 0, v36, vcc
	v_cmp_ngt_f32_e32 vcc, s78, v42
	v_mul_f32_e32 v35, v35, v37
	v_lshlrev_b32_e32 v44, 16, v41
	v_cndmask_b32_e32 v36, v97, v36, vcc
	v_add_f32_e32 v36, 1.0, v36
	v_div_scale_f32 v42, s[4:5], v36, v36, v34
	v_rcp_f32_e32 v43, v42
	v_cmp_nlt_f32_e64 s[4:5], s77, v40
	v_mul_f32_e32 v32, v32, v38
	v_and_b32_e32 v41, 0xffff0000, v41
	v_fma_f32 v45, -v42, v43, 1.0
	v_fmac_f32_e32 v43, v45, v43
	v_div_scale_f32 v45, vcc, v34, v36, v34
	v_mul_f32_e32 v46, v45, v43
	v_fma_f32 v47, -v42, v46, v45
	v_fmac_f32_e32 v46, v47, v43
	v_mul_f32_e32 v47, 0xbfb8aa3b, v40
	v_fma_f32 v48, v40, s76, -v47
	v_rndne_f32_e32 v49, v47
	v_fmac_f32_e32 v48, 0xb2a5705f, v40
	v_sub_f32_e32 v47, v47, v49
	v_add_f32_e32 v47, v47, v48
	v_exp_f32_e32 v47, v47
	v_cvt_i32_f32_e32 v48, v49
	v_fma_f32 v42, -v42, v46, v45
	v_div_fmas_f32 v42, v42, v43, v46
	v_div_fixup_f32 v34, v42, v36, v34
	v_ldexp_f32 v37, v47, v48
	v_cndmask_b32_e64 v37, 0, v37, s[4:5]
	v_cmp_ngt_f32_e64 s[4:5], s78, v40
	v_mul_f32_e32 v33, v33, v39
	s_nop 0
	v_cndmask_b32_e64 v37, v97, v37, s[4:5]
	v_add_f32_e32 v37, 1.0, v37
	v_div_scale_f32 v40, s[4:5], v37, v37, v35
	v_rcp_f32_e32 v45, v40
	v_cmp_nlt_f32_e64 s[4:5], s77, v44
	v_fma_f32 v36, -v40, v45, 1.0
	v_fmac_f32_e32 v45, v36, v45
	v_div_scale_f32 v36, vcc, v35, v37, v35
	v_mul_f32_e32 v42, v36, v45
	v_fma_f32 v43, -v40, v42, v36
	v_fmac_f32_e32 v42, v43, v45
	v_mul_f32_e32 v43, 0xbfb8aa3b, v44
	v_fma_f32 v46, v44, s76, -v43
	v_rndne_f32_e32 v47, v43
	v_fmac_f32_e32 v46, 0xb2a5705f, v44
	v_sub_f32_e32 v43, v43, v47
	v_add_f32_e32 v43, v43, v46
	v_exp_f32_e32 v43, v43
	v_cvt_i32_f32_e32 v46, v47
	v_fma_f32 v36, -v40, v42, v36
	v_div_fmas_f32 v36, v36, v45, v42
	v_div_fixup_f32 v35, v36, v37, v35
	v_ldexp_f32 v38, v43, v46
	v_cndmask_b32_e64 v38, 0, v38, s[4:5]
	v_cmp_ngt_f32_e64 s[4:5], s78, v44
	s_nop 1
	v_cndmask_b32_e64 v38, v97, v38, s[4:5]
	v_add_f32_e32 v38, 1.0, v38
	v_div_scale_f32 v40, s[4:5], v38, v38, v32
	v_rcp_f32_e32 v43, v40
	v_cmp_nlt_f32_e64 s[4:5], s77, v41
	v_fma_f32 v36, -v40, v43, 1.0
	v_fmac_f32_e32 v43, v36, v43
	v_div_scale_f32 v36, vcc, v32, v38, v32
	v_mul_f32_e32 v37, v36, v43
	v_fma_f32 v42, -v40, v37, v36
	v_fmac_f32_e32 v37, v42, v43
	v_mul_f32_e32 v42, 0xbfb8aa3b, v41
	v_fma_f32 v44, v41, s76, -v42
	v_rndne_f32_e32 v45, v42
	v_fmac_f32_e32 v44, 0xb2a5705f, v41
	v_sub_f32_e32 v42, v42, v45
	v_add_f32_e32 v42, v42, v44
	v_exp_f32_e32 v42, v42
	v_cvt_i32_f32_e32 v44, v45
	v_fma_f32 v36, -v40, v37, v36
	v_div_fmas_f32 v36, v36, v43, v37
	v_div_fixup_f32 v32, v36, v38, v32
	v_ldexp_f32 v39, v42, v44
	v_cndmask_b32_e64 v39, 0, v39, s[4:5]
	v_cmp_ngt_f32_e64 s[4:5], s78, v41
	s_nop 1
	v_cndmask_b32_e64 v39, v97, v39, s[4:5]
	v_add_f32_e32 v39, 1.0, v39
	v_div_scale_f32 v40, s[4:5], v39, v39, v33
	v_rcp_f32_e32 v41, v40
	s_nop 0
	v_fma_f32 v36, -v40, v41, 1.0
	v_fmac_f32_e32 v41, v36, v41
	v_div_scale_f32 v36, vcc, v33, v39, v33
	v_mul_f32_e32 v37, v36, v41
	v_fma_f32 v38, -v40, v37, v36
	v_fmac_f32_e32 v37, v38, v41
	v_fma_f32 v36, -v40, v37, v36
	v_div_fmas_f32 v36, v36, v41, v37
	v_div_fixup_f32 v33, v36, v39, v33
	v_cvt_pk_bf16_f32 v38, v34, v35
	v_cvt_pk_bf16_f32 v39, v32, v33
	v_or_b32_e32 v32, 0x120, v66
	v_mov_b32_e32 v33, v67
	v_lshl_add_u64 v[32:33], v[72:73], 0, v[32:33]
	global_load_dwordx2 v[36:37], v[32:33], off
	s_nop 0
	global_load_dwordx4 v[32:35], v75, s[28:29] offset:576
	s_waitcnt vmcnt(1)
	v_lshlrev_b32_e32 v40, 16, v36
	v_mul_f32_e32 v41, 0xbfb8aa3b, v40
	v_fma_f32 v42, v40, s76, -v41
	v_rndne_f32_e32 v43, v41
	v_fmac_f32_e32 v42, 0xb2a5705f, v40
	v_sub_f32_e32 v41, v41, v43
	v_add_f32_e32 v41, v41, v42
	v_exp_f32_e32 v41, v41
	v_cvt_i32_f32_e32 v42, v43
	s_waitcnt vmcnt(0)
	v_mul_f32_e32 v30, v30, v32
	v_cmp_nlt_f32_e32 vcc, s77, v40
	v_and_b32_e32 v36, 0xffff0000, v36
	v_ldexp_f32 v32, v41, v42
	v_cndmask_b32_e32 v32, 0, v32, vcc
	v_cmp_ngt_f32_e32 vcc, s78, v40
	v_mul_f32_e32 v31, v31, v33
	v_lshlrev_b32_e32 v42, 16, v37
	v_cndmask_b32_e32 v32, v97, v32, vcc
	v_add_f32_e32 v32, 1.0, v32
	v_div_scale_f32 v40, s[4:5], v32, v32, v30
	v_rcp_f32_e32 v41, v40
	v_cmp_nlt_f32_e64 s[4:5], s77, v36
	v_mul_f32_e32 v28, v28, v34
	v_and_b32_e32 v37, 0xffff0000, v37
	v_fma_f32 v43, -v40, v41, 1.0
	v_fmac_f32_e32 v41, v43, v41
	v_div_scale_f32 v43, vcc, v30, v32, v30
	v_mul_f32_e32 v44, v43, v41
	v_fma_f32 v45, -v40, v44, v43
	v_fmac_f32_e32 v44, v45, v41
	v_mul_f32_e32 v45, 0xbfb8aa3b, v36
	v_fma_f32 v46, v36, s76, -v45
	v_rndne_f32_e32 v47, v45
	v_fmac_f32_e32 v46, 0xb2a5705f, v36
	v_sub_f32_e32 v45, v45, v47
	v_add_f32_e32 v45, v45, v46
	v_exp_f32_e32 v45, v45
	v_cvt_i32_f32_e32 v46, v47
	v_fma_f32 v40, -v40, v44, v43
	v_div_fmas_f32 v40, v40, v41, v44
	v_div_fixup_f32 v30, v40, v32, v30
	v_ldexp_f32 v33, v45, v46
	v_cndmask_b32_e64 v33, 0, v33, s[4:5]
	v_cmp_ngt_f32_e64 s[4:5], s78, v36
	v_mul_f32_e32 v29, v29, v35
	s_nop 0
	v_cndmask_b32_e64 v33, v97, v33, s[4:5]
	v_add_f32_e32 v33, 1.0, v33
	v_div_scale_f32 v36, s[4:5], v33, v33, v31
	v_rcp_f32_e32 v43, v36
	v_cmp_nlt_f32_e64 s[4:5], s77, v42
	v_fma_f32 v32, -v36, v43, 1.0
	v_fmac_f32_e32 v43, v32, v43
	v_div_scale_f32 v32, vcc, v31, v33, v31
	v_mul_f32_e32 v40, v32, v43
	v_fma_f32 v41, -v36, v40, v32
	v_fmac_f32_e32 v40, v41, v43
	v_mul_f32_e32 v41, 0xbfb8aa3b, v42
	v_fma_f32 v44, v42, s76, -v41
	v_rndne_f32_e32 v45, v41
	v_fmac_f32_e32 v44, 0xb2a5705f, v42
	v_sub_f32_e32 v41, v41, v45
	v_add_f32_e32 v41, v41, v44
	v_exp_f32_e32 v41, v41
	v_cvt_i32_f32_e32 v44, v45
	v_fma_f32 v32, -v36, v40, v32
; __device__ __forceinline__ unsigned cvt_pk_bf16(float lo, float hi) { unsigned r; asm volatile("v_cvt_pk_bf16_f32 %0, %1, %2" : "=v"(r) : "v"(lo), "v"(hi)); return r; }
; __device__ __forceinline__ void mlstm_D(LAS unsigned char* lds, int c, int h, const bf16_t* Z, const float* gi, const float* bcum, const float* marr, const bf16_t* CST, const float* NST,
;                                         const float* hgain, bf16_t* YCAT) {
;     ...
; #pragma unroll
;     for (int j = 0; j < 16; j += 2) { u32x2 ab[2];
; #pragma unroll
;         for (int n = 0; n < 2; ++n) { const int col = h * DH + 16 * (j + n) + 4 * fq;
;             const f32x4 gn = *(const f32x4*)(hgain + col); const u32x2 ov = *(const u32x2*)(Z + trow * EVN + 4096 + col);
;             const float o0 = bf_lo(ov.x), o1 = bf_hi(ov.x), o2 = bf_lo(ov.y), o3 = bf_hi(ov.y);
;             const float y0 = acc[j + n][0] * rs * gn[0] / (1.0f + expf(-o0)), y1 = acc[j + n][1] * rs * gn[1] / (1.0f + expf(-o1));
;             const float y2 = acc[j + n][2] * rs * gn[2] / (1.0f + expf(-o2)), y3 = acc[j + n][3] * rs * gn[3] / (1.0f + expf(-o3));
;             ab[n].x = cvt_pk_bf16(y0, y1); ab[n].y = cvt_pk_bf16(y2, y3); }
;         const bool odd = fq & 1; const u32x2 give = odd ? ab[0] : ab[1];
;         u32x2 got; got.x = (unsigned)__shfl_xor((int)give.x, 16); got.y = (unsigned)__shfl_xor((int)give.y, 16);
;         u32x4 w; if (odd) { w.x = got.x; w.y = got.y; w.z = ab[1].x; w.w = ab[1].y; } else { w.x = ab[0].x; w.y = ab[0].y; w.z = got.x; w.w = got.y; }
;         *(u32x4*)(YCAT + trow * D + 1024 + h * DH + 16 * (j + (odd ? 1 : 0)) + 4 * (fq & 2)) = w; if ((j & 3) == 2) asm volatile("" ::: "memory"); }
	v_div_fmas_f32 v32, v32, v43, v40
	v_div_fixup_f32 v31, v32, v33, v31
	v_ldexp_f32 v34, v41, v44
	v_cndmask_b32_e64 v34, 0, v34, s[4:5]
	v_cmp_ngt_f32_e64 s[4:5], s78, v42
	v_cvt_pk_bf16_f32 v30, v30, v31
	s_nop 1
	v_cndmask_b32_e64 v34, v97, v34, s[4:5]
	v_add_f32_e32 v34, 1.0, v34
	v_div_scale_f32 v36, s[4:5], v34, v34, v28
	v_rcp_f32_e32 v41, v36
	v_cmp_nlt_f32_e64 s[4:5], s77, v37
	v_fma_f32 v32, -v36, v41, 1.0
	v_fmac_f32_e32 v41, v32, v41
	v_div_scale_f32 v32, vcc, v28, v34, v28
	v_mul_f32_e32 v33, v32, v41
	v_fma_f32 v40, -v36, v33, v32
	v_fmac_f32_e32 v33, v40, v41
	v_mul_f32_e32 v40, 0xbfb8aa3b, v37
	v_fma_f32 v42, v37, s76, -v40
	v_rndne_f32_e32 v43, v40
	v_fmac_f32_e32 v42, 0xb2a5705f, v37
	v_sub_f32_e32 v40, v40, v43
	v_add_f32_e32 v40, v40, v42
	v_exp_f32_e32 v40, v40
	v_cvt_i32_f32_e32 v42, v43
	v_fma_f32 v32, -v36, v33, v32
	v_div_fmas_f32 v32, v32, v41, v33
	v_div_fixup_f32 v28, v32, v34, v28
	v_ldexp_f32 v35, v40, v42
	v_cndmask_b32_e64 v35, 0, v35, s[4:5]
	v_cmp_ngt_f32_e64 s[4:5], s78, v37
	s_nop 1
	v_cndmask_b32_e64 v35, v97, v35, s[4:5]
	v_add_f32_e32 v35, 1.0, v35
	v_div_scale_f32 v36, s[4:5], v35, v35, v29
	v_rcp_f32_e32 v37, v36
	s_nop 0
	v_fma_f32 v32, -v36, v37, 1.0
	v_fmac_f32_e32 v37, v32, v37
	v_div_scale_f32 v32, vcc, v29, v35, v29
	v_mul_f32_e32 v33, v32, v37
	v_fma_f32 v34, -v36, v33, v32
	v_fmac_f32_e32 v33, v34, v37
	v_fma_f32 v32, -v36, v33, v32
	v_div_fmas_f32 v32, v32, v37, v33
	v_div_fixup_f32 v29, v32, v35, v29
	v_cvt_pk_bf16_f32 v29, v28, v29
	v_cndmask_b32_e64 v28, v38, v30, s[2:3]
	v_cndmask_b32_e64 v31, v39, v29, s[2:3]
	ds_bpermute_b32 v28, v98, v28
	ds_bpermute_b32 v32, v98, v31
	s_waitcnt lgkmcnt(1)
	v_cndmask_b32_e64 v30, v30, v28, s[2:3]
	v_cndmask_b32_e64 v28, v28, v38, s[2:3]
	s_waitcnt lgkmcnt(0)
	v_cndmask_b32_e64 v31, v29, v32, s[2:3]
	v_cndmask_b32_e64 v29, v32, v39, s[2:3]
	global_store_dwordx4 v[18:19], v[28:31], off offset:256
	s_nop 1
	v_or_b32_e32 v28, 0x140, v66
	v_mov_b32_e32 v29, v67
	v_lshl_add_u64 v[28:29], v[72:73], 0, v[28:29]
	global_load_dwordx2 v[32:33], v[28:29], off
	s_nop 0
	global_load_dwordx4 v[28:31], v75, s[28:29] offset:640
	s_waitcnt vmcnt(1)
	v_lshlrev_b32_e32 v34, 16, v32
	v_mul_f32_e32 v35, 0xbfb8aa3b, v34
	v_fma_f32 v36, v34, s76, -v35
	v_rndne_f32_e32 v37, v35
	v_fmac_f32_e32 v36, 0xb2a5705f, v34
	v_sub_f32_e32 v35, v35, v37
	v_add_f32_e32 v35, v35, v36
	v_exp_f32_e32 v35, v35
	v_cvt_i32_f32_e32 v36, v37
	s_waitcnt vmcnt(0)
	v_mul_f32_e32 v26, v26, v28
	v_cmp_nlt_f32_e32 vcc, s77, v34
	v_and_b32_e32 v32, 0xffff0000, v32
	v_ldexp_f32 v28, v35, v36
	v_cndmask_b32_e32 v28, 0, v28, vcc
	v_cmp_ngt_f32_e32 vcc, s78, v34
	v_mul_f32_e32 v27, v27, v29
	v_lshlrev_b32_e32 v36, 16, v33
	v_cndmask_b32_e32 v28, v97, v28, vcc
	v_add_f32_e32 v28, 1.0, v28
	v_div_scale_f32 v34, s[4:5], v28, v28, v26
	v_rcp_f32_e32 v35, v34
	v_cmp_nlt_f32_e64 s[4:5], s77, v32
	v_mul_f32_e32 v24, v24, v30
	v_and_b32_e32 v33, 0xffff0000, v33
	v_fma_f32 v37, -v34, v35, 1.0
	v_fmac_f32_e32 v35, v37, v35
	v_div_scale_f32 v37, vcc, v26, v28, v26
	v_mul_f32_e32 v38, v37, v35
	v_fma_f32 v39, -v34, v38, v37
	v_fmac_f32_e32 v38, v39, v35
	v_mul_f32_e32 v39, 0xbfb8aa3b, v32
	v_fma_f32 v40, v32, s76, -v39
	v_rndne_f32_e32 v41, v39
	v_fmac_f32_e32 v40, 0xb2a5705f, v32
	v_sub_f32_e32 v39, v39, v41
	v_add_f32_e32 v39, v39, v40
	v_exp_f32_e32 v39, v39
	v_cvt_i32_f32_e32 v40, v41
	v_fma_f32 v34, -v34, v38, v37
	v_div_fmas_f32 v34, v34, v35, v38
	v_div_fixup_f32 v26, v34, v28, v26
	v_ldexp_f32 v29, v39, v40
	v_cndmask_b32_e64 v29, 0, v29, s[4:5]
	v_cmp_ngt_f32_e64 s[4:5], s78, v32
	v_mul_f32_e32 v25, v25, v31
	s_nop 0
	v_cndmask_b32_e64 v29, v97, v29, s[4:5]
	v_add_f32_e32 v29, 1.0, v29
	v_div_scale_f32 v32, s[4:5], v29, v29, v27
	v_rcp_f32_e32 v37, v32
	v_cmp_nlt_f32_e64 s[4:5], s77, v36
	v_fma_f32 v28, -v32, v37, 1.0
	v_fmac_f32_e32 v37, v28, v37
	v_div_scale_f32 v28, vcc, v27, v29, v27
	v_mul_f32_e32 v34, v28, v37
	v_fma_f32 v35, -v32, v34, v28
	v_fmac_f32_e32 v34, v35, v37
	v_mul_f32_e32 v35, 0xbfb8aa3b, v36
	v_fma_f32 v38, v36, s76, -v35
	v_rndne_f32_e32 v39, v35
	v_fmac_f32_e32 v38, 0xb2a5705f, v36
	v_sub_f32_e32 v35, v35, v39
	v_add_f32_e32 v35, v35, v38
	v_exp_f32_e32 v35, v35
	v_cvt_i32_f32_e32 v38, v39
	v_fma_f32 v28, -v32, v34, v28
	v_div_fmas_f32 v28, v28, v37, v34
	v_div_fixup_f32 v27, v28, v29, v27
	v_ldexp_f32 v30, v35, v38
	v_cndmask_b32_e64 v30, 0, v30, s[4:5]
	v_cmp_ngt_f32_e64 s[4:5], s78, v36
	s_nop 1
	v_cndmask_b32_e64 v30, v97, v30, s[4:5]
	v_add_f32_e32 v30, 1.0, v30
	v_div_scale_f32 v32, s[4:5], v30, v30, v24
	v_rcp_f32_e32 v35, v32
	v_cmp_nlt_f32_e64 s[4:5], s77, v33
	v_fma_f32 v28, -v32, v35, 1.0
	v_fmac_f32_e32 v35, v28, v35
	v_div_scale_f32 v28, vcc, v24, v30, v24
	v_mul_f32_e32 v29, v28, v35
	v_fma_f32 v34, -v32, v29, v28
	v_fmac_f32_e32 v29, v34, v35
	v_mul_f32_e32 v34, 0xbfb8aa3b, v33
	v_fma_f32 v36, v33, s76, -v34
	v_rndne_f32_e32 v37, v34
	v_fmac_f32_e32 v36, 0xb2a5705f, v33
	v_sub_f32_e32 v34, v34, v37
	v_add_f32_e32 v34, v34, v36
	v_exp_f32_e32 v34, v34
	v_cvt_i32_f32_e32 v36, v37
	v_fma_f32 v28, -v32, v29, v28
	v_div_fmas_f32 v28, v28, v35, v29
	v_div_fixup_f32 v24, v28, v30, v24
	v_ldexp_f32 v31, v34, v36
	v_cndmask_b32_e64 v31, 0, v31, s[4:5]
	v_cmp_ngt_f32_e64 s[4:5], s78, v33
	s_nop 1
	v_cndmask_b32_e64 v31, v97, v31, s[4:5]
	v_add_f32_e32 v31, 1.0, v31
	v_div_scale_f32 v32, s[4:5], v31, v31, v25
	v_rcp_f32_e32 v33, v32
	s_nop 0
	v_fma_f32 v28, -v32, v33, 1.0
	v_fmac_f32_e32 v33, v28, v33
	v_div_scale_f32 v28, vcc, v25, v31, v25
	v_mul_f32_e32 v29, v28, v33
	v_fma_f32 v30, -v32, v29, v28
	v_fmac_f32_e32 v29, v30, v33
	v_fma_f32 v28, -v32, v29, v28
	v_div_fmas_f32 v28, v28, v33, v29
	v_div_fixup_f32 v25, v28, v31, v25
	v_cvt_pk_bf16_f32 v30, v26, v27
	v_cvt_pk_bf16_f32 v31, v24, v25
	v_or_b32_e32 v24, 0x160, v66
	v_mov_b32_e32 v25, v67
	v_lshl_add_u64 v[24:25], v[72:73], 0, v[24:25]
	global_load_dwordx2 v[28:29], v[24:25], off
	s_nop 0
	global_load_dwordx4 v[24:27], v75, s[28:29] offset:704
	s_waitcnt vmcnt(1)
; __device__ __forceinline__ unsigned cvt_pk_bf16(float lo, float hi) { unsigned r; asm volatile("v_cvt_pk_bf16_f32 %0, %1, %2" : "=v"(r) : "v"(lo), "v"(hi)); return r; }
; __device__ __forceinline__ void mlstm_D(LAS unsigned char* lds, int c, int h, const bf16_t* Z, const float* gi, const float* bcum, const float* marr, const bf16_t* CST, const float* NST,
;                                         const float* hgain, bf16_t* YCAT) {
;     ...
; #pragma unroll
;     for (int j = 0; j < 16; j += 2) { u32x2 ab[2];
; #pragma unroll
;         for (int n = 0; n < 2; ++n) { const int col = h * DH + 16 * (j + n) + 4 * fq;
;             const f32x4 gn = *(const f32x4*)(hgain + col); const u32x2 ov = *(const u32x2*)(Z + trow * EVN + 4096 + col);
;             const float o0 = bf_lo(ov.x), o1 = bf_hi(ov.x), o2 = bf_lo(ov.y), o3 = bf_hi(ov.y);
;             const float y0 = acc[j + n][0] * rs * gn[0] / (1.0f + expf(-o0)), y1 = acc[j + n][1] * rs * gn[1] / (1.0f + expf(-o1));
;             const float y2 = acc[j + n][2] * rs * gn[2] / (1.0f + expf(-o2)), y3 = acc[j + n][3] * rs * gn[3] / (1.0f + expf(-o3));
;             ab[n].x = cvt_pk_bf16(y0, y1); ab[n].y = cvt_pk_bf16(y2, y3); }
;         const bool odd = fq & 1; const u32x2 give = odd ? ab[0] : ab[1];
;         u32x2 got; got.x = (unsigned)__shfl_xor((int)give.x, 16); got.y = (unsigned)__shfl_xor((int)give.y, 16);
;         u32x4 w; if (odd) { w.x = got.x; w.y = got.y; w.z = ab[1].x; w.w = ab[1].y; } else { w.x = ab[0].x; w.y = ab[0].y; w.z = got.x; w.w = got.y; }
;         *(u32x4*)(YCAT + trow * D + 1024 + h * DH + 16 * (j + (odd ? 1 : 0)) + 4 * (fq & 2)) = w; if ((j & 3) == 2) asm volatile("" ::: "memory"); }
	v_lshlrev_b32_e32 v32, 16, v28
	v_mul_f32_e32 v33, 0xbfb8aa3b, v32
	v_fma_f32 v34, v32, s76, -v33
	v_rndne_f32_e32 v35, v33
	v_fmac_f32_e32 v34, 0xb2a5705f, v32
	v_sub_f32_e32 v33, v33, v35
	v_add_f32_e32 v33, v33, v34
	v_exp_f32_e32 v33, v33
	v_cvt_i32_f32_e32 v34, v35
	s_waitcnt vmcnt(0)
	v_mul_f32_e32 v22, v22, v24
	v_cmp_nlt_f32_e32 vcc, s77, v32
	v_and_b32_e32 v28, 0xffff0000, v28
	v_ldexp_f32 v24, v33, v34
	v_cndmask_b32_e32 v24, 0, v24, vcc
	v_cmp_ngt_f32_e32 vcc, s78, v32
	v_mul_f32_e32 v23, v23, v25
	v_lshlrev_b32_e32 v34, 16, v29
	v_cndmask_b32_e32 v24, v97, v24, vcc
	v_add_f32_e32 v24, 1.0, v24
	v_div_scale_f32 v32, s[4:5], v24, v24, v22
	v_rcp_f32_e32 v33, v32
	v_cmp_nlt_f32_e64 s[4:5], s77, v28
	v_mul_f32_e32 v20, v20, v26
	v_and_b32_e32 v29, 0xffff0000, v29
	v_fma_f32 v35, -v32, v33, 1.0
	v_fmac_f32_e32 v33, v35, v33
	v_div_scale_f32 v35, vcc, v22, v24, v22
	v_mul_f32_e32 v36, v35, v33
	v_fma_f32 v37, -v32, v36, v35
	v_fmac_f32_e32 v36, v37, v33
	v_mul_f32_e32 v37, 0xbfb8aa3b, v28
	v_fma_f32 v38, v28, s76, -v37
	v_rndne_f32_e32 v39, v37
	v_fmac_f32_e32 v38, 0xb2a5705f, v28
	v_sub_f32_e32 v37, v37, v39
	v_add_f32_e32 v37, v37, v38
	v_exp_f32_e32 v37, v37
	v_cvt_i32_f32_e32 v38, v39
	v_fma_f32 v32, -v32, v36, v35
	v_div_fmas_f32 v32, v32, v33, v36
	v_div_fixup_f32 v22, v32, v24, v22
	v_ldexp_f32 v25, v37, v38
	v_cndmask_b32_e64 v25, 0, v25, s[4:5]
	v_cmp_ngt_f32_e64 s[4:5], s78, v28
	v_mul_f32_e32 v21, v21, v27
	s_nop 0
	v_cndmask_b32_e64 v25, v97, v25, s[4:5]
	v_add_f32_e32 v25, 1.0, v25
	v_div_scale_f32 v28, s[4:5], v25, v25, v23
	v_rcp_f32_e32 v35, v28
	v_cmp_nlt_f32_e64 s[4:5], s77, v34
	v_fma_f32 v24, -v28, v35, 1.0
	v_fmac_f32_e32 v35, v24, v35
	v_div_scale_f32 v24, vcc, v23, v25, v23
	v_mul_f32_e32 v32, v24, v35
	v_fma_f32 v33, -v28, v32, v24
	v_fmac_f32_e32 v32, v33, v35
	v_mul_f32_e32 v33, 0xbfb8aa3b, v34
	v_fma_f32 v36, v34, s76, -v33
	v_rndne_f32_e32 v37, v33
	v_fmac_f32_e32 v36, 0xb2a5705f, v34
	v_sub_f32_e32 v33, v33, v37
	v_add_f32_e32 v33, v33, v36
	v_exp_f32_e32 v33, v33
	v_cvt_i32_f32_e32 v36, v37
	v_fma_f32 v24, -v28, v32, v24
	v_div_fmas_f32 v24, v24, v35, v32
	v_div_fixup_f32 v23, v24, v25, v23
	v_ldexp_f32 v26, v33, v36
	v_cndmask_b32_e64 v26, 0, v26, s[4:5]
	v_cmp_ngt_f32_e64 s[4:5], s78, v34
	v_cvt_pk_bf16_f32 v22, v22, v23
	s_nop 1
	v_cndmask_b32_e64 v26, v97, v26, s[4:5]
	v_add_f32_e32 v26, 1.0, v26
	v_div_scale_f32 v28, s[4:5], v26, v26, v20
	v_rcp_f32_e32 v33, v28
	v_cmp_nlt_f32_e64 s[4:5], s77, v29
	v_fma_f32 v24, -v28, v33, 1.0
	v_fmac_f32_e32 v33, v24, v33
	v_div_scale_f32 v24, vcc, v20, v26, v20
	v_mul_f32_e32 v25, v24, v33
	v_fma_f32 v32, -v28, v25, v24
	v_fmac_f32_e32 v25, v32, v33
	v_mul_f32_e32 v32, 0xbfb8aa3b, v29
	v_fma_f32 v34, v29, s76, -v32
	v_rndne_f32_e32 v35, v32
	v_fmac_f32_e32 v34, 0xb2a5705f, v29
	v_sub_f32_e32 v32, v32, v35
	v_add_f32_e32 v32, v32, v34
	v_exp_f32_e32 v32, v32
	v_cvt_i32_f32_e32 v34, v35
	v_fma_f32 v24, -v28, v25, v24
	v_div_fmas_f32 v24, v24, v33, v25
	v_div_fixup_f32 v20, v24, v26, v20
	v_ldexp_f32 v27, v32, v34
	v_cndmask_b32_e64 v27, 0, v27, s[4:5]
	v_cmp_ngt_f32_e64 s[4:5], s78, v29
	s_nop 1
	v_cndmask_b32_e64 v27, v97, v27, s[4:5]
	v_add_f32_e32 v27, 1.0, v27
	v_div_scale_f32 v28, s[4:5], v27, v27, v21
	v_rcp_f32_e32 v29, v28
	s_nop 0
	v_fma_f32 v24, -v28, v29, 1.0
	v_fmac_f32_e32 v29, v24, v29
	v_div_scale_f32 v24, vcc, v21, v27, v21
	v_mul_f32_e32 v25, v24, v29
	v_fma_f32 v26, -v28, v25, v24
	v_fmac_f32_e32 v25, v26, v29
	v_fma_f32 v24, -v28, v25, v24
	v_div_fmas_f32 v24, v24, v29, v25
	v_div_fixup_f32 v21, v24, v27, v21
	v_cvt_pk_bf16_f32 v21, v20, v21
	v_cndmask_b32_e64 v20, v30, v22, s[2:3]
	v_cndmask_b32_e64 v23, v31, v21, s[2:3]
	ds_bpermute_b32 v20, v98, v20
	ds_bpermute_b32 v24, v98, v23
	s_waitcnt lgkmcnt(1)
	v_cndmask_b32_e64 v22, v22, v20, s[2:3]
	v_cndmask_b32_e64 v20, v20, v30, s[2:3]
	s_waitcnt lgkmcnt(0)
	v_cndmask_b32_e64 v23, v21, v24, s[2:3]
	v_cndmask_b32_e64 v21, v24, v31, s[2:3]
	global_store_dwordx4 v[18:19], v[20:23], off offset:320
	s_nop 1
	v_or_b32_e32 v20, 0x180, v66
	v_mov_b32_e32 v21, v67
	v_lshl_add_u64 v[20:21], v[72:73], 0, v[20:21]
	global_load_dwordx2 v[24:25], v[20:21], off
	s_nop 0
	global_load_dwordx4 v[20:23], v75, s[28:29] offset:768
	s_waitcnt vmcnt(1)
	v_lshlrev_b32_e32 v26, 16, v24
	v_mul_f32_e32 v27, 0xbfb8aa3b, v26
	v_fma_f32 v28, v26, s76, -v27
	v_rndne_f32_e32 v29, v27
	v_fmac_f32_e32 v28, 0xb2a5705f, v26
	v_sub_f32_e32 v27, v27, v29
	v_add_f32_e32 v27, v27, v28
	v_exp_f32_e32 v27, v27
	v_cvt_i32_f32_e32 v28, v29
	s_waitcnt vmcnt(0)
; __device__ __forceinline__ unsigned cvt_pk_bf16(float lo, float hi) { unsigned r; asm volatile("v_cvt_pk_bf16_f32 %0, %1, %2" : "=v"(r) : "v"(lo), "v"(hi)); return r; }
; __device__ __forceinline__ void mlstm_D(LAS unsigned char* lds, int c, int h, const bf16_t* Z, const float* gi, const float* bcum, const float* marr, const bf16_t* CST, const float* NST,
;                                         const float* hgain, bf16_t* YCAT) {
;     ...
; #pragma unroll
;     for (int j = 0; j < 16; j += 2) { u32x2 ab[2];
; #pragma unroll
;         for (int n = 0; n < 2; ++n) { const int col = h * DH + 16 * (j + n) + 4 * fq;
;             const f32x4 gn = *(const f32x4*)(hgain + col); const u32x2 ov = *(const u32x2*)(Z + trow * EVN + 4096 + col);
;             const float o0 = bf_lo(ov.x), o1 = bf_hi(ov.x), o2 = bf_lo(ov.y), o3 = bf_hi(ov.y);
;             const float y0 = acc[j + n][0] * rs * gn[0] / (1.0f + expf(-o0)), y1 = acc[j + n][1] * rs * gn[1] / (1.0f + expf(-o1));
;             const float y2 = acc[j + n][2] * rs * gn[2] / (1.0f + expf(-o2)), y3 = acc[j + n][3] * rs * gn[3] / (1.0f + expf(-o3));
;             ab[n].x = cvt_pk_bf16(y0, y1); ab[n].y = cvt_pk_bf16(y2, y3); }
;         const bool odd = fq & 1; const u32x2 give = odd ? ab[0] : ab[1];
;         u32x2 got; got.x = (unsigned)__shfl_xor((int)give.x, 16); got.y = (unsigned)__shfl_xor((int)give.y, 16);
;         u32x4 w; if (odd) { w.x = got.x; w.y = got.y; w.z = ab[1].x; w.w = ab[1].y; } else { w.x = ab[0].x; w.y = ab[0].y; w.z = got.x; w.w = got.y; }
;         *(u32x4*)(YCAT + trow * D + 1024 + h * DH + 16 * (j + (odd ? 1 : 0)) + 4 * (fq & 2)) = w; if ((j & 3) == 2) asm volatile("" ::: "memory"); }
	v_mul_f32_e32 v14, v14, v20
	v_cmp_nlt_f32_e32 vcc, s77, v26
	v_and_b32_e32 v24, 0xffff0000, v24
	v_ldexp_f32 v20, v27, v28
	v_cndmask_b32_e32 v20, 0, v20, vcc
	v_cmp_ngt_f32_e32 vcc, s78, v26
	v_mul_f32_e32 v15, v15, v21
	v_lshlrev_b32_e32 v28, 16, v25
	v_cndmask_b32_e32 v20, v97, v20, vcc
	v_add_f32_e32 v20, 1.0, v20
	v_div_scale_f32 v26, s[4:5], v20, v20, v14
	v_rcp_f32_e32 v27, v26
	v_cmp_nlt_f32_e64 s[4:5], s77, v24
	v_mul_f32_e32 v16, v16, v22
	v_and_b32_e32 v25, 0xffff0000, v25
	v_fma_f32 v29, -v26, v27, 1.0
	v_fmac_f32_e32 v27, v29, v27
	v_div_scale_f32 v29, vcc, v14, v20, v14
	v_mul_f32_e32 v30, v29, v27
	v_fma_f32 v31, -v26, v30, v29
	v_fmac_f32_e32 v30, v31, v27
	v_mul_f32_e32 v31, 0xbfb8aa3b, v24
	v_fma_f32 v32, v24, s76, -v31
	v_rndne_f32_e32 v33, v31
	v_fmac_f32_e32 v32, 0xb2a5705f, v24
	v_sub_f32_e32 v31, v31, v33
	v_add_f32_e32 v31, v31, v32
	v_exp_f32_e32 v31, v31
	v_cvt_i32_f32_e32 v32, v33
	v_fma_f32 v26, -v26, v30, v29
	v_div_fmas_f32 v26, v26, v27, v30
	v_div_fixup_f32 v14, v26, v20, v14
	v_ldexp_f32 v21, v31, v32
	v_cndmask_b32_e64 v21, 0, v21, s[4:5]
	v_cmp_ngt_f32_e64 s[4:5], s78, v24
	v_mul_f32_e32 v17, v17, v23
	s_nop 0
	v_cndmask_b32_e64 v21, v97, v21, s[4:5]
	v_add_f32_e32 v21, 1.0, v21
	v_div_scale_f32 v24, s[4:5], v21, v21, v15
	v_rcp_f32_e32 v29, v24
	v_cmp_nlt_f32_e64 s[4:5], s77, v28
	v_fma_f32 v20, -v24, v29, 1.0
	v_fmac_f32_e32 v29, v20, v29
	v_div_scale_f32 v20, vcc, v15, v21, v15
	v_mul_f32_e32 v26, v20, v29
	v_fma_f32 v27, -v24, v26, v20
	v_fmac_f32_e32 v26, v27, v29
	v_mul_f32_e32 v27, 0xbfb8aa3b, v28
	v_fma_f32 v30, v28, s76, -v27
	v_rndne_f32_e32 v31, v27
	v_fmac_f32_e32 v30, 0xb2a5705f, v28
	v_sub_f32_e32 v27, v27, v31
	v_add_f32_e32 v27, v27, v30
	v_exp_f32_e32 v27, v27
	v_cvt_i32_f32_e32 v30, v31
	v_fma_f32 v20, -v24, v26, v20
	v_div_fmas_f32 v20, v20, v29, v26
	v_div_fixup_f32 v15, v20, v21, v15
	v_ldexp_f32 v22, v27, v30
	v_cndmask_b32_e64 v22, 0, v22, s[4:5]
	v_cmp_ngt_f32_e64 s[4:5], s78, v28
	s_nop 1
	v_cndmask_b32_e64 v22, v97, v22, s[4:5]
	v_add_f32_e32 v22, 1.0, v22
	v_div_scale_f32 v24, s[4:5], v22, v22, v16
	v_rcp_f32_e32 v27, v24
	v_cmp_nlt_f32_e64 s[4:5], s77, v25
	v_fma_f32 v20, -v24, v27, 1.0
	v_fmac_f32_e32 v27, v20, v27
	v_div_scale_f32 v20, vcc, v16, v22, v16
	v_mul_f32_e32 v21, v20, v27
	v_fma_f32 v26, -v24, v21, v20
	v_fmac_f32_e32 v21, v26, v27
	v_mul_f32_e32 v26, 0xbfb8aa3b, v25
	v_fma_f32 v28, v25, s76, -v26
	v_rndne_f32_e32 v29, v26
	v_fmac_f32_e32 v28, 0xb2a5705f, v25
	v_sub_f32_e32 v26, v26, v29
	v_add_f32_e32 v26, v26, v28
	v_exp_f32_e32 v26, v26
	v_cvt_i32_f32_e32 v28, v29
	v_fma_f32 v20, -v24, v21, v20
	v_div_fmas_f32 v20, v20, v27, v21
	v_div_fixup_f32 v16, v20, v22, v16
	v_ldexp_f32 v23, v26, v28
	v_cndmask_b32_e64 v23, 0, v23, s[4:5]
	v_cmp_ngt_f32_e64 s[4:5], s78, v25
	s_nop 1
	v_cndmask_b32_e64 v23, v97, v23, s[4:5]
	v_add_f32_e32 v23, 1.0, v23
	v_div_scale_f32 v24, s[4:5], v23, v23, v17
	v_rcp_f32_e32 v25, v24
	s_nop 0
	v_fma_f32 v20, -v24, v25, 1.0
	v_fmac_f32_e32 v25, v20, v25
	v_div_scale_f32 v20, vcc, v17, v23, v17
	v_mul_f32_e32 v21, v20, v25
	v_fma_f32 v22, -v24, v21, v20
	v_fmac_f32_e32 v21, v22, v25
	v_fma_f32 v20, -v24, v21, v20
	v_div_fmas_f32 v20, v20, v25, v21
	v_cvt_pk_bf16_f32 v22, v14, v15
	v_or_b32_e32 v14, 0x1a0, v66
	v_mov_b32_e32 v15, v67
	v_div_fixup_f32 v17, v20, v23, v17
	v_lshl_add_u64 v[14:15], v[72:73], 0, v[14:15]
	v_cvt_pk_bf16_f32 v23, v16, v17
	global_load_dwordx2 v[20:21], v[14:15], off
	s_nop 0
	global_load_dwordx4 v[14:17], v75, s[28:29] offset:832
	s_waitcnt vmcnt(1)
	v_lshlrev_b32_e32 v24, 16, v20
	v_mul_f32_e32 v25, 0xbfb8aa3b, v24
	v_fma_f32 v26, v24, s76, -v25
	v_rndne_f32_e32 v27, v25
	v_fmac_f32_e32 v26, 0xb2a5705f, v24
	v_sub_f32_e32 v25, v25, v27
	v_add_f32_e32 v25, v25, v26
	v_exp_f32_e32 v25, v25
	v_cvt_i32_f32_e32 v26, v27
	s_waitcnt vmcnt(0)
	v_mul_f32_e32 v10, v10, v14
	v_cmp_nlt_f32_e32 vcc, s77, v24
	v_and_b32_e32 v20, 0xffff0000, v20
	v_ldexp_f32 v14, v25, v26
	v_cndmask_b32_e32 v14, 0, v14, vcc
	v_cmp_ngt_f32_e32 vcc, s78, v24
	v_mul_f32_e32 v11, v11, v15
	v_lshlrev_b32_e32 v26, 16, v21
	v_cndmask_b32_e32 v14, v97, v14, vcc
	v_add_f32_e32 v14, 1.0, v14
	v_div_scale_f32 v24, s[4:5], v14, v14, v10
	v_rcp_f32_e32 v25, v24
	v_cmp_nlt_f32_e64 s[4:5], s77, v20
	v_mul_f32_e32 v12, v12, v16
	v_and_b32_e32 v21, 0xffff0000, v21
	v_fma_f32 v27, -v24, v25, 1.0
	v_fmac_f32_e32 v25, v27, v25
	v_div_scale_f32 v27, vcc, v10, v14, v10
	v_mul_f32_e32 v28, v27, v25
	v_fma_f32 v29, -v24, v28, v27
	v_fmac_f32_e32 v28, v29, v25
	v_mul_f32_e32 v29, 0xbfb8aa3b, v20
	v_fma_f32 v30, v20, s76, -v29
	v_rndne_f32_e32 v31, v29
	v_fmac_f32_e32 v30, 0xb2a5705f, v20
	v_sub_f32_e32 v29, v29, v31
	v_add_f32_e32 v29, v29, v30
	v_exp_f32_e32 v29, v29
	v_cvt_i32_f32_e32 v30, v31
	v_fma_f32 v24, -v24, v28, v27
	v_div_fmas_f32 v24, v24, v25, v28
	v_div_fixup_f32 v10, v24, v14, v10
	v_ldexp_f32 v15, v29, v30
	v_cndmask_b32_e64 v15, 0, v15, s[4:5]
	v_cmp_ngt_f32_e64 s[4:5], s78, v20
	v_mul_f32_e32 v13, v13, v17
	s_nop 0
	v_cndmask_b32_e64 v15, v97, v15, s[4:5]
	v_add_f32_e32 v15, 1.0, v15
	v_div_scale_f32 v20, s[4:5], v15, v15, v11
	v_rcp_f32_e32 v27, v20
	v_cmp_nlt_f32_e64 s[4:5], s77, v26
	v_fma_f32 v14, -v20, v27, 1.0
	v_fmac_f32_e32 v27, v14, v27
	v_div_scale_f32 v14, vcc, v11, v15, v11
	v_mul_f32_e32 v24, v14, v27
	v_fma_f32 v25, -v20, v24, v14
	v_fmac_f32_e32 v24, v25, v27
	v_mul_f32_e32 v25, 0xbfb8aa3b, v26
	v_fma_f32 v28, v26, s76, -v25
	v_rndne_f32_e32 v29, v25
	v_fmac_f32_e32 v28, 0xb2a5705f, v26
	v_sub_f32_e32 v25, v25, v29
	v_add_f32_e32 v25, v25, v28
	v_exp_f32_e32 v25, v25
	v_cvt_i32_f32_e32 v28, v29
	v_fma_f32 v14, -v20, v24, v14
; __device__ __forceinline__ unsigned cvt_pk_bf16(float lo, float hi) { unsigned r; asm volatile("v_cvt_pk_bf16_f32 %0, %1, %2" : "=v"(r) : "v"(lo), "v"(hi)); return r; }
; __device__ __forceinline__ void mlstm_D(LAS unsigned char* lds, int c, int h, const bf16_t* Z, const float* gi, const float* bcum, const float* marr, const bf16_t* CST, const float* NST,
;                                         const float* hgain, bf16_t* YCAT) {
;     ...
; #pragma unroll
;     for (int j = 0; j < 16; j += 2) { u32x2 ab[2];
; #pragma unroll
;         for (int n = 0; n < 2; ++n) { const int col = h * DH + 16 * (j + n) + 4 * fq;
;             const f32x4 gn = *(const f32x4*)(hgain + col); const u32x2 ov = *(const u32x2*)(Z + trow * EVN + 4096 + col);
;             const float o0 = bf_lo(ov.x), o1 = bf_hi(ov.x), o2 = bf_lo(ov.y), o3 = bf_hi(ov.y);
;             const float y0 = acc[j + n][0] * rs * gn[0] / (1.0f + expf(-o0)), y1 = acc[j + n][1] * rs * gn[1] / (1.0f + expf(-o1));
;             const float y2 = acc[j + n][2] * rs * gn[2] / (1.0f + expf(-o2)), y3 = acc[j + n][3] * rs * gn[3] / (1.0f + expf(-o3));
;             ab[n].x = cvt_pk_bf16(y0, y1); ab[n].y = cvt_pk_bf16(y2, y3); }
;         const bool odd = fq & 1; const u32x2 give = odd ? ab[0] : ab[1];
;         u32x2 got; got.x = (unsigned)__shfl_xor((int)give.x, 16); got.y = (unsigned)__shfl_xor((int)give.y, 16);
;         u32x4 w; if (odd) { w.x = got.x; w.y = got.y; w.z = ab[1].x; w.w = ab[1].y; } else { w.x = ab[0].x; w.y = ab[0].y; w.z = got.x; w.w = got.y; }
;         *(u32x4*)(YCAT + trow * D + 1024 + h * DH + 16 * (j + (odd ? 1 : 0)) + 4 * (fq & 2)) = w; if ((j & 3) == 2) asm volatile("" ::: "memory"); }
	v_div_fmas_f32 v14, v14, v27, v24
	v_div_fixup_f32 v11, v14, v15, v11
	v_ldexp_f32 v16, v25, v28
	v_cndmask_b32_e64 v16, 0, v16, s[4:5]
	v_cmp_ngt_f32_e64 s[4:5], s78, v26
	v_cvt_pk_bf16_f32 v10, v10, v11
	s_nop 1
	v_cndmask_b32_e64 v16, v97, v16, s[4:5]
	v_add_f32_e32 v16, 1.0, v16
	v_div_scale_f32 v20, s[4:5], v16, v16, v12
	v_rcp_f32_e32 v25, v20
	v_cmp_nlt_f32_e64 s[4:5], s77, v21
	v_fma_f32 v14, -v20, v25, 1.0
	v_fmac_f32_e32 v25, v14, v25
	v_div_scale_f32 v14, vcc, v12, v16, v12
	v_mul_f32_e32 v15, v14, v25
	v_fma_f32 v24, -v20, v15, v14
	v_fmac_f32_e32 v15, v24, v25
	v_mul_f32_e32 v24, 0xbfb8aa3b, v21
	v_fma_f32 v26, v21, s76, -v24
	v_rndne_f32_e32 v27, v24
	v_fmac_f32_e32 v26, 0xb2a5705f, v21
	v_sub_f32_e32 v24, v24, v27
	v_add_f32_e32 v24, v24, v26
	v_exp_f32_e32 v24, v24
	v_cvt_i32_f32_e32 v26, v27
	v_fma_f32 v14, -v20, v15, v14
	v_div_fmas_f32 v14, v14, v25, v15
	v_div_fixup_f32 v12, v14, v16, v12
	v_ldexp_f32 v17, v24, v26
	v_cndmask_b32_e64 v17, 0, v17, s[4:5]
	v_cmp_ngt_f32_e64 s[4:5], s78, v21
	s_nop 1
	v_cndmask_b32_e64 v17, v97, v17, s[4:5]
	v_add_f32_e32 v17, 1.0, v17
	v_div_scale_f32 v20, s[4:5], v17, v17, v13
	v_rcp_f32_e32 v21, v20
	s_nop 0
	v_fma_f32 v14, -v20, v21, 1.0
	v_fmac_f32_e32 v21, v14, v21
	v_div_scale_f32 v14, vcc, v13, v17, v13
	v_mul_f32_e32 v15, v14, v21
	v_fma_f32 v16, -v20, v15, v14
	v_fmac_f32_e32 v15, v16, v21
	v_fma_f32 v14, -v20, v15, v14
	v_div_fmas_f32 v14, v14, v21, v15
	v_div_fixup_f32 v13, v14, v17, v13
	v_cvt_pk_bf16_f32 v11, v12, v13
	v_cndmask_b32_e64 v12, v22, v10, s[2:3]
	ds_bpermute_b32 v13, v98, v12
	v_cndmask_b32_e64 v12, v23, v11, s[2:3]
	ds_bpermute_b32 v14, v98, v12
	s_waitcnt lgkmcnt(1)
	v_cndmask_b32_e64 v12, v10, v13, s[2:3]
	v_cndmask_b32_e64 v10, v13, v22, s[2:3]
	s_waitcnt lgkmcnt(0)
	v_cndmask_b32_e64 v13, v11, v14, s[2:3]
	v_cndmask_b32_e64 v11, v14, v23, s[2:3]
	global_store_dwordx4 v[18:19], v[10:13], off offset:384
	s_nop 1
	v_or_b32_e32 v10, 0x1c0, v66
	v_mov_b32_e32 v11, v67
	v_lshl_add_u64 v[10:11], v[72:73], 0, v[10:11]
	global_load_dwordx2 v[14:15], v[10:11], off
	s_nop 0
	global_load_dwordx4 v[10:13], v75, s[28:29] offset:896
	v_or_b32_e32 v66, 0x1e0, v66
	s_waitcnt vmcnt(1)
	v_lshlrev_b32_e32 v16, 16, v14
	v_mul_f32_e32 v17, 0xbfb8aa3b, v16
	v_fma_f32 v20, v16, s76, -v17
	v_rndne_f32_e32 v21, v17
	v_fmac_f32_e32 v20, 0xb2a5705f, v16
	v_sub_f32_e32 v17, v17, v21
	v_add_f32_e32 v17, v17, v20
	v_exp_f32_e32 v17, v17
	v_cvt_i32_f32_e32 v20, v21
	s_waitcnt vmcnt(0)
	v_mul_f32_e32 v6, v6, v10
	v_cmp_nlt_f32_e32 vcc, s77, v16
	v_and_b32_e32 v14, 0xffff0000, v14
	v_ldexp_f32 v10, v17, v20
	v_cndmask_b32_e32 v10, 0, v10, vcc
	v_cmp_ngt_f32_e32 vcc, s78, v16
	v_mul_f32_e32 v7, v7, v11
	v_lshlrev_b32_e32 v20, 16, v15
	v_cndmask_b32_e32 v10, v97, v10, vcc
	v_add_f32_e32 v10, 1.0, v10
	v_div_scale_f32 v16, s[4:5], v10, v10, v6
	v_rcp_f32_e32 v17, v16
	v_cmp_nlt_f32_e64 s[4:5], s77, v14
	v_mul_f32_e32 v8, v8, v12
	v_and_b32_e32 v15, 0xffff0000, v15
	v_fma_f32 v21, -v16, v17, 1.0
	v_fmac_f32_e32 v17, v21, v17
	v_div_scale_f32 v21, vcc, v6, v10, v6
	v_mul_f32_e32 v22, v21, v17
	v_fma_f32 v23, -v16, v22, v21
	v_fmac_f32_e32 v22, v23, v17
	v_mul_f32_e32 v23, 0xbfb8aa3b, v14
	v_fma_f32 v24, v14, s76, -v23
	v_rndne_f32_e32 v25, v23
	v_fmac_f32_e32 v24, 0xb2a5705f, v14
	v_sub_f32_e32 v23, v23, v25
	v_add_f32_e32 v23, v23, v24
	v_exp_f32_e32 v23, v23
	v_cvt_i32_f32_e32 v24, v25
	v_fma_f32 v16, -v16, v22, v21
	v_div_fmas_f32 v16, v16, v17, v22
	v_div_fixup_f32 v6, v16, v10, v6
	v_ldexp_f32 v11, v23, v24
	v_cndmask_b32_e64 v11, 0, v11, s[4:5]
	v_cmp_ngt_f32_e64 s[4:5], s78, v14
	v_mul_f32_e32 v9, v9, v13
	s_nop 0
	v_cndmask_b32_e64 v11, v97, v11, s[4:5]
	v_add_f32_e32 v11, 1.0, v11
	v_div_scale_f32 v14, s[4:5], v11, v11, v7
	v_rcp_f32_e32 v21, v14
	v_cmp_nlt_f32_e64 s[4:5], s77, v20
	v_fma_f32 v10, -v14, v21, 1.0
	v_fmac_f32_e32 v21, v10, v21
	v_div_scale_f32 v10, vcc, v7, v11, v7
	v_mul_f32_e32 v16, v10, v21
	v_fma_f32 v17, -v14, v16, v10
	v_fmac_f32_e32 v16, v17, v21
	v_mul_f32_e32 v17, 0xbfb8aa3b, v20
	v_fma_f32 v22, v20, s76, -v17
	v_rndne_f32_e32 v23, v17
	v_fmac_f32_e32 v22, 0xb2a5705f, v20
	v_sub_f32_e32 v17, v17, v23
	v_add_f32_e32 v17, v17, v22
	v_exp_f32_e32 v17, v17
	v_cvt_i32_f32_e32 v22, v23
	v_fma_f32 v10, -v14, v16, v10
	v_div_fmas_f32 v10, v10, v21, v16
	v_div_fixup_f32 v7, v10, v11, v7
	v_ldexp_f32 v12, v17, v22
	v_cndmask_b32_e64 v12, 0, v12, s[4:5]
	v_cmp_ngt_f32_e64 s[4:5], s78, v20
	s_nop 1
	v_cndmask_b32_e64 v12, v97, v12, s[4:5]
	v_add_f32_e32 v12, 1.0, v12
	v_div_scale_f32 v14, s[4:5], v12, v12, v8
	v_rcp_f32_e32 v17, v14
	v_cmp_nlt_f32_e64 s[4:5], s77, v15
	v_fma_f32 v10, -v14, v17, 1.0
	v_fmac_f32_e32 v17, v10, v17
	v_div_scale_f32 v10, vcc, v8, v12, v8
	v_mul_f32_e32 v11, v10, v17
	v_fma_f32 v16, -v14, v11, v10
	v_fmac_f32_e32 v11, v16, v17
	v_mul_f32_e32 v16, 0xbfb8aa3b, v15
	v_fma_f32 v20, v15, s76, -v16
	v_rndne_f32_e32 v21, v16
	v_fmac_f32_e32 v20, 0xb2a5705f, v15
	v_sub_f32_e32 v16, v16, v21
	v_add_f32_e32 v16, v16, v20
	v_exp_f32_e32 v16, v16
	v_cvt_i32_f32_e32 v20, v21
	v_fma_f32 v10, -v14, v11, v10
	v_div_fmas_f32 v10, v10, v17, v11
	v_div_fixup_f32 v8, v10, v12, v8
	v_ldexp_f32 v13, v16, v20
	v_cndmask_b32_e64 v13, 0, v13, s[4:5]
	v_cmp_ngt_f32_e64 s[4:5], s78, v15
	s_nop 1
	v_cndmask_b32_e64 v13, v97, v13, s[4:5]
	v_add_f32_e32 v13, 1.0, v13
	v_div_scale_f32 v14, s[4:5], v13, v13, v9
	v_rcp_f32_e32 v15, v14
	s_nop 0
	v_fma_f32 v10, -v14, v15, 1.0
	v_fmac_f32_e32 v15, v10, v15
	v_div_scale_f32 v10, vcc, v9, v13, v9
	v_mul_f32_e32 v11, v10, v15
	v_fma_f32 v12, -v14, v11, v10
	v_fmac_f32_e32 v11, v12, v15
	v_fma_f32 v10, -v14, v11, v10
	v_div_fmas_f32 v10, v10, v15, v11
	v_div_fixup_f32 v9, v10, v13, v9
	v_cvt_pk_bf16_f32 v12, v6, v7
	v_lshl_add_u64 v[6:7], v[72:73], 0, v[66:67]
	v_cvt_pk_bf16_f32 v13, v8, v9
	global_load_dwordx2 v[10:11], v[6:7], off
	s_nop 0
	global_load_dwordx4 v[6:9], v75, s[28:29] offset:960
	s_waitcnt vmcnt(1)
; __device__ __forceinline__ unsigned cvt_pk_bf16(float lo, float hi) { unsigned r; asm volatile("v_cvt_pk_bf16_f32 %0, %1, %2" : "=v"(r) : "v"(lo), "v"(hi)); return r; }
; __device__ __forceinline__ void mlstm_D(LAS unsigned char* lds, int c, int h, const bf16_t* Z, const float* gi, const float* bcum, const float* marr, const bf16_t* CST, const float* NST,
;                                         const float* hgain, bf16_t* YCAT) {
;     ...
; #pragma unroll
;     for (int j = 0; j < 16; j += 2) { u32x2 ab[2];
; #pragma unroll
;         for (int n = 0; n < 2; ++n) { const int col = h * DH + 16 * (j + n) + 4 * fq;
;             const f32x4 gn = *(const f32x4*)(hgain + col); const u32x2 ov = *(const u32x2*)(Z + trow * EVN + 4096 + col);
;             const float o0 = bf_lo(ov.x), o1 = bf_hi(ov.x), o2 = bf_lo(ov.y), o3 = bf_hi(ov.y);
;             const float y0 = acc[j + n][0] * rs * gn[0] / (1.0f + expf(-o0)), y1 = acc[j + n][1] * rs * gn[1] / (1.0f + expf(-o1));
;             const float y2 = acc[j + n][2] * rs * gn[2] / (1.0f + expf(-o2)), y3 = acc[j + n][3] * rs * gn[3] / (1.0f + expf(-o3));
;             ab[n].x = cvt_pk_bf16(y0, y1); ab[n].y = cvt_pk_bf16(y2, y3); }
;         const bool odd = fq & 1; const u32x2 give = odd ? ab[0] : ab[1];
;         u32x2 got; got.x = (unsigned)__shfl_xor((int)give.x, 16); got.y = (unsigned)__shfl_xor((int)give.y, 16);
;         u32x4 w; if (odd) { w.x = got.x; w.y = got.y; w.z = ab[1].x; w.w = ab[1].y; } else { w.x = ab[0].x; w.y = ab[0].y; w.z = got.x; w.w = got.y; }
;         *(u32x4*)(YCAT + trow * D + 1024 + h * DH + 16 * (j + (odd ? 1 : 0)) + 4 * (fq & 2)) = w; if ((j & 3) == 2) asm volatile("" ::: "memory"); }
; __global__ void __launch_bounds__(NTHR, 2) mk_fwd(Args args) {
;     ...
;             for (int rep = 0; rep < NREP(3); ++rep) {
;             for (int u = bx; u < NCH * NH; u += G) mlstm_D(lds, u >> 2, u & 3, Z, GI, BCUM, MARR, CST, NST, ev_head_norm, YCAT);
;             }
	v_lshlrev_b32_e32 v14, 16, v10
	v_mul_f32_e32 v15, 0xbfb8aa3b, v14
	v_fma_f32 v16, v14, s76, -v15
	v_rndne_f32_e32 v17, v15
	v_fmac_f32_e32 v16, 0xb2a5705f, v14
	v_sub_f32_e32 v15, v15, v17
	v_add_f32_e32 v15, v15, v16
	v_exp_f32_e32 v15, v15
	v_cvt_i32_f32_e32 v16, v17
	s_waitcnt vmcnt(0)
	v_mul_f32_e32 v2, v2, v6
	v_cmp_nlt_f32_e32 vcc, s77, v14
	v_and_b32_e32 v10, 0xffff0000, v10
	v_ldexp_f32 v6, v15, v16
	v_cndmask_b32_e32 v6, 0, v6, vcc
	v_cmp_ngt_f32_e32 vcc, s78, v14
	v_mul_f32_e32 v3, v3, v7
	v_lshlrev_b32_e32 v16, 16, v11
	v_cndmask_b32_e32 v6, v97, v6, vcc
	v_add_f32_e32 v6, 1.0, v6
	v_div_scale_f32 v14, s[4:5], v6, v6, v2
	v_rcp_f32_e32 v15, v14
	v_cmp_nlt_f32_e64 s[4:5], s77, v10
	v_mul_f32_e32 v4, v4, v8
	v_and_b32_e32 v11, 0xffff0000, v11
	v_fma_f32 v17, -v14, v15, 1.0
	v_fmac_f32_e32 v15, v17, v15
	v_div_scale_f32 v17, vcc, v2, v6, v2
	v_mul_f32_e32 v20, v17, v15
	v_fma_f32 v21, -v14, v20, v17
	v_fmac_f32_e32 v20, v21, v15
	v_mul_f32_e32 v21, 0xbfb8aa3b, v10
	v_fma_f32 v22, v10, s76, -v21
	v_rndne_f32_e32 v23, v21
	v_fmac_f32_e32 v22, 0xb2a5705f, v10
	v_sub_f32_e32 v21, v21, v23
	v_add_f32_e32 v21, v21, v22
	v_exp_f32_e32 v21, v21
	v_cvt_i32_f32_e32 v22, v23
	v_fma_f32 v14, -v14, v20, v17
	v_div_fmas_f32 v14, v14, v15, v20
	v_div_fixup_f32 v2, v14, v6, v2
	v_ldexp_f32 v7, v21, v22
	v_cndmask_b32_e64 v7, 0, v7, s[4:5]
	v_cmp_ngt_f32_e64 s[4:5], s78, v10
	v_mul_f32_e32 v5, v5, v9
	s_nop 0
	v_cndmask_b32_e64 v7, v97, v7, s[4:5]
	v_add_f32_e32 v7, 1.0, v7
	v_div_scale_f32 v10, s[4:5], v7, v7, v3
	v_rcp_f32_e32 v17, v10
	v_cmp_nlt_f32_e64 s[4:5], s77, v16
	v_fma_f32 v6, -v10, v17, 1.0
	v_fmac_f32_e32 v17, v6, v17
	v_div_scale_f32 v6, vcc, v3, v7, v3
	v_mul_f32_e32 v14, v6, v17
	v_fma_f32 v15, -v10, v14, v6
	v_fmac_f32_e32 v14, v15, v17
	v_mul_f32_e32 v15, 0xbfb8aa3b, v16
	v_fma_f32 v20, v16, s76, -v15
	v_rndne_f32_e32 v21, v15
	v_fmac_f32_e32 v20, 0xb2a5705f, v16
	v_sub_f32_e32 v15, v15, v21
	v_add_f32_e32 v15, v15, v20
	v_exp_f32_e32 v15, v15
	v_cvt_i32_f32_e32 v20, v21
	v_fma_f32 v6, -v10, v14, v6
	v_div_fmas_f32 v6, v6, v17, v14
	v_div_fixup_f32 v3, v6, v7, v3
	v_ldexp_f32 v8, v15, v20
	v_cndmask_b32_e64 v8, 0, v8, s[4:5]
	v_cmp_ngt_f32_e64 s[4:5], s78, v16
	v_cvt_pk_bf16_f32 v2, v2, v3
	s_nop 1
	v_cndmask_b32_e64 v8, v97, v8, s[4:5]
	v_add_f32_e32 v8, 1.0, v8
	v_div_scale_f32 v10, s[4:5], v8, v8, v4
	v_rcp_f32_e32 v15, v10
	v_cmp_nlt_f32_e64 s[4:5], s77, v11
	v_fma_f32 v6, -v10, v15, 1.0
	v_fmac_f32_e32 v15, v6, v15
	v_div_scale_f32 v6, vcc, v4, v8, v4
	v_mul_f32_e32 v7, v6, v15
	v_fma_f32 v14, -v10, v7, v6
	v_fmac_f32_e32 v7, v14, v15
	v_mul_f32_e32 v14, 0xbfb8aa3b, v11
	v_fma_f32 v16, v11, s76, -v14
	v_rndne_f32_e32 v17, v14
	v_fmac_f32_e32 v16, 0xb2a5705f, v11
	v_sub_f32_e32 v14, v14, v17
	v_add_f32_e32 v14, v14, v16
	v_exp_f32_e32 v14, v14
	v_cvt_i32_f32_e32 v16, v17
	v_fma_f32 v6, -v10, v7, v6
	v_div_fmas_f32 v6, v6, v15, v7
	v_div_fixup_f32 v4, v6, v8, v4
	v_ldexp_f32 v9, v14, v16
	v_cndmask_b32_e64 v9, 0, v9, s[4:5]
	v_cmp_ngt_f32_e64 s[4:5], s78, v11
	s_nop 1
	v_cndmask_b32_e64 v9, v97, v9, s[4:5]
	v_add_f32_e32 v9, 1.0, v9
	v_div_scale_f32 v10, s[4:5], v9, v9, v5
	v_rcp_f32_e32 v11, v10
	s_nop 0
	v_fma_f32 v6, -v10, v11, 1.0
	v_fmac_f32_e32 v11, v6, v11
	v_div_scale_f32 v6, vcc, v5, v9, v5
	v_mul_f32_e32 v7, v6, v11
	v_fma_f32 v8, -v10, v7, v6
	v_fmac_f32_e32 v7, v8, v11
	v_fma_f32 v6, -v10, v7, v6
	v_div_fmas_f32 v6, v6, v11, v7
	v_div_fixup_f32 v5, v6, v9, v5
	v_cvt_pk_bf16_f32 v3, v4, v5
	v_cndmask_b32_e64 v4, v12, v2, s[2:3]
	ds_bpermute_b32 v5, v98, v4
	v_cndmask_b32_e64 v4, v13, v3, s[2:3]
	ds_bpermute_b32 v6, v98, v4
	s_waitcnt lgkmcnt(1)
	v_cndmask_b32_e64 v4, v2, v5, s[2:3]
	v_cndmask_b32_e64 v2, v5, v12, s[2:3]
	s_waitcnt lgkmcnt(0)
	v_cndmask_b32_e64 v5, v3, v6, s[2:3]
	v_cndmask_b32_e64 v3, v6, v13, s[2:3]
	global_store_dwordx4 v[18:19], v[2:5], off offset:448
	s_cbranch_scc0 .LBB0_558
